# PEER gather restructured: column-sliced across XCDs in three passes (u-side partial dots, v-side with per-slice sum of squares, final scaling) so each XCD L2 holds half of its 8 MiB table slice; all f
# speedup vs baseline: 1.0251x; 1.0201x over previous
.LBB0_1463:
	s_mov_b64 exec, -1
	s_waitcnt vmcnt(0)
	v_cmp_eq_u32_e32 vcc, 0, v0
	s_waitcnt vmcnt(0) lgkmcnt(0)
	s_barrier
	s_and_saveexec_b64 s[2:3], vcc
	s_cbranch_execz .Lgba_1444
	v_readlane_b32 s4, v237, 5
	s_waitcnt vmcnt(0) expcnt(0) lgkmcnt(0)
	s_nop 0
	v_mov_b32_e32 v1, s4
	ds_read_b32 v3, v1
	ds_read_b32 v1, v1 offset:4
	s_waitcnt lgkmcnt(1)
	v_cmp_ne_u32_e32 vcc, 0, v3
	s_branch .Lgba_1412
	v_readlane_b32 s4, v237, 2
	v_readlane_b32 s5, v237, 3
	s_load_dwordx2 s[8:9], s[6:7], 0x4
	s_lshl_b64 s[4:5], s[4:5], 2
	v_readlane_b32 s6, v237, 0
	s_add_u32 s4, s6, s4
	v_readlane_b32 s6, v237, 1
	s_addc_u32 s5, s6, s5
	s_add_u32 s6, s4, 0x1000
	s_addc_u32 s7, s5, 0
	s_waitcnt lgkmcnt(0)
	s_mul_i32 s20, s8, s38
	s_add_u32 s8, s4, 0x1100
	s_mul_i32 s20, s20, s9
	s_addc_u32 s9, s5, 0
	s_add_u32 s10, s4, 0x1200
	s_addc_u32 s11, s5, 0
	s_add_u32 s12, s4, 0x1300
	s_addc_u32 s13, s5, 0
	s_mov_b32 s21, 1
	v_mov_b32_e32 v17, 0
	s_branch .Lgba_1400

.Lgba_1444:
	s_or_b64 exec, exec, s[2:3]
	s_waitcnt lgkmcnt(0)
	s_barrier
	s_mov_b64 exec, -1
	v_and_b32_e32 v1, 63, v0
	v_readfirstlane_b32 s16, v0
	s_load_dwordx2 s[12:13], s[0:1], 0xc0
	s_lshr_b32 s16, s16, 6
	s_and_b32 s18, s33, 7
	s_lshr_b32 s19, s33, 3
	s_lshl_b32 s19, s19, 8
	s_lshl_b32 s16, s16, 5
	s_add_i32 s16, s16, s19
	s_add_i32 s17, s16, 32
	s_add_i32 s24, s17, -1
	s_lshl_b32 s19, s18, 9
	v_lshl_add_u32 v162, v1, 3, s19
	v_mov_b32_e32 v163, 0
	s_mov_b32 s31, 0
	v_and_b32_e32 v4, 8, v1
	v_cmp_eq_u32_e64 s[8:9], 0, v4
	v_and_b32_e32 v4, 4, v1
	v_cmp_eq_u32_e64 s[10:11], 0, v4
	v_and_b32_e32 v4, 2, v1
	v_cmp_eq_u32_e64 s[14:15], 0, v4
	s_mov_b32 s2, 0x55555555
	s_mov_b32 s3, 0x55555555
	s_load_dwordx2 s[4:5], s[0:1], 0x88
	s_waitcnt lgkmcnt(0)
	v_lshl_add_u64 v[160:161], v[162:163], 2, s[4:5]
	global_load_dwordx4 v[100:103], v[160:161], off
	global_load_dwordx4 v[104:107], v[160:161], off offset:16
	s_lshl_b32 s19, s18, 2
	s_add_u32 s22, s12, 0x25c00000
	s_addc_u32 s23, s13, 0
	s_add_u32 s22, s22, s19
	s_addc_u32 s23, s23, 0
	s_add_u32 s26, s12, 0xfc00000
	s_addc_u32 s27, s13, 0
	s_add_u32 s20, s12, 0x100000
	s_addc_u32 s21, s13, 0
	v_lshl_add_u64 v[172:173], v[162:163], 1, s[20:21]
	s_add_u32 s20, s12, 0x4da00000
	s_addc_u32 s21, s13, 0
	v_mov_b32_e32 v4, v1
	v_mov_b32_e32 v5, 0
	v_lshl_add_u64 v[174:175], v[4:5], 2, s[20:21]
	s_lshl_b32 s19, s18, 22
	s_add_u32 s20, s12, 0x23c00000
	s_addc_u32 s21, s13, 0
	s_add_u32 s20, s20, s19
	s_addc_u32 s21, s21, 0
	v_lshl_add_u64 v[176:177], v[4:5], 1, s[20:21]
	s_lshl_b32 s30, s16, 13
	v_lshl_add_u64 v[160:161], v[172:173], 0, s[30:31]
	global_load_dwordx4 v[116:119], v[160:161], off
	s_lshl_b32 s30, s16, 9
	v_lshl_add_u64 v[160:161], v[174:175], 0, s[30:31]
	global_load_dword v122, v[160:161], off
	global_load_dword v123, v[160:161], off offset:256
	s_waitcnt vmcnt(0)
	v_readlane_b32 s30, v122, 0
	s_lshl_b32 s30, s30, 12
	s_add_u32 s28, s26, s30
	s_addc_u32 s29, s27, 0
	global_load_dwordx2 v[24:25], v162, s[28:29]
	v_readlane_b32 s30, v122, 1
	s_lshl_b32 s30, s30, 12
	s_add_u32 s28, s26, s30
	s_addc_u32 s29, s27, 0
	global_load_dwordx2 v[26:27], v162, s[28:29]
	v_readlane_b32 s30, v122, 2
	s_lshl_b32 s30, s30, 12
	s_add_u32 s28, s26, s30
	s_addc_u32 s29, s27, 0
	global_load_dwordx2 v[28:29], v162, s[28:29]
	v_readlane_b32 s30, v122, 3
	s_lshl_b32 s30, s30, 12
	s_add_u32 s28, s26, s30
	s_addc_u32 s29, s27, 0
	global_load_dwordx2 v[30:31], v162, s[28:29]
	v_readlane_b32 s30, v122, 4
	s_lshl_b32 s30, s30, 12
	s_add_u32 s28, s26, s30
	s_addc_u32 s29, s27, 0
	global_load_dwordx2 v[32:33], v162, s[28:29]
	v_readlane_b32 s30, v122, 5
	s_lshl_b32 s30, s30, 12
	s_add_u32 s28, s26, s30
	s_addc_u32 s29, s27, 0
	global_load_dwordx2 v[34:35], v162, s[28:29]
	v_readlane_b32 s30, v122, 6
	s_lshl_b32 s30, s30, 12
	s_add_u32 s28, s26, s30
	s_addc_u32 s29, s27, 0
	global_load_dwordx2 v[36:37], v162, s[28:29]
	v_readlane_b32 s30, v122, 7
	s_lshl_b32 s30, s30, 12
	s_add_u32 s28, s26, s30
	s_addc_u32 s29, s27, 0
	global_load_dwordx2 v[38:39], v162, s[28:29]
	v_readlane_b32 s30, v122, 8
	s_lshl_b32 s30, s30, 12
	s_add_u32 s28, s26, s30
	s_addc_u32 s29, s27, 0
	global_load_dwordx2 v[40:41], v162, s[28:29]
	v_readlane_b32 s30, v122, 9
	s_lshl_b32 s30, s30, 12
	s_add_u32 s28, s26, s30
	s_addc_u32 s29, s27, 0
	global_load_dwordx2 v[42:43], v162, s[28:29]
	v_readlane_b32 s30, v122, 10
	s_lshl_b32 s30, s30, 12
	s_add_u32 s28, s26, s30
	s_addc_u32 s29, s27, 0
	global_load_dwordx2 v[44:45], v162, s[28:29]
	v_readlane_b32 s30, v122, 11
	s_lshl_b32 s30, s30, 12
	s_add_u32 s28, s26, s30
	s_addc_u32 s29, s27, 0
	global_load_dwordx2 v[46:47], v162, s[28:29]
	v_readlane_b32 s30, v122, 12
	s_lshl_b32 s30, s30, 12
	s_add_u32 s28, s26, s30
	s_addc_u32 s29, s27, 0
	global_load_dwordx2 v[48:49], v162, s[28:29]
	v_readlane_b32 s30, v122, 13
	s_lshl_b32 s30, s30, 12
	s_add_u32 s28, s26, s30
	s_addc_u32 s29, s27, 0
	global_load_dwordx2 v[50:51], v162, s[28:29]
	v_readlane_b32 s30, v122, 14
	s_lshl_b32 s30, s30, 12
	s_add_u32 s28, s26, s30
	s_addc_u32 s29, s27, 0
	global_load_dwordx2 v[52:53], v162, s[28:29]
	v_readlane_b32 s30, v122, 15
	s_lshl_b32 s30, s30, 12
	s_add_u32 s28, s26, s30
	s_addc_u32 s29, s27, 0
	global_load_dwordx2 v[54:55], v162, s[28:29]
	v_readlane_b32 s30, v122, 16
	s_lshl_b32 s30, s30, 12
	s_add_u32 s28, s26, s30
	s_addc_u32 s29, s27, 0
	global_load_dwordx2 v[56:57], v162, s[28:29]
	v_readlane_b32 s30, v122, 17
	s_lshl_b32 s30, s30, 12
	s_add_u32 s28, s26, s30
	s_addc_u32 s29, s27, 0
	global_load_dwordx2 v[58:59], v162, s[28:29]
	v_readlane_b32 s30, v122, 18
	s_lshl_b32 s30, s30, 12
	s_add_u32 s28, s26, s30
	s_addc_u32 s29, s27, 0
	global_load_dwordx2 v[60:61], v162, s[28:29]
	v_readlane_b32 s30, v122, 19
	s_lshl_b32 s30, s30, 12
	s_add_u32 s28, s26, s30
	s_addc_u32 s29, s27, 0
	global_load_dwordx2 v[62:63], v162, s[28:29]
	v_readlane_b32 s30, v122, 20
	s_lshl_b32 s30, s30, 12
	s_add_u32 s28, s26, s30
	s_addc_u32 s29, s27, 0
	global_load_dwordx2 v[64:65], v162, s[28:29]
	v_readlane_b32 s30, v122, 21
	s_lshl_b32 s30, s30, 12
	s_add_u32 s28, s26, s30
	s_addc_u32 s29, s27, 0
	global_load_dwordx2 v[66:67], v162, s[28:29]
	v_readlane_b32 s30, v122, 22
	s_lshl_b32 s30, s30, 12
	s_add_u32 s28, s26, s30
	s_addc_u32 s29, s27, 0
	global_load_dwordx2 v[68:69], v162, s[28:29]
	v_readlane_b32 s30, v122, 23
	s_lshl_b32 s30, s30, 12
	s_add_u32 s28, s26, s30
	s_addc_u32 s29, s27, 0
	global_load_dwordx2 v[70:71], v162, s[28:29]
	v_readlane_b32 s30, v122, 24
	s_lshl_b32 s30, s30, 12
	s_add_u32 s28, s26, s30
	s_addc_u32 s29, s27, 0
	global_load_dwordx2 v[72:73], v162, s[28:29]
	v_readlane_b32 s30, v122, 25
	s_lshl_b32 s30, s30, 12
	s_add_u32 s28, s26, s30
	s_addc_u32 s29, s27, 0
	global_load_dwordx2 v[74:75], v162, s[28:29]
	v_readlane_b32 s30, v122, 26
	s_lshl_b32 s30, s30, 12
	s_add_u32 s28, s26, s30
	s_addc_u32 s29, s27, 0
	global_load_dwordx2 v[76:77], v162, s[28:29]
	v_readlane_b32 s30, v122, 27
	s_lshl_b32 s30, s30, 12
	s_add_u32 s28, s26, s30
	s_addc_u32 s29, s27, 0
	global_load_dwordx2 v[78:79], v162, s[28:29]
	v_readlane_b32 s30, v122, 28
	s_lshl_b32 s30, s30, 12
	s_add_u32 s28, s26, s30
	s_addc_u32 s29, s27, 0
	global_load_dwordx2 v[80:81], v162, s[28:29]
	v_readlane_b32 s30, v122, 29
	s_lshl_b32 s30, s30, 12
	s_add_u32 s28, s26, s30
	s_addc_u32 s29, s27, 0
	global_load_dwordx2 v[82:83], v162, s[28:29]
	v_readlane_b32 s30, v122, 30
	s_lshl_b32 s30, s30, 12
	s_add_u32 s28, s26, s30
	s_addc_u32 s29, s27, 0
	global_load_dwordx2 v[84:85], v162, s[28:29]
	v_readlane_b32 s30, v122, 31
	s_lshl_b32 s30, s30, 12
	s_add_u32 s28, s26, s30
	s_addc_u32 s29, s27, 0
	global_load_dwordx2 v[86:87], v162, s[28:29]
.Lpa_tok:
	v_lshlrev_b32_e32 v124, 16, v116
	v_and_b32_e32 v125, 0xffff0000, v116
	v_pk_mul_f32 v[108:109], v[124:125], v[100:101]
	v_lshlrev_b32_e32 v124, 16, v117
	v_and_b32_e32 v125, 0xffff0000, v117
	v_pk_mul_f32 v[110:111], v[124:125], v[102:103]
	v_lshlrev_b32_e32 v124, 16, v118
	v_and_b32_e32 v125, 0xffff0000, v118
	v_pk_mul_f32 v[112:113], v[124:125], v[104:105]
	v_lshlrev_b32_e32 v124, 16, v119
	v_and_b32_e32 v125, 0xffff0000, v119
	v_pk_mul_f32 v[114:115], v[124:125], v[106:107]
	v_add_f32_e32 v16, v108, v109
	v_add_f32_e32 v17, v110, v111
	v_add_f32_e32 v18, v112, v113
	v_add_f32_e32 v19, v114, v115
	v_add_f32_e32 v16, v16, v17
	v_add_f32_e32 v18, v18, v19
	v_add_f32_e32 v16, v16, v18
	s_nop 1
	v_add_f32_dpp v17, v16, v16 quad_perm:[1,0,3,2] row_mask:0xf bank_mask:0xf
	s_nop 1
	v_add_f32_dpp v16, v17, v17 quad_perm:[2,3,0,1] row_mask:0xf bank_mask:0xf
	s_nop 1
	v_add_f32_dpp v17, v16, v16 row_half_mirror row_mask:0xf bank_mask:0xf
	s_nop 1
	v_add_f32_dpp v16, v17, v17 row_ror:8 row_mask:0xf bank_mask:0xf
	v_mov_b32_e32 v17, v16
	s_nop 1
	v_permlane16_swap_b32_e32 v16, v17
	v_add_f32_e32 v16, v16, v17
	v_mov_b32_e32 v17, v16
	s_nop 1
	v_permlane32_swap_b32_e32 v16, v17
	v_add_f32_e32 v16, v16, v17
	s_lshl_b32 s30, s16, 5
	s_add_u32 s28, s22, s30
	s_addc_u32 s29, s23, 0
	v_mov_b32_e32 v19, 0
	s_mov_b64 exec, 1
	global_store_dword v19, v16, s[28:29]
	s_mov_b64 exec, -1
	v_mov_b32_e32 v120, v122
	v_mov_b32_e32 v121, v123
	s_lshl_b32 s30, s16, 9
	v_lshl_add_u64 v[22:23], v[176:177], 0, s[30:31]
	s_add_i32 s18, s16, 1
	s_min_i32 s18, s18, s24
	s_lshl_b32 s30, s18, 13
	v_lshl_add_u64 v[160:161], v[172:173], 0, s[30:31]
	global_load_dwordx4 v[116:119], v[160:161], off
	s_lshl_b32 s30, s18, 9
	v_lshl_add_u64 v[160:161], v[174:175], 0, s[30:31]
	global_load_dword v122, v[160:161], off
	global_load_dword v123, v[160:161], off offset:256
	s_waitcnt vmcnt(34)
	v_cvt_f32_ubyte0_e32 v124, v24
	v_cvt_f32_ubyte1_e32 v126, v24
	v_cvt_f32_ubyte2_e32 v128, v24
	v_cvt_f32_ubyte3_e32 v130, v24
	v_cvt_f32_ubyte0_e32 v132, v25
	v_cvt_f32_ubyte1_e32 v134, v25
	v_cvt_f32_ubyte2_e32 v136, v25
	v_cvt_f32_ubyte3_e32 v138, v25
	v_readlane_b32 s30, v120, 32
	s_lshl_b32 s30, s30, 12
	s_add_u32 s28, s26, s30
	s_addc_u32 s29, s27, 0
	global_load_dwordx2 v[24:25], v162, s[28:29]
	s_waitcnt vmcnt(34)
	v_cvt_f32_ubyte0_e32 v125, v26
	v_cvt_f32_ubyte1_e32 v127, v26
	v_cvt_f32_ubyte2_e32 v129, v26
	v_cvt_f32_ubyte3_e32 v131, v26
	v_cvt_f32_ubyte0_e32 v133, v27
	v_cvt_f32_ubyte1_e32 v135, v27
	v_cvt_f32_ubyte2_e32 v137, v27
	v_cvt_f32_ubyte3_e32 v139, v27
	v_readlane_b32 s30, v120, 33
	s_lshl_b32 s30, s30, 12
	s_add_u32 s28, s26, s30
	s_addc_u32 s29, s27, 0
	global_load_dwordx2 v[26:27], v162, s[28:29]
	s_waitcnt vmcnt(34)
	v_cvt_f32_ubyte0_e32 v140, v28
	v_cvt_f32_ubyte1_e32 v142, v28
	v_cvt_f32_ubyte2_e32 v144, v28
	v_cvt_f32_ubyte3_e32 v146, v28
	v_cvt_f32_ubyte0_e32 v148, v29
	v_cvt_f32_ubyte1_e32 v150, v29
	v_cvt_f32_ubyte2_e32 v152, v29
	v_cvt_f32_ubyte3_e32 v154, v29
	v_readlane_b32 s30, v120, 34
	s_lshl_b32 s30, s30, 12
	s_add_u32 s28, s26, s30
	s_addc_u32 s29, s27, 0
	global_load_dwordx2 v[28:29], v162, s[28:29]
	s_waitcnt vmcnt(34)
	v_cvt_f32_ubyte0_e32 v141, v30
	v_cvt_f32_ubyte1_e32 v143, v30
	v_cvt_f32_ubyte2_e32 v145, v30
	v_cvt_f32_ubyte3_e32 v147, v30
	v_cvt_f32_ubyte0_e32 v149, v31
	v_cvt_f32_ubyte1_e32 v151, v31
	v_cvt_f32_ubyte2_e32 v153, v31
	v_cvt_f32_ubyte3_e32 v155, v31
	v_readlane_b32 s30, v120, 35
	s_lshl_b32 s30, s30, 12
	s_add_u32 s28, s26, s30
	s_addc_u32 s29, s27, 0
	global_load_dwordx2 v[30:31], v162, s[28:29]
	v_mul_f32_e32 v178, v124, v108
	v_mul_f32_e32 v179, v125, v108
	v_mul_f32_e32 v180, v140, v108
	v_mul_f32_e32 v181, v141, v108
	v_fmac_f32_e32 v178, v126, v109
	v_fmac_f32_e32 v179, v127, v109
	v_fmac_f32_e32 v180, v142, v109
	v_fmac_f32_e32 v181, v143, v109
	v_fmac_f32_e32 v178, v128, v110
	v_fmac_f32_e32 v179, v129, v110
	v_fmac_f32_e32 v180, v144, v110
	v_fmac_f32_e32 v181, v145, v110
	v_fmac_f32_e32 v178, v130, v111
	v_fmac_f32_e32 v179, v131, v111
	v_fmac_f32_e32 v180, v146, v111
	v_fmac_f32_e32 v181, v147, v111
	v_fmac_f32_e32 v178, v132, v112
	v_fmac_f32_e32 v179, v133, v112
	v_fmac_f32_e32 v180, v148, v112
	v_fmac_f32_e32 v181, v149, v112
	v_fmac_f32_e32 v178, v134, v113
	v_fmac_f32_e32 v179, v135, v113
	v_fmac_f32_e32 v180, v150, v113
	v_fmac_f32_e32 v181, v151, v113
	v_fmac_f32_e32 v178, v136, v114
	v_fmac_f32_e32 v179, v137, v114
	v_fmac_f32_e32 v180, v152, v114
	v_fmac_f32_e32 v181, v153, v114
	v_fmac_f32_e32 v178, v138, v115
	v_fmac_f32_e32 v179, v139, v115
	v_fmac_f32_e32 v180, v154, v115
	v_fmac_f32_e32 v181, v155, v115
	s_waitcnt vmcnt(34)
	v_cvt_f32_ubyte0_e32 v124, v32
	v_cvt_f32_ubyte1_e32 v126, v32
	v_cvt_f32_ubyte2_e32 v128, v32
	v_cvt_f32_ubyte3_e32 v130, v32
	v_cvt_f32_ubyte0_e32 v132, v33
	v_cvt_f32_ubyte1_e32 v134, v33
	v_cvt_f32_ubyte2_e32 v136, v33
	v_cvt_f32_ubyte3_e32 v138, v33
	v_readlane_b32 s30, v120, 36
	s_lshl_b32 s30, s30, 12
	s_add_u32 s28, s26, s30
	s_addc_u32 s29, s27, 0
	global_load_dwordx2 v[32:33], v162, s[28:29]
	s_waitcnt vmcnt(34)
	v_cvt_f32_ubyte0_e32 v125, v34
	v_cvt_f32_ubyte1_e32 v127, v34
	v_cvt_f32_ubyte2_e32 v129, v34
	v_cvt_f32_ubyte3_e32 v131, v34
	v_cvt_f32_ubyte0_e32 v133, v35
	v_cvt_f32_ubyte1_e32 v135, v35
	v_cvt_f32_ubyte2_e32 v137, v35
	v_cvt_f32_ubyte3_e32 v139, v35
	v_readlane_b32 s30, v120, 37
	s_lshl_b32 s30, s30, 12
	s_add_u32 s28, s26, s30
	s_addc_u32 s29, s27, 0
	global_load_dwordx2 v[34:35], v162, s[28:29]
	s_waitcnt vmcnt(34)
	v_cvt_f32_ubyte0_e32 v140, v36
	v_cvt_f32_ubyte1_e32 v142, v36
	v_cvt_f32_ubyte2_e32 v144, v36
	v_cvt_f32_ubyte3_e32 v146, v36
	v_cvt_f32_ubyte0_e32 v148, v37
	v_cvt_f32_ubyte1_e32 v150, v37
	v_cvt_f32_ubyte2_e32 v152, v37
	v_cvt_f32_ubyte3_e32 v154, v37
	v_readlane_b32 s30, v120, 38
	s_lshl_b32 s30, s30, 12
	s_add_u32 s28, s26, s30
	s_addc_u32 s29, s27, 0
	global_load_dwordx2 v[36:37], v162, s[28:29]
	s_waitcnt vmcnt(34)
	v_cvt_f32_ubyte0_e32 v141, v38
	v_cvt_f32_ubyte1_e32 v143, v38
	v_cvt_f32_ubyte2_e32 v145, v38
	v_cvt_f32_ubyte3_e32 v147, v38
	v_cvt_f32_ubyte0_e32 v149, v39
	v_cvt_f32_ubyte1_e32 v151, v39
	v_cvt_f32_ubyte2_e32 v153, v39
	v_cvt_f32_ubyte3_e32 v155, v39
	v_readlane_b32 s30, v120, 39
	s_lshl_b32 s30, s30, 12
	s_add_u32 s28, s26, s30
	s_addc_u32 s29, s27, 0
	global_load_dwordx2 v[38:39], v162, s[28:29]
	v_mul_f32_e32 v182, v124, v108
	v_mul_f32_e32 v183, v125, v108
	v_mul_f32_e32 v184, v140, v108
	v_mul_f32_e32 v185, v141, v108
	v_fmac_f32_e32 v182, v126, v109
	v_fmac_f32_e32 v183, v127, v109
	v_fmac_f32_e32 v184, v142, v109
	v_fmac_f32_e32 v185, v143, v109
	v_fmac_f32_e32 v182, v128, v110
	v_fmac_f32_e32 v183, v129, v110
	v_fmac_f32_e32 v184, v144, v110
	v_fmac_f32_e32 v185, v145, v110
	v_fmac_f32_e32 v182, v130, v111
	v_fmac_f32_e32 v183, v131, v111
	v_fmac_f32_e32 v184, v146, v111
	v_fmac_f32_e32 v185, v147, v111
	v_fmac_f32_e32 v182, v132, v112
	v_fmac_f32_e32 v183, v133, v112
	v_fmac_f32_e32 v184, v148, v112
	v_fmac_f32_e32 v185, v149, v112
	v_fmac_f32_e32 v182, v134, v113
	v_fmac_f32_e32 v183, v135, v113
	v_fmac_f32_e32 v184, v150, v113
	v_fmac_f32_e32 v185, v151, v113
	v_fmac_f32_e32 v182, v136, v114
	v_fmac_f32_e32 v183, v137, v114
	v_fmac_f32_e32 v184, v152, v114
	v_fmac_f32_e32 v185, v153, v114
	v_fmac_f32_e32 v182, v138, v115
	v_fmac_f32_e32 v183, v139, v115
	v_fmac_f32_e32 v184, v154, v115
	v_fmac_f32_e32 v185, v155, v115
	s_waitcnt vmcnt(34)
	v_cvt_f32_ubyte0_e32 v124, v40
	v_cvt_f32_ubyte1_e32 v126, v40
	v_cvt_f32_ubyte2_e32 v128, v40
	v_cvt_f32_ubyte3_e32 v130, v40
	v_cvt_f32_ubyte0_e32 v132, v41
	v_cvt_f32_ubyte1_e32 v134, v41
	v_cvt_f32_ubyte2_e32 v136, v41
	v_cvt_f32_ubyte3_e32 v138, v41
	v_readlane_b32 s30, v120, 40
	s_lshl_b32 s30, s30, 12
	s_add_u32 s28, s26, s30
	s_addc_u32 s29, s27, 0
	global_load_dwordx2 v[40:41], v162, s[28:29]
	s_waitcnt vmcnt(34)
	v_cvt_f32_ubyte0_e32 v125, v42
	v_cvt_f32_ubyte1_e32 v127, v42
	v_cvt_f32_ubyte2_e32 v129, v42
	v_cvt_f32_ubyte3_e32 v131, v42
	v_cvt_f32_ubyte0_e32 v133, v43
	v_cvt_f32_ubyte1_e32 v135, v43
	v_cvt_f32_ubyte2_e32 v137, v43
	v_cvt_f32_ubyte3_e32 v139, v43
	v_readlane_b32 s30, v120, 41
	s_lshl_b32 s30, s30, 12
	s_add_u32 s28, s26, s30
	s_addc_u32 s29, s27, 0
	global_load_dwordx2 v[42:43], v162, s[28:29]
	s_waitcnt vmcnt(34)
	v_cvt_f32_ubyte0_e32 v140, v44
	v_cvt_f32_ubyte1_e32 v142, v44
	v_cvt_f32_ubyte2_e32 v144, v44
	v_cvt_f32_ubyte3_e32 v146, v44
	v_cvt_f32_ubyte0_e32 v148, v45
	v_cvt_f32_ubyte1_e32 v150, v45
	v_cvt_f32_ubyte2_e32 v152, v45
	v_cvt_f32_ubyte3_e32 v154, v45
	v_readlane_b32 s30, v120, 42
	s_lshl_b32 s30, s30, 12
	s_add_u32 s28, s26, s30
	s_addc_u32 s29, s27, 0
	global_load_dwordx2 v[44:45], v162, s[28:29]
	s_waitcnt vmcnt(34)
	v_cvt_f32_ubyte0_e32 v141, v46
	v_cvt_f32_ubyte1_e32 v143, v46
	v_cvt_f32_ubyte2_e32 v145, v46
	v_cvt_f32_ubyte3_e32 v147, v46
	v_cvt_f32_ubyte0_e32 v149, v47
	v_cvt_f32_ubyte1_e32 v151, v47
	v_cvt_f32_ubyte2_e32 v153, v47
	v_cvt_f32_ubyte3_e32 v155, v47
	v_readlane_b32 s30, v120, 43
	s_lshl_b32 s30, s30, 12
	s_add_u32 s28, s26, s30
	s_addc_u32 s29, s27, 0
	global_load_dwordx2 v[46:47], v162, s[28:29]
	v_mul_f32_e32 v186, v124, v108
	v_mul_f32_e32 v187, v125, v108
	v_mul_f32_e32 v188, v140, v108
	v_mul_f32_e32 v189, v141, v108
	v_fmac_f32_e32 v186, v126, v109
	v_fmac_f32_e32 v187, v127, v109
	v_fmac_f32_e32 v188, v142, v109
	v_fmac_f32_e32 v189, v143, v109
	v_fmac_f32_e32 v186, v128, v110
	v_fmac_f32_e32 v187, v129, v110
	v_fmac_f32_e32 v188, v144, v110
	v_fmac_f32_e32 v189, v145, v110
	v_fmac_f32_e32 v186, v130, v111
	v_fmac_f32_e32 v187, v131, v111
	v_fmac_f32_e32 v188, v146, v111
	v_fmac_f32_e32 v189, v147, v111
	v_fmac_f32_e32 v186, v132, v112
	v_fmac_f32_e32 v187, v133, v112
	v_fmac_f32_e32 v188, v148, v112
	v_fmac_f32_e32 v189, v149, v112
	v_fmac_f32_e32 v186, v134, v113
	v_fmac_f32_e32 v187, v135, v113
	v_fmac_f32_e32 v188, v150, v113
	v_fmac_f32_e32 v189, v151, v113
	v_fmac_f32_e32 v186, v136, v114
	v_fmac_f32_e32 v187, v137, v114
	v_fmac_f32_e32 v188, v152, v114
	v_fmac_f32_e32 v189, v153, v114
	v_fmac_f32_e32 v186, v138, v115
	v_fmac_f32_e32 v187, v139, v115
	v_fmac_f32_e32 v188, v154, v115
	v_fmac_f32_e32 v189, v155, v115
	s_waitcnt vmcnt(34)
	v_cvt_f32_ubyte0_e32 v124, v48
	v_cvt_f32_ubyte1_e32 v126, v48
	v_cvt_f32_ubyte2_e32 v128, v48
	v_cvt_f32_ubyte3_e32 v130, v48
	v_cvt_f32_ubyte0_e32 v132, v49
	v_cvt_f32_ubyte1_e32 v134, v49
	v_cvt_f32_ubyte2_e32 v136, v49
	v_cvt_f32_ubyte3_e32 v138, v49
	v_readlane_b32 s30, v120, 44
	s_lshl_b32 s30, s30, 12
	s_add_u32 s28, s26, s30
	s_addc_u32 s29, s27, 0
	global_load_dwordx2 v[48:49], v162, s[28:29]
	s_waitcnt vmcnt(34)
	v_cvt_f32_ubyte0_e32 v125, v50
	v_cvt_f32_ubyte1_e32 v127, v50
	v_cvt_f32_ubyte2_e32 v129, v50
	v_cvt_f32_ubyte3_e32 v131, v50
	v_cvt_f32_ubyte0_e32 v133, v51
	v_cvt_f32_ubyte1_e32 v135, v51
	v_cvt_f32_ubyte2_e32 v137, v51
	v_cvt_f32_ubyte3_e32 v139, v51
	v_readlane_b32 s30, v120, 45
	s_lshl_b32 s30, s30, 12
	s_add_u32 s28, s26, s30
	s_addc_u32 s29, s27, 0
	global_load_dwordx2 v[50:51], v162, s[28:29]
	s_waitcnt vmcnt(34)
	v_cvt_f32_ubyte0_e32 v140, v52
	v_cvt_f32_ubyte1_e32 v142, v52
	v_cvt_f32_ubyte2_e32 v144, v52
	v_cvt_f32_ubyte3_e32 v146, v52
	v_cvt_f32_ubyte0_e32 v148, v53
	v_cvt_f32_ubyte1_e32 v150, v53
	v_cvt_f32_ubyte2_e32 v152, v53
	v_cvt_f32_ubyte3_e32 v154, v53
	v_readlane_b32 s30, v120, 46
	s_lshl_b32 s30, s30, 12
	s_add_u32 s28, s26, s30
	s_addc_u32 s29, s27, 0
	global_load_dwordx2 v[52:53], v162, s[28:29]
	s_waitcnt vmcnt(34)
	v_cvt_f32_ubyte0_e32 v141, v54
	v_cvt_f32_ubyte1_e32 v143, v54
	v_cvt_f32_ubyte2_e32 v145, v54
	v_cvt_f32_ubyte3_e32 v147, v54
	v_cvt_f32_ubyte0_e32 v149, v55
	v_cvt_f32_ubyte1_e32 v151, v55
	v_cvt_f32_ubyte2_e32 v153, v55
	v_cvt_f32_ubyte3_e32 v155, v55
	v_readlane_b32 s30, v120, 47
	s_lshl_b32 s30, s30, 12
	s_add_u32 s28, s26, s30
	s_addc_u32 s29, s27, 0
	global_load_dwordx2 v[54:55], v162, s[28:29]
	v_mul_f32_e32 v190, v124, v108
	v_mul_f32_e32 v191, v125, v108
	v_mul_f32_e32 v192, v140, v108
	v_mul_f32_e32 v193, v141, v108
	v_fmac_f32_e32 v190, v126, v109
	v_fmac_f32_e32 v191, v127, v109
	v_fmac_f32_e32 v192, v142, v109
	v_fmac_f32_e32 v193, v143, v109
	v_fmac_f32_e32 v190, v128, v110
	v_fmac_f32_e32 v191, v129, v110
	v_fmac_f32_e32 v192, v144, v110
	v_fmac_f32_e32 v193, v145, v110
	v_fmac_f32_e32 v190, v130, v111
	v_fmac_f32_e32 v191, v131, v111
	v_fmac_f32_e32 v192, v146, v111
	v_fmac_f32_e32 v193, v147, v111
	v_fmac_f32_e32 v190, v132, v112
	v_fmac_f32_e32 v191, v133, v112
	v_fmac_f32_e32 v192, v148, v112
	v_fmac_f32_e32 v193, v149, v112
	v_fmac_f32_e32 v190, v134, v113
	v_fmac_f32_e32 v191, v135, v113
	v_fmac_f32_e32 v192, v150, v113
	v_fmac_f32_e32 v193, v151, v113
	v_fmac_f32_e32 v190, v136, v114
	v_fmac_f32_e32 v191, v137, v114
	v_fmac_f32_e32 v192, v152, v114
	v_fmac_f32_e32 v193, v153, v114
	v_fmac_f32_e32 v190, v138, v115
	v_fmac_f32_e32 v191, v139, v115
	v_fmac_f32_e32 v192, v154, v115
	v_fmac_f32_e32 v193, v155, v115
	s_waitcnt vmcnt(34)
	v_cvt_f32_ubyte0_e32 v124, v56
	v_cvt_f32_ubyte1_e32 v126, v56
	v_cvt_f32_ubyte2_e32 v128, v56
	v_cvt_f32_ubyte3_e32 v130, v56
	v_cvt_f32_ubyte0_e32 v132, v57
	v_cvt_f32_ubyte1_e32 v134, v57
	v_cvt_f32_ubyte2_e32 v136, v57
	v_cvt_f32_ubyte3_e32 v138, v57
	v_readlane_b32 s30, v120, 48
	s_lshl_b32 s30, s30, 12
	s_add_u32 s28, s26, s30
	s_addc_u32 s29, s27, 0
	global_load_dwordx2 v[56:57], v162, s[28:29]
	s_waitcnt vmcnt(34)
	v_cvt_f32_ubyte0_e32 v125, v58
	v_cvt_f32_ubyte1_e32 v127, v58
	v_cvt_f32_ubyte2_e32 v129, v58
	v_cvt_f32_ubyte3_e32 v131, v58
	v_cvt_f32_ubyte0_e32 v133, v59
	v_cvt_f32_ubyte1_e32 v135, v59
	v_cvt_f32_ubyte2_e32 v137, v59
	v_cvt_f32_ubyte3_e32 v139, v59
	v_readlane_b32 s30, v120, 49
	s_lshl_b32 s30, s30, 12
	s_add_u32 s28, s26, s30
	s_addc_u32 s29, s27, 0
	global_load_dwordx2 v[58:59], v162, s[28:29]
	s_waitcnt vmcnt(34)
	v_cvt_f32_ubyte0_e32 v140, v60
	v_cvt_f32_ubyte1_e32 v142, v60
	v_cvt_f32_ubyte2_e32 v144, v60
	v_cvt_f32_ubyte3_e32 v146, v60
	v_cvt_f32_ubyte0_e32 v148, v61
	v_cvt_f32_ubyte1_e32 v150, v61
	v_cvt_f32_ubyte2_e32 v152, v61
	v_cvt_f32_ubyte3_e32 v154, v61
	v_readlane_b32 s30, v120, 50
	s_lshl_b32 s30, s30, 12
	s_add_u32 s28, s26, s30
	s_addc_u32 s29, s27, 0
	global_load_dwordx2 v[60:61], v162, s[28:29]
	s_waitcnt vmcnt(34)
	v_cvt_f32_ubyte0_e32 v141, v62
	v_cvt_f32_ubyte1_e32 v143, v62
	v_cvt_f32_ubyte2_e32 v145, v62
	v_cvt_f32_ubyte3_e32 v147, v62
	v_cvt_f32_ubyte0_e32 v149, v63
	v_cvt_f32_ubyte1_e32 v151, v63
	v_cvt_f32_ubyte2_e32 v153, v63
	v_cvt_f32_ubyte3_e32 v155, v63
	v_readlane_b32 s30, v120, 51
	s_lshl_b32 s30, s30, 12
	s_add_u32 s28, s26, s30
	s_addc_u32 s29, s27, 0
	global_load_dwordx2 v[62:63], v162, s[28:29]
	v_mul_f32_e32 v194, v124, v108
	v_mul_f32_e32 v195, v125, v108
	v_mul_f32_e32 v196, v140, v108
	v_mul_f32_e32 v197, v141, v108
	v_fmac_f32_e32 v194, v126, v109
	v_fmac_f32_e32 v195, v127, v109
	v_fmac_f32_e32 v196, v142, v109
	v_fmac_f32_e32 v197, v143, v109
	v_fmac_f32_e32 v194, v128, v110
	v_fmac_f32_e32 v195, v129, v110
	v_fmac_f32_e32 v196, v144, v110
	v_fmac_f32_e32 v197, v145, v110
	v_fmac_f32_e32 v194, v130, v111
	v_fmac_f32_e32 v195, v131, v111
	v_fmac_f32_e32 v196, v146, v111
	v_fmac_f32_e32 v197, v147, v111
	v_fmac_f32_e32 v194, v132, v112
	v_fmac_f32_e32 v195, v133, v112
	v_fmac_f32_e32 v196, v148, v112
	v_fmac_f32_e32 v197, v149, v112
	v_fmac_f32_e32 v194, v134, v113
	v_fmac_f32_e32 v195, v135, v113
	v_fmac_f32_e32 v196, v150, v113
	v_fmac_f32_e32 v197, v151, v113
	v_fmac_f32_e32 v194, v136, v114
	v_fmac_f32_e32 v195, v137, v114
	v_fmac_f32_e32 v196, v152, v114
	v_fmac_f32_e32 v197, v153, v114
	v_fmac_f32_e32 v194, v138, v115
	v_fmac_f32_e32 v195, v139, v115
	v_fmac_f32_e32 v196, v154, v115
	v_fmac_f32_e32 v197, v155, v115
	s_waitcnt vmcnt(34)
	v_cvt_f32_ubyte0_e32 v124, v64
	v_cvt_f32_ubyte1_e32 v126, v64
	v_cvt_f32_ubyte2_e32 v128, v64
	v_cvt_f32_ubyte3_e32 v130, v64
	v_cvt_f32_ubyte0_e32 v132, v65
	v_cvt_f32_ubyte1_e32 v134, v65
	v_cvt_f32_ubyte2_e32 v136, v65
	v_cvt_f32_ubyte3_e32 v138, v65
	v_readlane_b32 s30, v120, 52
	s_lshl_b32 s30, s30, 12
	s_add_u32 s28, s26, s30
	s_addc_u32 s29, s27, 0
	global_load_dwordx2 v[64:65], v162, s[28:29]
	s_waitcnt vmcnt(34)
	v_cvt_f32_ubyte0_e32 v125, v66
	v_cvt_f32_ubyte1_e32 v127, v66
	v_cvt_f32_ubyte2_e32 v129, v66
	v_cvt_f32_ubyte3_e32 v131, v66
	v_cvt_f32_ubyte0_e32 v133, v67
	v_cvt_f32_ubyte1_e32 v135, v67
	v_cvt_f32_ubyte2_e32 v137, v67
	v_cvt_f32_ubyte3_e32 v139, v67
	v_readlane_b32 s30, v120, 53
	s_lshl_b32 s30, s30, 12
	s_add_u32 s28, s26, s30
	s_addc_u32 s29, s27, 0
	global_load_dwordx2 v[66:67], v162, s[28:29]
	s_waitcnt vmcnt(34)
	v_cvt_f32_ubyte0_e32 v140, v68
	v_cvt_f32_ubyte1_e32 v142, v68
	v_cvt_f32_ubyte2_e32 v144, v68
	v_cvt_f32_ubyte3_e32 v146, v68
	v_cvt_f32_ubyte0_e32 v148, v69
	v_cvt_f32_ubyte1_e32 v150, v69
	v_cvt_f32_ubyte2_e32 v152, v69
	v_cvt_f32_ubyte3_e32 v154, v69
	v_readlane_b32 s30, v120, 54
	s_lshl_b32 s30, s30, 12
	s_add_u32 s28, s26, s30
	s_addc_u32 s29, s27, 0
	global_load_dwordx2 v[68:69], v162, s[28:29]
	s_waitcnt vmcnt(34)
	v_cvt_f32_ubyte0_e32 v141, v70
	v_cvt_f32_ubyte1_e32 v143, v70
	v_cvt_f32_ubyte2_e32 v145, v70
	v_cvt_f32_ubyte3_e32 v147, v70
	v_cvt_f32_ubyte0_e32 v149, v71
	v_cvt_f32_ubyte1_e32 v151, v71
	v_cvt_f32_ubyte2_e32 v153, v71
	v_cvt_f32_ubyte3_e32 v155, v71
	v_readlane_b32 s30, v120, 55
	s_lshl_b32 s30, s30, 12
	s_add_u32 s28, s26, s30
	s_addc_u32 s29, s27, 0
	global_load_dwordx2 v[70:71], v162, s[28:29]
	v_mul_f32_e32 v198, v124, v108
	v_mul_f32_e32 v199, v125, v108
	v_mul_f32_e32 v200, v140, v108
	v_mul_f32_e32 v201, v141, v108
	v_fmac_f32_e32 v198, v126, v109
	v_fmac_f32_e32 v199, v127, v109
	v_fmac_f32_e32 v200, v142, v109
	v_fmac_f32_e32 v201, v143, v109
	v_fmac_f32_e32 v198, v128, v110
	v_fmac_f32_e32 v199, v129, v110
	v_fmac_f32_e32 v200, v144, v110
	v_fmac_f32_e32 v201, v145, v110
	v_fmac_f32_e32 v198, v130, v111
	v_fmac_f32_e32 v199, v131, v111
	v_fmac_f32_e32 v200, v146, v111
	v_fmac_f32_e32 v201, v147, v111
	v_fmac_f32_e32 v198, v132, v112
	v_fmac_f32_e32 v199, v133, v112
	v_fmac_f32_e32 v200, v148, v112
	v_fmac_f32_e32 v201, v149, v112
	v_fmac_f32_e32 v198, v134, v113
	v_fmac_f32_e32 v199, v135, v113
	v_fmac_f32_e32 v200, v150, v113
	v_fmac_f32_e32 v201, v151, v113
	v_fmac_f32_e32 v198, v136, v114
	v_fmac_f32_e32 v199, v137, v114
	v_fmac_f32_e32 v200, v152, v114
	v_fmac_f32_e32 v201, v153, v114
	v_fmac_f32_e32 v198, v138, v115
	v_fmac_f32_e32 v199, v139, v115
	v_fmac_f32_e32 v200, v154, v115
	v_fmac_f32_e32 v201, v155, v115
	s_waitcnt vmcnt(34)
	v_cvt_f32_ubyte0_e32 v124, v72
	v_cvt_f32_ubyte1_e32 v126, v72
	v_cvt_f32_ubyte2_e32 v128, v72
	v_cvt_f32_ubyte3_e32 v130, v72
	v_cvt_f32_ubyte0_e32 v132, v73
	v_cvt_f32_ubyte1_e32 v134, v73
	v_cvt_f32_ubyte2_e32 v136, v73
	v_cvt_f32_ubyte3_e32 v138, v73
	v_readlane_b32 s30, v120, 56
	s_lshl_b32 s30, s30, 12
	s_add_u32 s28, s26, s30
	s_addc_u32 s29, s27, 0
	global_load_dwordx2 v[72:73], v162, s[28:29]
	s_waitcnt vmcnt(34)
	v_cvt_f32_ubyte0_e32 v125, v74
	v_cvt_f32_ubyte1_e32 v127, v74
	v_cvt_f32_ubyte2_e32 v129, v74
	v_cvt_f32_ubyte3_e32 v131, v74
	v_cvt_f32_ubyte0_e32 v133, v75
	v_cvt_f32_ubyte1_e32 v135, v75
	v_cvt_f32_ubyte2_e32 v137, v75
	v_cvt_f32_ubyte3_e32 v139, v75
	v_readlane_b32 s30, v120, 57
	s_lshl_b32 s30, s30, 12
	s_add_u32 s28, s26, s30
	s_addc_u32 s29, s27, 0
	global_load_dwordx2 v[74:75], v162, s[28:29]
	s_waitcnt vmcnt(34)
	v_cvt_f32_ubyte0_e32 v140, v76
	v_cvt_f32_ubyte1_e32 v142, v76
	v_cvt_f32_ubyte2_e32 v144, v76
	v_cvt_f32_ubyte3_e32 v146, v76
	v_cvt_f32_ubyte0_e32 v148, v77
	v_cvt_f32_ubyte1_e32 v150, v77
	v_cvt_f32_ubyte2_e32 v152, v77
	v_cvt_f32_ubyte3_e32 v154, v77
	v_readlane_b32 s30, v120, 58
	s_lshl_b32 s30, s30, 12
	s_add_u32 s28, s26, s30
	s_addc_u32 s29, s27, 0
	global_load_dwordx2 v[76:77], v162, s[28:29]
	s_waitcnt vmcnt(34)
	v_cvt_f32_ubyte0_e32 v141, v78
	v_cvt_f32_ubyte1_e32 v143, v78
	v_cvt_f32_ubyte2_e32 v145, v78
	v_cvt_f32_ubyte3_e32 v147, v78
	v_cvt_f32_ubyte0_e32 v149, v79
	v_cvt_f32_ubyte1_e32 v151, v79
	v_cvt_f32_ubyte2_e32 v153, v79
	v_cvt_f32_ubyte3_e32 v155, v79
	v_readlane_b32 s30, v120, 59
	s_lshl_b32 s30, s30, 12
	s_add_u32 s28, s26, s30
	s_addc_u32 s29, s27, 0
	global_load_dwordx2 v[78:79], v162, s[28:29]
	v_mul_f32_e32 v202, v124, v108
	v_mul_f32_e32 v203, v125, v108
	v_mul_f32_e32 v204, v140, v108
	v_mul_f32_e32 v205, v141, v108
	v_fmac_f32_e32 v202, v126, v109
	v_fmac_f32_e32 v203, v127, v109
	v_fmac_f32_e32 v204, v142, v109
	v_fmac_f32_e32 v205, v143, v109
	v_fmac_f32_e32 v202, v128, v110
	v_fmac_f32_e32 v203, v129, v110
	v_fmac_f32_e32 v204, v144, v110
	v_fmac_f32_e32 v205, v145, v110
	v_fmac_f32_e32 v202, v130, v111
	v_fmac_f32_e32 v203, v131, v111
	v_fmac_f32_e32 v204, v146, v111
	v_fmac_f32_e32 v205, v147, v111
	v_fmac_f32_e32 v202, v132, v112
	v_fmac_f32_e32 v203, v133, v112
	v_fmac_f32_e32 v204, v148, v112
	v_fmac_f32_e32 v205, v149, v112
	v_fmac_f32_e32 v202, v134, v113
	v_fmac_f32_e32 v203, v135, v113
	v_fmac_f32_e32 v204, v150, v113
	v_fmac_f32_e32 v205, v151, v113
	v_fmac_f32_e32 v202, v136, v114
	v_fmac_f32_e32 v203, v137, v114
	v_fmac_f32_e32 v204, v152, v114
	v_fmac_f32_e32 v205, v153, v114
	v_fmac_f32_e32 v202, v138, v115
	v_fmac_f32_e32 v203, v139, v115
	v_fmac_f32_e32 v204, v154, v115
	v_fmac_f32_e32 v205, v155, v115
	s_waitcnt vmcnt(34)
	v_cvt_f32_ubyte0_e32 v124, v80
	v_cvt_f32_ubyte1_e32 v126, v80
	v_cvt_f32_ubyte2_e32 v128, v80
	v_cvt_f32_ubyte3_e32 v130, v80
	v_cvt_f32_ubyte0_e32 v132, v81
	v_cvt_f32_ubyte1_e32 v134, v81
	v_cvt_f32_ubyte2_e32 v136, v81
	v_cvt_f32_ubyte3_e32 v138, v81
	v_readlane_b32 s30, v120, 60
	s_lshl_b32 s30, s30, 12
	s_add_u32 s28, s26, s30
	s_addc_u32 s29, s27, 0
	global_load_dwordx2 v[80:81], v162, s[28:29]
	s_waitcnt vmcnt(34)
	v_cvt_f32_ubyte0_e32 v125, v82
	v_cvt_f32_ubyte1_e32 v127, v82
	v_cvt_f32_ubyte2_e32 v129, v82
	v_cvt_f32_ubyte3_e32 v131, v82
	v_cvt_f32_ubyte0_e32 v133, v83
	v_cvt_f32_ubyte1_e32 v135, v83
	v_cvt_f32_ubyte2_e32 v137, v83
	v_cvt_f32_ubyte3_e32 v139, v83
	v_readlane_b32 s30, v120, 61
	s_lshl_b32 s30, s30, 12
	s_add_u32 s28, s26, s30
	s_addc_u32 s29, s27, 0
	global_load_dwordx2 v[82:83], v162, s[28:29]
	s_waitcnt vmcnt(34)
	v_cvt_f32_ubyte0_e32 v140, v84
	v_cvt_f32_ubyte1_e32 v142, v84
	v_cvt_f32_ubyte2_e32 v144, v84
	v_cvt_f32_ubyte3_e32 v146, v84
	v_cvt_f32_ubyte0_e32 v148, v85
	v_cvt_f32_ubyte1_e32 v150, v85
	v_cvt_f32_ubyte2_e32 v152, v85
	v_cvt_f32_ubyte3_e32 v154, v85
	v_readlane_b32 s30, v120, 62
	s_lshl_b32 s30, s30, 12
	s_add_u32 s28, s26, s30
	s_addc_u32 s29, s27, 0
	global_load_dwordx2 v[84:85], v162, s[28:29]
	s_waitcnt vmcnt(34)
	v_cvt_f32_ubyte0_e32 v141, v86
	v_cvt_f32_ubyte1_e32 v143, v86
	v_cvt_f32_ubyte2_e32 v145, v86
	v_cvt_f32_ubyte3_e32 v147, v86
	v_cvt_f32_ubyte0_e32 v149, v87
	v_cvt_f32_ubyte1_e32 v151, v87
	v_cvt_f32_ubyte2_e32 v153, v87
	v_cvt_f32_ubyte3_e32 v155, v87
	v_readlane_b32 s30, v120, 63
	s_lshl_b32 s30, s30, 12
	s_add_u32 s28, s26, s30
	s_addc_u32 s29, s27, 0
	global_load_dwordx2 v[86:87], v162, s[28:29]
	v_mul_f32_e32 v206, v124, v108
	v_mul_f32_e32 v207, v125, v108
	v_mul_f32_e32 v208, v140, v108
	v_mul_f32_e32 v209, v141, v108
	v_fmac_f32_e32 v206, v126, v109
	v_fmac_f32_e32 v207, v127, v109
	v_fmac_f32_e32 v208, v142, v109
	v_fmac_f32_e32 v209, v143, v109
	v_fmac_f32_e32 v206, v128, v110
	v_fmac_f32_e32 v207, v129, v110
	v_fmac_f32_e32 v208, v144, v110
	v_fmac_f32_e32 v209, v145, v110
	v_fmac_f32_e32 v206, v130, v111
	v_fmac_f32_e32 v207, v131, v111
	v_fmac_f32_e32 v208, v146, v111
	v_fmac_f32_e32 v209, v147, v111
	v_fmac_f32_e32 v206, v132, v112
	v_fmac_f32_e32 v207, v133, v112
	v_fmac_f32_e32 v208, v148, v112
	v_fmac_f32_e32 v209, v149, v112
	v_fmac_f32_e32 v206, v134, v113
	v_fmac_f32_e32 v207, v135, v113
	v_fmac_f32_e32 v208, v150, v113
	v_fmac_f32_e32 v209, v151, v113
	v_fmac_f32_e32 v206, v136, v114
	v_fmac_f32_e32 v207, v137, v114
	v_fmac_f32_e32 v208, v152, v114
	v_fmac_f32_e32 v209, v153, v114
	v_fmac_f32_e32 v206, v138, v115
	v_fmac_f32_e32 v207, v139, v115
	v_fmac_f32_e32 v208, v154, v115
	v_fmac_f32_e32 v209, v155, v115
	v_permlane32_swap_b32_e32 v178, v194
	v_permlane32_swap_b32_e32 v179, v195
	v_permlane32_swap_b32_e32 v180, v196
	v_permlane32_swap_b32_e32 v181, v197
	v_permlane32_swap_b32_e32 v182, v198
	v_permlane32_swap_b32_e32 v183, v199
	v_permlane32_swap_b32_e32 v184, v200
	v_permlane32_swap_b32_e32 v185, v201
	v_permlane32_swap_b32_e32 v186, v202
	v_permlane32_swap_b32_e32 v187, v203
	v_permlane32_swap_b32_e32 v188, v204
	v_permlane32_swap_b32_e32 v189, v205
	v_permlane32_swap_b32_e32 v190, v206
	v_permlane32_swap_b32_e32 v191, v207
	v_permlane32_swap_b32_e32 v192, v208
	v_permlane32_swap_b32_e32 v193, v209
	v_add_f32_e32 v178, v178, v194
	v_add_f32_e32 v179, v179, v195
	v_add_f32_e32 v180, v180, v196
	v_add_f32_e32 v181, v181, v197
	v_add_f32_e32 v182, v182, v198
	v_add_f32_e32 v183, v183, v199
	v_add_f32_e32 v184, v184, v200
	v_add_f32_e32 v185, v185, v201
	v_add_f32_e32 v186, v186, v202
	v_add_f32_e32 v187, v187, v203
	v_add_f32_e32 v188, v188, v204
	v_add_f32_e32 v189, v189, v205
	v_add_f32_e32 v190, v190, v206
	v_add_f32_e32 v191, v191, v207
	v_add_f32_e32 v192, v192, v208
	v_add_f32_e32 v193, v193, v209
	v_permlane16_swap_b32_e32 v178, v186
	v_permlane16_swap_b32_e32 v179, v187
	v_permlane16_swap_b32_e32 v180, v188
	v_permlane16_swap_b32_e32 v181, v189
	v_permlane16_swap_b32_e32 v182, v190
	v_permlane16_swap_b32_e32 v183, v191
	v_permlane16_swap_b32_e32 v184, v192
	v_permlane16_swap_b32_e32 v185, v193
	v_add_f32_e32 v178, v178, v186
	v_add_f32_e32 v179, v179, v187
	v_add_f32_e32 v180, v180, v188
	v_add_f32_e32 v181, v181, v189
	v_add_f32_e32 v182, v182, v190
	v_add_f32_e32 v183, v183, v191
	v_add_f32_e32 v184, v184, v192
	v_add_f32_e32 v185, v185, v193
	v_cndmask_b32_e64 v2, v178, v182, s[8:9]
	v_cndmask_b32_e64 v3, v179, v183, s[8:9]
	v_cndmask_b32_e64 v4, v180, v184, s[8:9]
	v_cndmask_b32_e64 v5, v181, v185, s[8:9]
	v_cndmask_b32_e64 v6, v182, v178, s[8:9]
	v_cndmask_b32_e64 v7, v183, v179, s[8:9]
	v_cndmask_b32_e64 v8, v184, v180, s[8:9]
	v_cndmask_b32_e64 v9, v185, v181, s[8:9]
	v_add_f32_dpp v6, v2, v6 row_ror:8 row_mask:0xf bank_mask:0xf
	v_add_f32_dpp v7, v3, v7 row_ror:8 row_mask:0xf bank_mask:0xf
	v_add_f32_dpp v8, v4, v8 row_ror:8 row_mask:0xf bank_mask:0xf
	v_add_f32_dpp v9, v5, v9 row_ror:8 row_mask:0xf bank_mask:0xf
	v_cndmask_b32_e64 v2, v6, v8, s[10:11]
	v_cndmask_b32_e64 v3, v7, v9, s[10:11]
	v_cndmask_b32_e64 v4, v8, v6, s[10:11]
	v_cndmask_b32_e64 v5, v9, v7, s[10:11]
	v_add_f32_dpp v4, v2, v4 row_half_mirror row_mask:0xf bank_mask:0xf
	v_add_f32_dpp v5, v3, v5 row_half_mirror row_mask:0xf bank_mask:0xf
	v_cndmask_b32_e64 v2, v4, v5, s[14:15]
	v_cndmask_b32_e64 v3, v5, v4, s[14:15]
	s_nop 0
	v_add_f32_dpp v3, v2, v3 quad_perm:[2,3,0,1] row_mask:0xf bank_mask:0xf
	s_nop 1
	v_add_f32_dpp v11, v3, v3 quad_perm:[1,0,3,2] row_mask:0xf bank_mask:0xf
	s_mov_b64 exec, s[2:3]
	global_store_dword v[22:23], v11, off
	s_mov_b64 exec, -1
	s_waitcnt vmcnt(32)
	v_cvt_f32_ubyte0_e32 v124, v24
	v_cvt_f32_ubyte1_e32 v126, v24
	v_cvt_f32_ubyte2_e32 v128, v24
	v_cvt_f32_ubyte3_e32 v130, v24
	v_cvt_f32_ubyte0_e32 v132, v25
	v_cvt_f32_ubyte1_e32 v134, v25
	v_cvt_f32_ubyte2_e32 v136, v25
	v_cvt_f32_ubyte3_e32 v138, v25
	v_readlane_b32 s30, v121, 0
	s_lshl_b32 s30, s30, 12
	s_add_u32 s28, s26, s30
	s_addc_u32 s29, s27, 0
	global_load_dwordx2 v[24:25], v162, s[28:29]
	s_waitcnt vmcnt(32)
	v_cvt_f32_ubyte0_e32 v125, v26
	v_cvt_f32_ubyte1_e32 v127, v26
	v_cvt_f32_ubyte2_e32 v129, v26
	v_cvt_f32_ubyte3_e32 v131, v26
	v_cvt_f32_ubyte0_e32 v133, v27
	v_cvt_f32_ubyte1_e32 v135, v27
	v_cvt_f32_ubyte2_e32 v137, v27
	v_cvt_f32_ubyte3_e32 v139, v27
	v_readlane_b32 s30, v121, 1
	s_lshl_b32 s30, s30, 12
	s_add_u32 s28, s26, s30
	s_addc_u32 s29, s27, 0
	global_load_dwordx2 v[26:27], v162, s[28:29]
	s_waitcnt vmcnt(32)
	v_cvt_f32_ubyte0_e32 v140, v28
	v_cvt_f32_ubyte1_e32 v142, v28
	v_cvt_f32_ubyte2_e32 v144, v28
	v_cvt_f32_ubyte3_e32 v146, v28
	v_cvt_f32_ubyte0_e32 v148, v29
	v_cvt_f32_ubyte1_e32 v150, v29
	v_cvt_f32_ubyte2_e32 v152, v29
	v_cvt_f32_ubyte3_e32 v154, v29
	v_readlane_b32 s30, v121, 2
	s_lshl_b32 s30, s30, 12
	s_add_u32 s28, s26, s30
	s_addc_u32 s29, s27, 0
	global_load_dwordx2 v[28:29], v162, s[28:29]
	s_waitcnt vmcnt(32)
	v_cvt_f32_ubyte0_e32 v141, v30
	v_cvt_f32_ubyte1_e32 v143, v30
	v_cvt_f32_ubyte2_e32 v145, v30
	v_cvt_f32_ubyte3_e32 v147, v30
	v_cvt_f32_ubyte0_e32 v149, v31
	v_cvt_f32_ubyte1_e32 v151, v31
	v_cvt_f32_ubyte2_e32 v153, v31
	v_cvt_f32_ubyte3_e32 v155, v31
	v_readlane_b32 s30, v121, 3
	s_lshl_b32 s30, s30, 12
	s_add_u32 s28, s26, s30
	s_addc_u32 s29, s27, 0
	global_load_dwordx2 v[30:31], v162, s[28:29]
	v_mul_f32_e32 v178, v124, v108
	v_mul_f32_e32 v179, v125, v108
	v_mul_f32_e32 v180, v140, v108
	v_mul_f32_e32 v181, v141, v108
	v_fmac_f32_e32 v178, v126, v109
	v_fmac_f32_e32 v179, v127, v109
	v_fmac_f32_e32 v180, v142, v109
	v_fmac_f32_e32 v181, v143, v109
	v_fmac_f32_e32 v178, v128, v110
	v_fmac_f32_e32 v179, v129, v110
	v_fmac_f32_e32 v180, v144, v110
	v_fmac_f32_e32 v181, v145, v110
	v_fmac_f32_e32 v178, v130, v111
	v_fmac_f32_e32 v179, v131, v111
	v_fmac_f32_e32 v180, v146, v111
	v_fmac_f32_e32 v181, v147, v111
	v_fmac_f32_e32 v178, v132, v112
	v_fmac_f32_e32 v179, v133, v112
	v_fmac_f32_e32 v180, v148, v112
	v_fmac_f32_e32 v181, v149, v112
	v_fmac_f32_e32 v178, v134, v113
	v_fmac_f32_e32 v179, v135, v113
	v_fmac_f32_e32 v180, v150, v113
	v_fmac_f32_e32 v181, v151, v113
	v_fmac_f32_e32 v178, v136, v114
	v_fmac_f32_e32 v179, v137, v114
	v_fmac_f32_e32 v180, v152, v114
	v_fmac_f32_e32 v181, v153, v114
	v_fmac_f32_e32 v178, v138, v115
	v_fmac_f32_e32 v179, v139, v115
	v_fmac_f32_e32 v180, v154, v115
	v_fmac_f32_e32 v181, v155, v115
	s_waitcnt vmcnt(32)
	v_cvt_f32_ubyte0_e32 v124, v32
	v_cvt_f32_ubyte1_e32 v126, v32
	v_cvt_f32_ubyte2_e32 v128, v32
	v_cvt_f32_ubyte3_e32 v130, v32
	v_cvt_f32_ubyte0_e32 v132, v33
	v_cvt_f32_ubyte1_e32 v134, v33
	v_cvt_f32_ubyte2_e32 v136, v33
	v_cvt_f32_ubyte3_e32 v138, v33
	v_readlane_b32 s30, v121, 4
	s_lshl_b32 s30, s30, 12
	s_add_u32 s28, s26, s30
	s_addc_u32 s29, s27, 0
	global_load_dwordx2 v[32:33], v162, s[28:29]
	s_waitcnt vmcnt(32)
	v_cvt_f32_ubyte0_e32 v125, v34
	v_cvt_f32_ubyte1_e32 v127, v34
	v_cvt_f32_ubyte2_e32 v129, v34
	v_cvt_f32_ubyte3_e32 v131, v34
	v_cvt_f32_ubyte0_e32 v133, v35
	v_cvt_f32_ubyte1_e32 v135, v35
	v_cvt_f32_ubyte2_e32 v137, v35
	v_cvt_f32_ubyte3_e32 v139, v35
	v_readlane_b32 s30, v121, 5
	s_lshl_b32 s30, s30, 12
	s_add_u32 s28, s26, s30
	s_addc_u32 s29, s27, 0
	global_load_dwordx2 v[34:35], v162, s[28:29]
	s_waitcnt vmcnt(32)
	v_cvt_f32_ubyte0_e32 v140, v36
	v_cvt_f32_ubyte1_e32 v142, v36
	v_cvt_f32_ubyte2_e32 v144, v36
	v_cvt_f32_ubyte3_e32 v146, v36
	v_cvt_f32_ubyte0_e32 v148, v37
	v_cvt_f32_ubyte1_e32 v150, v37
	v_cvt_f32_ubyte2_e32 v152, v37
	v_cvt_f32_ubyte3_e32 v154, v37
	v_readlane_b32 s30, v121, 6
	s_lshl_b32 s30, s30, 12
	s_add_u32 s28, s26, s30
	s_addc_u32 s29, s27, 0
	global_load_dwordx2 v[36:37], v162, s[28:29]
	s_waitcnt vmcnt(32)
	v_cvt_f32_ubyte0_e32 v141, v38
	v_cvt_f32_ubyte1_e32 v143, v38
	v_cvt_f32_ubyte2_e32 v145, v38
	v_cvt_f32_ubyte3_e32 v147, v38
	v_cvt_f32_ubyte0_e32 v149, v39
	v_cvt_f32_ubyte1_e32 v151, v39
	v_cvt_f32_ubyte2_e32 v153, v39
	v_cvt_f32_ubyte3_e32 v155, v39
	v_readlane_b32 s30, v121, 7
	s_lshl_b32 s30, s30, 12
	s_add_u32 s28, s26, s30
	s_addc_u32 s29, s27, 0
	global_load_dwordx2 v[38:39], v162, s[28:29]
	v_mul_f32_e32 v182, v124, v108
	v_mul_f32_e32 v183, v125, v108
	v_mul_f32_e32 v184, v140, v108
	v_mul_f32_e32 v185, v141, v108
	v_fmac_f32_e32 v182, v126, v109
	v_fmac_f32_e32 v183, v127, v109
	v_fmac_f32_e32 v184, v142, v109
	v_fmac_f32_e32 v185, v143, v109
	v_fmac_f32_e32 v182, v128, v110
	v_fmac_f32_e32 v183, v129, v110
	v_fmac_f32_e32 v184, v144, v110
	v_fmac_f32_e32 v185, v145, v110
	v_fmac_f32_e32 v182, v130, v111
	v_fmac_f32_e32 v183, v131, v111
	v_fmac_f32_e32 v184, v146, v111
	v_fmac_f32_e32 v185, v147, v111
	v_fmac_f32_e32 v182, v132, v112
	v_fmac_f32_e32 v183, v133, v112
	v_fmac_f32_e32 v184, v148, v112
	v_fmac_f32_e32 v185, v149, v112
	v_fmac_f32_e32 v182, v134, v113
	v_fmac_f32_e32 v183, v135, v113
	v_fmac_f32_e32 v184, v150, v113
	v_fmac_f32_e32 v185, v151, v113
	v_fmac_f32_e32 v182, v136, v114
	v_fmac_f32_e32 v183, v137, v114
	v_fmac_f32_e32 v184, v152, v114
	v_fmac_f32_e32 v185, v153, v114
	v_fmac_f32_e32 v182, v138, v115
	v_fmac_f32_e32 v183, v139, v115
	v_fmac_f32_e32 v184, v154, v115
	v_fmac_f32_e32 v185, v155, v115
	s_waitcnt vmcnt(32)
	v_cvt_f32_ubyte0_e32 v124, v40
	v_cvt_f32_ubyte1_e32 v126, v40
	v_cvt_f32_ubyte2_e32 v128, v40
	v_cvt_f32_ubyte3_e32 v130, v40
	v_cvt_f32_ubyte0_e32 v132, v41
	v_cvt_f32_ubyte1_e32 v134, v41
	v_cvt_f32_ubyte2_e32 v136, v41
	v_cvt_f32_ubyte3_e32 v138, v41
	v_readlane_b32 s30, v121, 8
	s_lshl_b32 s30, s30, 12
	s_add_u32 s28, s26, s30
	s_addc_u32 s29, s27, 0
	global_load_dwordx2 v[40:41], v162, s[28:29]
	s_waitcnt vmcnt(32)
	v_cvt_f32_ubyte0_e32 v125, v42
	v_cvt_f32_ubyte1_e32 v127, v42
	v_cvt_f32_ubyte2_e32 v129, v42
	v_cvt_f32_ubyte3_e32 v131, v42
	v_cvt_f32_ubyte0_e32 v133, v43
	v_cvt_f32_ubyte1_e32 v135, v43
	v_cvt_f32_ubyte2_e32 v137, v43
	v_cvt_f32_ubyte3_e32 v139, v43
	v_readlane_b32 s30, v121, 9
	s_lshl_b32 s30, s30, 12
	s_add_u32 s28, s26, s30
	s_addc_u32 s29, s27, 0
	global_load_dwordx2 v[42:43], v162, s[28:29]
	s_waitcnt vmcnt(32)
	v_cvt_f32_ubyte0_e32 v140, v44
	v_cvt_f32_ubyte1_e32 v142, v44
	v_cvt_f32_ubyte2_e32 v144, v44
	v_cvt_f32_ubyte3_e32 v146, v44
	v_cvt_f32_ubyte0_e32 v148, v45
	v_cvt_f32_ubyte1_e32 v150, v45
	v_cvt_f32_ubyte2_e32 v152, v45
	v_cvt_f32_ubyte3_e32 v154, v45
	v_readlane_b32 s30, v121, 10
	s_lshl_b32 s30, s30, 12
	s_add_u32 s28, s26, s30
	s_addc_u32 s29, s27, 0
	global_load_dwordx2 v[44:45], v162, s[28:29]
	s_waitcnt vmcnt(32)
	v_cvt_f32_ubyte0_e32 v141, v46
	v_cvt_f32_ubyte1_e32 v143, v46
	v_cvt_f32_ubyte2_e32 v145, v46
	v_cvt_f32_ubyte3_e32 v147, v46
	v_cvt_f32_ubyte0_e32 v149, v47
	v_cvt_f32_ubyte1_e32 v151, v47
	v_cvt_f32_ubyte2_e32 v153, v47
	v_cvt_f32_ubyte3_e32 v155, v47
	v_readlane_b32 s30, v121, 11
	s_lshl_b32 s30, s30, 12
	s_add_u32 s28, s26, s30
	s_addc_u32 s29, s27, 0
	global_load_dwordx2 v[46:47], v162, s[28:29]
	v_mul_f32_e32 v186, v124, v108
	v_mul_f32_e32 v187, v125, v108
	v_mul_f32_e32 v188, v140, v108
	v_mul_f32_e32 v189, v141, v108
	v_fmac_f32_e32 v186, v126, v109
	v_fmac_f32_e32 v187, v127, v109
	v_fmac_f32_e32 v188, v142, v109
	v_fmac_f32_e32 v189, v143, v109
	v_fmac_f32_e32 v186, v128, v110
	v_fmac_f32_e32 v187, v129, v110
	v_fmac_f32_e32 v188, v144, v110
	v_fmac_f32_e32 v189, v145, v110
	v_fmac_f32_e32 v186, v130, v111
	v_fmac_f32_e32 v187, v131, v111
	v_fmac_f32_e32 v188, v146, v111
	v_fmac_f32_e32 v189, v147, v111
	v_fmac_f32_e32 v186, v132, v112
	v_fmac_f32_e32 v187, v133, v112
	v_fmac_f32_e32 v188, v148, v112
	v_fmac_f32_e32 v189, v149, v112
	v_fmac_f32_e32 v186, v134, v113
	v_fmac_f32_e32 v187, v135, v113
	v_fmac_f32_e32 v188, v150, v113
	v_fmac_f32_e32 v189, v151, v113
	v_fmac_f32_e32 v186, v136, v114
	v_fmac_f32_e32 v187, v137, v114
	v_fmac_f32_e32 v188, v152, v114
	v_fmac_f32_e32 v189, v153, v114
	v_fmac_f32_e32 v186, v138, v115
	v_fmac_f32_e32 v187, v139, v115
	v_fmac_f32_e32 v188, v154, v115
	v_fmac_f32_e32 v189, v155, v115
	s_waitcnt vmcnt(32)
	v_cvt_f32_ubyte0_e32 v124, v48
	v_cvt_f32_ubyte1_e32 v126, v48
	v_cvt_f32_ubyte2_e32 v128, v48
	v_cvt_f32_ubyte3_e32 v130, v48
	v_cvt_f32_ubyte0_e32 v132, v49
	v_cvt_f32_ubyte1_e32 v134, v49
	v_cvt_f32_ubyte2_e32 v136, v49
	v_cvt_f32_ubyte3_e32 v138, v49
	v_readlane_b32 s30, v121, 12
	s_lshl_b32 s30, s30, 12
	s_add_u32 s28, s26, s30
	s_addc_u32 s29, s27, 0
	global_load_dwordx2 v[48:49], v162, s[28:29]
	s_waitcnt vmcnt(32)
	v_cvt_f32_ubyte0_e32 v125, v50
	v_cvt_f32_ubyte1_e32 v127, v50
	v_cvt_f32_ubyte2_e32 v129, v50
	v_cvt_f32_ubyte3_e32 v131, v50
	v_cvt_f32_ubyte0_e32 v133, v51
	v_cvt_f32_ubyte1_e32 v135, v51
	v_cvt_f32_ubyte2_e32 v137, v51
	v_cvt_f32_ubyte3_e32 v139, v51
	v_readlane_b32 s30, v121, 13
	s_lshl_b32 s30, s30, 12
	s_add_u32 s28, s26, s30
	s_addc_u32 s29, s27, 0
	global_load_dwordx2 v[50:51], v162, s[28:29]
	s_waitcnt vmcnt(32)
	v_cvt_f32_ubyte0_e32 v140, v52
	v_cvt_f32_ubyte1_e32 v142, v52
	v_cvt_f32_ubyte2_e32 v144, v52
	v_cvt_f32_ubyte3_e32 v146, v52
	v_cvt_f32_ubyte0_e32 v148, v53
	v_cvt_f32_ubyte1_e32 v150, v53
	v_cvt_f32_ubyte2_e32 v152, v53
	v_cvt_f32_ubyte3_e32 v154, v53
	v_readlane_b32 s30, v121, 14
	s_lshl_b32 s30, s30, 12
	s_add_u32 s28, s26, s30
	s_addc_u32 s29, s27, 0
	global_load_dwordx2 v[52:53], v162, s[28:29]
	s_waitcnt vmcnt(32)
	v_cvt_f32_ubyte0_e32 v141, v54
	v_cvt_f32_ubyte1_e32 v143, v54
	v_cvt_f32_ubyte2_e32 v145, v54
	v_cvt_f32_ubyte3_e32 v147, v54
	v_cvt_f32_ubyte0_e32 v149, v55
	v_cvt_f32_ubyte1_e32 v151, v55
	v_cvt_f32_ubyte2_e32 v153, v55
	v_cvt_f32_ubyte3_e32 v155, v55
	v_readlane_b32 s30, v121, 15
	s_lshl_b32 s30, s30, 12
	s_add_u32 s28, s26, s30
	s_addc_u32 s29, s27, 0
	global_load_dwordx2 v[54:55], v162, s[28:29]
	v_mul_f32_e32 v190, v124, v108
	v_mul_f32_e32 v191, v125, v108
	v_mul_f32_e32 v192, v140, v108
	v_mul_f32_e32 v193, v141, v108
	v_fmac_f32_e32 v190, v126, v109
	v_fmac_f32_e32 v191, v127, v109
	v_fmac_f32_e32 v192, v142, v109
	v_fmac_f32_e32 v193, v143, v109
	v_fmac_f32_e32 v190, v128, v110
	v_fmac_f32_e32 v191, v129, v110
	v_fmac_f32_e32 v192, v144, v110
	v_fmac_f32_e32 v193, v145, v110
	v_fmac_f32_e32 v190, v130, v111
	v_fmac_f32_e32 v191, v131, v111
	v_fmac_f32_e32 v192, v146, v111
	v_fmac_f32_e32 v193, v147, v111
	v_fmac_f32_e32 v190, v132, v112
	v_fmac_f32_e32 v191, v133, v112
	v_fmac_f32_e32 v192, v148, v112
	v_fmac_f32_e32 v193, v149, v112
	v_fmac_f32_e32 v190, v134, v113
	v_fmac_f32_e32 v191, v135, v113
	v_fmac_f32_e32 v192, v150, v113
	v_fmac_f32_e32 v193, v151, v113
	v_fmac_f32_e32 v190, v136, v114
	v_fmac_f32_e32 v191, v137, v114
	v_fmac_f32_e32 v192, v152, v114
	v_fmac_f32_e32 v193, v153, v114
	v_fmac_f32_e32 v190, v138, v115
	v_fmac_f32_e32 v191, v139, v115
	v_fmac_f32_e32 v192, v154, v115
	v_fmac_f32_e32 v193, v155, v115
	s_waitcnt vmcnt(32)
	v_cvt_f32_ubyte0_e32 v124, v56
	v_cvt_f32_ubyte1_e32 v126, v56
	v_cvt_f32_ubyte2_e32 v128, v56
	v_cvt_f32_ubyte3_e32 v130, v56
	v_cvt_f32_ubyte0_e32 v132, v57
	v_cvt_f32_ubyte1_e32 v134, v57
	v_cvt_f32_ubyte2_e32 v136, v57
	v_cvt_f32_ubyte3_e32 v138, v57
	v_readlane_b32 s30, v121, 16
	s_lshl_b32 s30, s30, 12
	s_add_u32 s28, s26, s30
	s_addc_u32 s29, s27, 0
	global_load_dwordx2 v[56:57], v162, s[28:29]
	s_waitcnt vmcnt(32)
	v_cvt_f32_ubyte0_e32 v125, v58
	v_cvt_f32_ubyte1_e32 v127, v58
	v_cvt_f32_ubyte2_e32 v129, v58
	v_cvt_f32_ubyte3_e32 v131, v58
	v_cvt_f32_ubyte0_e32 v133, v59
	v_cvt_f32_ubyte1_e32 v135, v59
	v_cvt_f32_ubyte2_e32 v137, v59
	v_cvt_f32_ubyte3_e32 v139, v59
	v_readlane_b32 s30, v121, 17
	s_lshl_b32 s30, s30, 12
	s_add_u32 s28, s26, s30
	s_addc_u32 s29, s27, 0
	global_load_dwordx2 v[58:59], v162, s[28:29]
	s_waitcnt vmcnt(32)
	v_cvt_f32_ubyte0_e32 v140, v60
	v_cvt_f32_ubyte1_e32 v142, v60
	v_cvt_f32_ubyte2_e32 v144, v60
	v_cvt_f32_ubyte3_e32 v146, v60
	v_cvt_f32_ubyte0_e32 v148, v61
	v_cvt_f32_ubyte1_e32 v150, v61
	v_cvt_f32_ubyte2_e32 v152, v61
	v_cvt_f32_ubyte3_e32 v154, v61
	v_readlane_b32 s30, v121, 18
	s_lshl_b32 s30, s30, 12
	s_add_u32 s28, s26, s30
	s_addc_u32 s29, s27, 0
	global_load_dwordx2 v[60:61], v162, s[28:29]
	s_waitcnt vmcnt(32)
	v_cvt_f32_ubyte0_e32 v141, v62
	v_cvt_f32_ubyte1_e32 v143, v62
	v_cvt_f32_ubyte2_e32 v145, v62
	v_cvt_f32_ubyte3_e32 v147, v62
	v_cvt_f32_ubyte0_e32 v149, v63
	v_cvt_f32_ubyte1_e32 v151, v63
	v_cvt_f32_ubyte2_e32 v153, v63
	v_cvt_f32_ubyte3_e32 v155, v63
	v_readlane_b32 s30, v121, 19
	s_lshl_b32 s30, s30, 12
	s_add_u32 s28, s26, s30
	s_addc_u32 s29, s27, 0
	global_load_dwordx2 v[62:63], v162, s[28:29]
	v_mul_f32_e32 v194, v124, v108
	v_mul_f32_e32 v195, v125, v108
	v_mul_f32_e32 v196, v140, v108
	v_mul_f32_e32 v197, v141, v108
	v_fmac_f32_e32 v194, v126, v109
	v_fmac_f32_e32 v195, v127, v109
	v_fmac_f32_e32 v196, v142, v109
	v_fmac_f32_e32 v197, v143, v109
	v_fmac_f32_e32 v194, v128, v110
	v_fmac_f32_e32 v195, v129, v110
	v_fmac_f32_e32 v196, v144, v110
	v_fmac_f32_e32 v197, v145, v110
	v_fmac_f32_e32 v194, v130, v111
	v_fmac_f32_e32 v195, v131, v111
	v_fmac_f32_e32 v196, v146, v111
	v_fmac_f32_e32 v197, v147, v111
	v_fmac_f32_e32 v194, v132, v112
	v_fmac_f32_e32 v195, v133, v112
	v_fmac_f32_e32 v196, v148, v112
	v_fmac_f32_e32 v197, v149, v112
	v_fmac_f32_e32 v194, v134, v113
	v_fmac_f32_e32 v195, v135, v113
	v_fmac_f32_e32 v196, v150, v113
	v_fmac_f32_e32 v197, v151, v113
	v_fmac_f32_e32 v194, v136, v114
	v_fmac_f32_e32 v195, v137, v114
	v_fmac_f32_e32 v196, v152, v114
	v_fmac_f32_e32 v197, v153, v114
	v_fmac_f32_e32 v194, v138, v115
	v_fmac_f32_e32 v195, v139, v115
	v_fmac_f32_e32 v196, v154, v115
	v_fmac_f32_e32 v197, v155, v115
	s_waitcnt vmcnt(32)
	v_cvt_f32_ubyte0_e32 v124, v64
	v_cvt_f32_ubyte1_e32 v126, v64
	v_cvt_f32_ubyte2_e32 v128, v64
	v_cvt_f32_ubyte3_e32 v130, v64
	v_cvt_f32_ubyte0_e32 v132, v65
	v_cvt_f32_ubyte1_e32 v134, v65
	v_cvt_f32_ubyte2_e32 v136, v65
	v_cvt_f32_ubyte3_e32 v138, v65
	v_readlane_b32 s30, v121, 20
	s_lshl_b32 s30, s30, 12
	s_add_u32 s28, s26, s30
	s_addc_u32 s29, s27, 0
	global_load_dwordx2 v[64:65], v162, s[28:29]
	s_waitcnt vmcnt(32)
	v_cvt_f32_ubyte0_e32 v125, v66
	v_cvt_f32_ubyte1_e32 v127, v66
	v_cvt_f32_ubyte2_e32 v129, v66
	v_cvt_f32_ubyte3_e32 v131, v66
	v_cvt_f32_ubyte0_e32 v133, v67
	v_cvt_f32_ubyte1_e32 v135, v67
	v_cvt_f32_ubyte2_e32 v137, v67
	v_cvt_f32_ubyte3_e32 v139, v67
	v_readlane_b32 s30, v121, 21
	s_lshl_b32 s30, s30, 12
	s_add_u32 s28, s26, s30
	s_addc_u32 s29, s27, 0
	global_load_dwordx2 v[66:67], v162, s[28:29]
	s_waitcnt vmcnt(32)
	v_cvt_f32_ubyte0_e32 v140, v68
	v_cvt_f32_ubyte1_e32 v142, v68
	v_cvt_f32_ubyte2_e32 v144, v68
	v_cvt_f32_ubyte3_e32 v146, v68
	v_cvt_f32_ubyte0_e32 v148, v69
	v_cvt_f32_ubyte1_e32 v150, v69
	v_cvt_f32_ubyte2_e32 v152, v69
	v_cvt_f32_ubyte3_e32 v154, v69
	v_readlane_b32 s30, v121, 22
	s_lshl_b32 s30, s30, 12
	s_add_u32 s28, s26, s30
	s_addc_u32 s29, s27, 0
	global_load_dwordx2 v[68:69], v162, s[28:29]
	s_waitcnt vmcnt(32)
	v_cvt_f32_ubyte0_e32 v141, v70
	v_cvt_f32_ubyte1_e32 v143, v70
	v_cvt_f32_ubyte2_e32 v145, v70
	v_cvt_f32_ubyte3_e32 v147, v70
	v_cvt_f32_ubyte0_e32 v149, v71
	v_cvt_f32_ubyte1_e32 v151, v71
	v_cvt_f32_ubyte2_e32 v153, v71
	v_cvt_f32_ubyte3_e32 v155, v71
	v_readlane_b32 s30, v121, 23
	s_lshl_b32 s30, s30, 12
	s_add_u32 s28, s26, s30
	s_addc_u32 s29, s27, 0
	global_load_dwordx2 v[70:71], v162, s[28:29]
	v_mul_f32_e32 v198, v124, v108
	v_mul_f32_e32 v199, v125, v108
	v_mul_f32_e32 v200, v140, v108
	v_mul_f32_e32 v201, v141, v108
	v_fmac_f32_e32 v198, v126, v109
	v_fmac_f32_e32 v199, v127, v109
	v_fmac_f32_e32 v200, v142, v109
	v_fmac_f32_e32 v201, v143, v109
	v_fmac_f32_e32 v198, v128, v110
	v_fmac_f32_e32 v199, v129, v110
	v_fmac_f32_e32 v200, v144, v110
	v_fmac_f32_e32 v201, v145, v110
	v_fmac_f32_e32 v198, v130, v111
	v_fmac_f32_e32 v199, v131, v111
	v_fmac_f32_e32 v200, v146, v111
	v_fmac_f32_e32 v201, v147, v111
	v_fmac_f32_e32 v198, v132, v112
	v_fmac_f32_e32 v199, v133, v112
	v_fmac_f32_e32 v200, v148, v112
	v_fmac_f32_e32 v201, v149, v112
	v_fmac_f32_e32 v198, v134, v113
	v_fmac_f32_e32 v199, v135, v113
	v_fmac_f32_e32 v200, v150, v113
	v_fmac_f32_e32 v201, v151, v113
	v_fmac_f32_e32 v198, v136, v114
	v_fmac_f32_e32 v199, v137, v114
	v_fmac_f32_e32 v200, v152, v114
	v_fmac_f32_e32 v201, v153, v114
	v_fmac_f32_e32 v198, v138, v115
	v_fmac_f32_e32 v199, v139, v115
	v_fmac_f32_e32 v200, v154, v115
	v_fmac_f32_e32 v201, v155, v115
	s_waitcnt vmcnt(32)
	v_cvt_f32_ubyte0_e32 v124, v72
	v_cvt_f32_ubyte1_e32 v126, v72
	v_cvt_f32_ubyte2_e32 v128, v72
	v_cvt_f32_ubyte3_e32 v130, v72
	v_cvt_f32_ubyte0_e32 v132, v73
	v_cvt_f32_ubyte1_e32 v134, v73
	v_cvt_f32_ubyte2_e32 v136, v73
	v_cvt_f32_ubyte3_e32 v138, v73
	v_readlane_b32 s30, v121, 24
	s_lshl_b32 s30, s30, 12
	s_add_u32 s28, s26, s30
	s_addc_u32 s29, s27, 0
	global_load_dwordx2 v[72:73], v162, s[28:29]
	s_waitcnt vmcnt(32)
	v_cvt_f32_ubyte0_e32 v125, v74
	v_cvt_f32_ubyte1_e32 v127, v74
	v_cvt_f32_ubyte2_e32 v129, v74
	v_cvt_f32_ubyte3_e32 v131, v74
	v_cvt_f32_ubyte0_e32 v133, v75
	v_cvt_f32_ubyte1_e32 v135, v75
	v_cvt_f32_ubyte2_e32 v137, v75
	v_cvt_f32_ubyte3_e32 v139, v75
	v_readlane_b32 s30, v121, 25
	s_lshl_b32 s30, s30, 12
	s_add_u32 s28, s26, s30
	s_addc_u32 s29, s27, 0
	global_load_dwordx2 v[74:75], v162, s[28:29]
	s_waitcnt vmcnt(32)
	v_cvt_f32_ubyte0_e32 v140, v76
	v_cvt_f32_ubyte1_e32 v142, v76
	v_cvt_f32_ubyte2_e32 v144, v76
	v_cvt_f32_ubyte3_e32 v146, v76
	v_cvt_f32_ubyte0_e32 v148, v77
	v_cvt_f32_ubyte1_e32 v150, v77
	v_cvt_f32_ubyte2_e32 v152, v77
	v_cvt_f32_ubyte3_e32 v154, v77
	v_readlane_b32 s30, v121, 26
	s_lshl_b32 s30, s30, 12
	s_add_u32 s28, s26, s30
	s_addc_u32 s29, s27, 0
	global_load_dwordx2 v[76:77], v162, s[28:29]
	s_waitcnt vmcnt(32)
	v_cvt_f32_ubyte0_e32 v141, v78
	v_cvt_f32_ubyte1_e32 v143, v78
	v_cvt_f32_ubyte2_e32 v145, v78
	v_cvt_f32_ubyte3_e32 v147, v78
	v_cvt_f32_ubyte0_e32 v149, v79
	v_cvt_f32_ubyte1_e32 v151, v79
	v_cvt_f32_ubyte2_e32 v153, v79
	v_cvt_f32_ubyte3_e32 v155, v79
	v_readlane_b32 s30, v121, 27
	s_lshl_b32 s30, s30, 12
	s_add_u32 s28, s26, s30
	s_addc_u32 s29, s27, 0
	global_load_dwordx2 v[78:79], v162, s[28:29]
	v_mul_f32_e32 v202, v124, v108
	v_mul_f32_e32 v203, v125, v108
	v_mul_f32_e32 v204, v140, v108
	v_mul_f32_e32 v205, v141, v108
	v_fmac_f32_e32 v202, v126, v109
	v_fmac_f32_e32 v203, v127, v109
	v_fmac_f32_e32 v204, v142, v109
	v_fmac_f32_e32 v205, v143, v109
	v_fmac_f32_e32 v202, v128, v110
	v_fmac_f32_e32 v203, v129, v110
	v_fmac_f32_e32 v204, v144, v110
	v_fmac_f32_e32 v205, v145, v110
	v_fmac_f32_e32 v202, v130, v111
	v_fmac_f32_e32 v203, v131, v111
	v_fmac_f32_e32 v204, v146, v111
	v_fmac_f32_e32 v205, v147, v111
	v_fmac_f32_e32 v202, v132, v112
	v_fmac_f32_e32 v203, v133, v112
	v_fmac_f32_e32 v204, v148, v112
	v_fmac_f32_e32 v205, v149, v112
	v_fmac_f32_e32 v202, v134, v113
	v_fmac_f32_e32 v203, v135, v113
	v_fmac_f32_e32 v204, v150, v113
	v_fmac_f32_e32 v205, v151, v113
	v_fmac_f32_e32 v202, v136, v114
	v_fmac_f32_e32 v203, v137, v114
	v_fmac_f32_e32 v204, v152, v114
	v_fmac_f32_e32 v205, v153, v114
	v_fmac_f32_e32 v202, v138, v115
	v_fmac_f32_e32 v203, v139, v115
	v_fmac_f32_e32 v204, v154, v115
	v_fmac_f32_e32 v205, v155, v115
	s_waitcnt vmcnt(32)
	v_cvt_f32_ubyte0_e32 v124, v80
	v_cvt_f32_ubyte1_e32 v126, v80
	v_cvt_f32_ubyte2_e32 v128, v80
	v_cvt_f32_ubyte3_e32 v130, v80
	v_cvt_f32_ubyte0_e32 v132, v81
	v_cvt_f32_ubyte1_e32 v134, v81
	v_cvt_f32_ubyte2_e32 v136, v81
	v_cvt_f32_ubyte3_e32 v138, v81
	v_readlane_b32 s30, v121, 28
	s_lshl_b32 s30, s30, 12
	s_add_u32 s28, s26, s30
	s_addc_u32 s29, s27, 0
	global_load_dwordx2 v[80:81], v162, s[28:29]
	s_waitcnt vmcnt(32)
	v_cvt_f32_ubyte0_e32 v125, v82
	v_cvt_f32_ubyte1_e32 v127, v82
	v_cvt_f32_ubyte2_e32 v129, v82
	v_cvt_f32_ubyte3_e32 v131, v82
	v_cvt_f32_ubyte0_e32 v133, v83
	v_cvt_f32_ubyte1_e32 v135, v83
	v_cvt_f32_ubyte2_e32 v137, v83
	v_cvt_f32_ubyte3_e32 v139, v83
	v_readlane_b32 s30, v121, 29
	s_lshl_b32 s30, s30, 12
	s_add_u32 s28, s26, s30
	s_addc_u32 s29, s27, 0
	global_load_dwordx2 v[82:83], v162, s[28:29]
	s_waitcnt vmcnt(32)
	v_cvt_f32_ubyte0_e32 v140, v84
	v_cvt_f32_ubyte1_e32 v142, v84
	v_cvt_f32_ubyte2_e32 v144, v84
	v_cvt_f32_ubyte3_e32 v146, v84
	v_cvt_f32_ubyte0_e32 v148, v85
	v_cvt_f32_ubyte1_e32 v150, v85
	v_cvt_f32_ubyte2_e32 v152, v85
	v_cvt_f32_ubyte3_e32 v154, v85
	v_readlane_b32 s30, v121, 30
	s_lshl_b32 s30, s30, 12
	s_add_u32 s28, s26, s30
	s_addc_u32 s29, s27, 0
	global_load_dwordx2 v[84:85], v162, s[28:29]
	s_waitcnt vmcnt(32)
	v_cvt_f32_ubyte0_e32 v141, v86
	v_cvt_f32_ubyte1_e32 v143, v86
	v_cvt_f32_ubyte2_e32 v145, v86
	v_cvt_f32_ubyte3_e32 v147, v86
	v_cvt_f32_ubyte0_e32 v149, v87
	v_cvt_f32_ubyte1_e32 v151, v87
	v_cvt_f32_ubyte2_e32 v153, v87
	v_cvt_f32_ubyte3_e32 v155, v87
	v_readlane_b32 s30, v121, 31
	s_lshl_b32 s30, s30, 12
	s_add_u32 s28, s26, s30
	s_addc_u32 s29, s27, 0
	global_load_dwordx2 v[86:87], v162, s[28:29]
	v_mul_f32_e32 v206, v124, v108
	v_mul_f32_e32 v207, v125, v108
	v_mul_f32_e32 v208, v140, v108
	v_mul_f32_e32 v209, v141, v108
	v_fmac_f32_e32 v206, v126, v109
	v_fmac_f32_e32 v207, v127, v109
	v_fmac_f32_e32 v208, v142, v109
	v_fmac_f32_e32 v209, v143, v109
	v_fmac_f32_e32 v206, v128, v110
	v_fmac_f32_e32 v207, v129, v110
	v_fmac_f32_e32 v208, v144, v110
	v_fmac_f32_e32 v209, v145, v110
	v_fmac_f32_e32 v206, v130, v111
	v_fmac_f32_e32 v207, v131, v111
	v_fmac_f32_e32 v208, v146, v111
	v_fmac_f32_e32 v209, v147, v111
	v_fmac_f32_e32 v206, v132, v112
	v_fmac_f32_e32 v207, v133, v112
	v_fmac_f32_e32 v208, v148, v112
	v_fmac_f32_e32 v209, v149, v112
	v_fmac_f32_e32 v206, v134, v113
	v_fmac_f32_e32 v207, v135, v113
	v_fmac_f32_e32 v208, v150, v113
	v_fmac_f32_e32 v209, v151, v113
	v_fmac_f32_e32 v206, v136, v114
	v_fmac_f32_e32 v207, v137, v114
	v_fmac_f32_e32 v208, v152, v114
	v_fmac_f32_e32 v209, v153, v114
	v_fmac_f32_e32 v206, v138, v115
	v_fmac_f32_e32 v207, v139, v115
	v_fmac_f32_e32 v208, v154, v115
	v_fmac_f32_e32 v209, v155, v115
	v_permlane32_swap_b32_e32 v178, v194
	v_permlane32_swap_b32_e32 v179, v195
	v_permlane32_swap_b32_e32 v180, v196
	v_permlane32_swap_b32_e32 v181, v197
	v_permlane32_swap_b32_e32 v182, v198
	v_permlane32_swap_b32_e32 v183, v199
	v_permlane32_swap_b32_e32 v184, v200
	v_permlane32_swap_b32_e32 v185, v201
	v_permlane32_swap_b32_e32 v186, v202
	v_permlane32_swap_b32_e32 v187, v203
	v_permlane32_swap_b32_e32 v188, v204
	v_permlane32_swap_b32_e32 v189, v205
	v_permlane32_swap_b32_e32 v190, v206
	v_permlane32_swap_b32_e32 v191, v207
	v_permlane32_swap_b32_e32 v192, v208
	v_permlane32_swap_b32_e32 v193, v209
	v_add_f32_e32 v178, v178, v194
	v_add_f32_e32 v179, v179, v195
	v_add_f32_e32 v180, v180, v196
	v_add_f32_e32 v181, v181, v197
	v_add_f32_e32 v182, v182, v198
	v_add_f32_e32 v183, v183, v199
	v_add_f32_e32 v184, v184, v200
	v_add_f32_e32 v185, v185, v201
	v_add_f32_e32 v186, v186, v202
	v_add_f32_e32 v187, v187, v203
	v_add_f32_e32 v188, v188, v204
	v_add_f32_e32 v189, v189, v205
	v_add_f32_e32 v190, v190, v206
	v_add_f32_e32 v191, v191, v207
	v_add_f32_e32 v192, v192, v208
	v_add_f32_e32 v193, v193, v209
	v_permlane16_swap_b32_e32 v178, v186
	v_permlane16_swap_b32_e32 v179, v187
	v_permlane16_swap_b32_e32 v180, v188
	v_permlane16_swap_b32_e32 v181, v189
	v_permlane16_swap_b32_e32 v182, v190
	v_permlane16_swap_b32_e32 v183, v191
	v_permlane16_swap_b32_e32 v184, v192
	v_permlane16_swap_b32_e32 v185, v193
	v_add_f32_e32 v178, v178, v186
	v_add_f32_e32 v179, v179, v187
	v_add_f32_e32 v180, v180, v188
	v_add_f32_e32 v181, v181, v189
	v_add_f32_e32 v182, v182, v190
	v_add_f32_e32 v183, v183, v191
	v_add_f32_e32 v184, v184, v192
	v_add_f32_e32 v185, v185, v193
	v_cndmask_b32_e64 v2, v178, v182, s[8:9]
	v_cndmask_b32_e64 v3, v179, v183, s[8:9]
	v_cndmask_b32_e64 v4, v180, v184, s[8:9]
	v_cndmask_b32_e64 v5, v181, v185, s[8:9]
	v_cndmask_b32_e64 v6, v182, v178, s[8:9]
	v_cndmask_b32_e64 v7, v183, v179, s[8:9]
	v_cndmask_b32_e64 v8, v184, v180, s[8:9]
	v_cndmask_b32_e64 v9, v185, v181, s[8:9]
	v_add_f32_dpp v6, v2, v6 row_ror:8 row_mask:0xf bank_mask:0xf
	v_add_f32_dpp v7, v3, v7 row_ror:8 row_mask:0xf bank_mask:0xf
	v_add_f32_dpp v8, v4, v8 row_ror:8 row_mask:0xf bank_mask:0xf
	v_add_f32_dpp v9, v5, v9 row_ror:8 row_mask:0xf bank_mask:0xf
	v_cndmask_b32_e64 v2, v6, v8, s[10:11]
	v_cndmask_b32_e64 v3, v7, v9, s[10:11]
	v_cndmask_b32_e64 v4, v8, v6, s[10:11]
	v_cndmask_b32_e64 v5, v9, v7, s[10:11]
	v_add_f32_dpp v4, v2, v4 row_half_mirror row_mask:0xf bank_mask:0xf
	v_add_f32_dpp v5, v3, v5 row_half_mirror row_mask:0xf bank_mask:0xf
	v_cndmask_b32_e64 v2, v4, v5, s[14:15]
	v_cndmask_b32_e64 v3, v5, v4, s[14:15]
	s_nop 0
	v_add_f32_dpp v3, v2, v3 quad_perm:[2,3,0,1] row_mask:0xf bank_mask:0xf
	s_nop 1
	v_add_f32_dpp v11, v3, v3 quad_perm:[1,0,3,2] row_mask:0xf bank_mask:0xf
	s_mov_b64 exec, s[2:3]
	global_store_dword v[22:23], v11, off offset:128
	s_mov_b64 exec, -1
	s_waitcnt vmcnt(32)
	v_cvt_f32_ubyte0_e32 v124, v24
	v_cvt_f32_ubyte1_e32 v126, v24
	v_cvt_f32_ubyte2_e32 v128, v24
	v_cvt_f32_ubyte3_e32 v130, v24
	v_cvt_f32_ubyte0_e32 v132, v25
	v_cvt_f32_ubyte1_e32 v134, v25
	v_cvt_f32_ubyte2_e32 v136, v25
	v_cvt_f32_ubyte3_e32 v138, v25
	v_readlane_b32 s30, v121, 32
	s_lshl_b32 s30, s30, 12
	s_add_u32 s28, s26, s30
	s_addc_u32 s29, s27, 0
	global_load_dwordx2 v[24:25], v162, s[28:29]
	s_waitcnt vmcnt(32)
	v_cvt_f32_ubyte0_e32 v125, v26
	v_cvt_f32_ubyte1_e32 v127, v26
	v_cvt_f32_ubyte2_e32 v129, v26
	v_cvt_f32_ubyte3_e32 v131, v26
	v_cvt_f32_ubyte0_e32 v133, v27
	v_cvt_f32_ubyte1_e32 v135, v27
	v_cvt_f32_ubyte2_e32 v137, v27
	v_cvt_f32_ubyte3_e32 v139, v27
	v_readlane_b32 s30, v121, 33
	s_lshl_b32 s30, s30, 12
	s_add_u32 s28, s26, s30
	s_addc_u32 s29, s27, 0
	global_load_dwordx2 v[26:27], v162, s[28:29]
	s_waitcnt vmcnt(32)
	v_cvt_f32_ubyte0_e32 v140, v28
	v_cvt_f32_ubyte1_e32 v142, v28
	v_cvt_f32_ubyte2_e32 v144, v28
	v_cvt_f32_ubyte3_e32 v146, v28
	v_cvt_f32_ubyte0_e32 v148, v29
	v_cvt_f32_ubyte1_e32 v150, v29
	v_cvt_f32_ubyte2_e32 v152, v29
	v_cvt_f32_ubyte3_e32 v154, v29
	v_readlane_b32 s30, v121, 34
	s_lshl_b32 s30, s30, 12
	s_add_u32 s28, s26, s30
	s_addc_u32 s29, s27, 0
	global_load_dwordx2 v[28:29], v162, s[28:29]
	s_waitcnt vmcnt(32)
	v_cvt_f32_ubyte0_e32 v141, v30
	v_cvt_f32_ubyte1_e32 v143, v30
	v_cvt_f32_ubyte2_e32 v145, v30
	v_cvt_f32_ubyte3_e32 v147, v30
	v_cvt_f32_ubyte0_e32 v149, v31
	v_cvt_f32_ubyte1_e32 v151, v31
	v_cvt_f32_ubyte2_e32 v153, v31
	v_cvt_f32_ubyte3_e32 v155, v31
	v_readlane_b32 s30, v121, 35
	s_lshl_b32 s30, s30, 12
	s_add_u32 s28, s26, s30
	s_addc_u32 s29, s27, 0
	global_load_dwordx2 v[30:31], v162, s[28:29]
	v_mul_f32_e32 v178, v124, v108
	v_mul_f32_e32 v179, v125, v108
	v_mul_f32_e32 v180, v140, v108
	v_mul_f32_e32 v181, v141, v108
	v_fmac_f32_e32 v178, v126, v109
	v_fmac_f32_e32 v179, v127, v109
	v_fmac_f32_e32 v180, v142, v109
	v_fmac_f32_e32 v181, v143, v109
	v_fmac_f32_e32 v178, v128, v110
	v_fmac_f32_e32 v179, v129, v110
	v_fmac_f32_e32 v180, v144, v110
	v_fmac_f32_e32 v181, v145, v110
	v_fmac_f32_e32 v178, v130, v111
	v_fmac_f32_e32 v179, v131, v111
	v_fmac_f32_e32 v180, v146, v111
	v_fmac_f32_e32 v181, v147, v111
	v_fmac_f32_e32 v178, v132, v112
	v_fmac_f32_e32 v179, v133, v112
	v_fmac_f32_e32 v180, v148, v112
	v_fmac_f32_e32 v181, v149, v112
	v_fmac_f32_e32 v178, v134, v113
	v_fmac_f32_e32 v179, v135, v113
	v_fmac_f32_e32 v180, v150, v113
	v_fmac_f32_e32 v181, v151, v113
	v_fmac_f32_e32 v178, v136, v114
	v_fmac_f32_e32 v179, v137, v114
	v_fmac_f32_e32 v180, v152, v114
	v_fmac_f32_e32 v181, v153, v114
	v_fmac_f32_e32 v178, v138, v115
	v_fmac_f32_e32 v179, v139, v115
	v_fmac_f32_e32 v180, v154, v115
	v_fmac_f32_e32 v181, v155, v115
	s_waitcnt vmcnt(32)
	v_cvt_f32_ubyte0_e32 v124, v32
	v_cvt_f32_ubyte1_e32 v126, v32
	v_cvt_f32_ubyte2_e32 v128, v32
	v_cvt_f32_ubyte3_e32 v130, v32
	v_cvt_f32_ubyte0_e32 v132, v33
	v_cvt_f32_ubyte1_e32 v134, v33
	v_cvt_f32_ubyte2_e32 v136, v33
	v_cvt_f32_ubyte3_e32 v138, v33
	v_readlane_b32 s30, v121, 36
	s_lshl_b32 s30, s30, 12
	s_add_u32 s28, s26, s30
	s_addc_u32 s29, s27, 0
	global_load_dwordx2 v[32:33], v162, s[28:29]
	s_waitcnt vmcnt(32)
	v_cvt_f32_ubyte0_e32 v125, v34
	v_cvt_f32_ubyte1_e32 v127, v34
	v_cvt_f32_ubyte2_e32 v129, v34
	v_cvt_f32_ubyte3_e32 v131, v34
	v_cvt_f32_ubyte0_e32 v133, v35
	v_cvt_f32_ubyte1_e32 v135, v35
	v_cvt_f32_ubyte2_e32 v137, v35
	v_cvt_f32_ubyte3_e32 v139, v35
	v_readlane_b32 s30, v121, 37
	s_lshl_b32 s30, s30, 12
	s_add_u32 s28, s26, s30
	s_addc_u32 s29, s27, 0
	global_load_dwordx2 v[34:35], v162, s[28:29]
	s_waitcnt vmcnt(32)
	v_cvt_f32_ubyte0_e32 v140, v36
	v_cvt_f32_ubyte1_e32 v142, v36
	v_cvt_f32_ubyte2_e32 v144, v36
	v_cvt_f32_ubyte3_e32 v146, v36
	v_cvt_f32_ubyte0_e32 v148, v37
	v_cvt_f32_ubyte1_e32 v150, v37
	v_cvt_f32_ubyte2_e32 v152, v37
	v_cvt_f32_ubyte3_e32 v154, v37
	v_readlane_b32 s30, v121, 38
	s_lshl_b32 s30, s30, 12
	s_add_u32 s28, s26, s30
	s_addc_u32 s29, s27, 0
	global_load_dwordx2 v[36:37], v162, s[28:29]
	s_waitcnt vmcnt(32)
	v_cvt_f32_ubyte0_e32 v141, v38
	v_cvt_f32_ubyte1_e32 v143, v38
	v_cvt_f32_ubyte2_e32 v145, v38
	v_cvt_f32_ubyte3_e32 v147, v38
	v_cvt_f32_ubyte0_e32 v149, v39
	v_cvt_f32_ubyte1_e32 v151, v39
	v_cvt_f32_ubyte2_e32 v153, v39
	v_cvt_f32_ubyte3_e32 v155, v39
	v_readlane_b32 s30, v121, 39
	s_lshl_b32 s30, s30, 12
	s_add_u32 s28, s26, s30
	s_addc_u32 s29, s27, 0
	global_load_dwordx2 v[38:39], v162, s[28:29]
	v_mul_f32_e32 v182, v124, v108
	v_mul_f32_e32 v183, v125, v108
	v_mul_f32_e32 v184, v140, v108
	v_mul_f32_e32 v185, v141, v108
	v_fmac_f32_e32 v182, v126, v109
	v_fmac_f32_e32 v183, v127, v109
	v_fmac_f32_e32 v184, v142, v109
	v_fmac_f32_e32 v185, v143, v109
	v_fmac_f32_e32 v182, v128, v110
	v_fmac_f32_e32 v183, v129, v110
	v_fmac_f32_e32 v184, v144, v110
	v_fmac_f32_e32 v185, v145, v110
	v_fmac_f32_e32 v182, v130, v111
	v_fmac_f32_e32 v183, v131, v111
	v_fmac_f32_e32 v184, v146, v111
	v_fmac_f32_e32 v185, v147, v111
	v_fmac_f32_e32 v182, v132, v112
	v_fmac_f32_e32 v183, v133, v112
	v_fmac_f32_e32 v184, v148, v112
	v_fmac_f32_e32 v185, v149, v112
	v_fmac_f32_e32 v182, v134, v113
	v_fmac_f32_e32 v183, v135, v113
	v_fmac_f32_e32 v184, v150, v113
	v_fmac_f32_e32 v185, v151, v113
	v_fmac_f32_e32 v182, v136, v114
	v_fmac_f32_e32 v183, v137, v114
	v_fmac_f32_e32 v184, v152, v114
	v_fmac_f32_e32 v185, v153, v114
	v_fmac_f32_e32 v182, v138, v115
	v_fmac_f32_e32 v183, v139, v115
	v_fmac_f32_e32 v184, v154, v115
	v_fmac_f32_e32 v185, v155, v115
	s_waitcnt vmcnt(32)
	v_cvt_f32_ubyte0_e32 v124, v40
	v_cvt_f32_ubyte1_e32 v126, v40
	v_cvt_f32_ubyte2_e32 v128, v40
	v_cvt_f32_ubyte3_e32 v130, v40
	v_cvt_f32_ubyte0_e32 v132, v41
	v_cvt_f32_ubyte1_e32 v134, v41
	v_cvt_f32_ubyte2_e32 v136, v41
	v_cvt_f32_ubyte3_e32 v138, v41
	v_readlane_b32 s30, v121, 40
	s_lshl_b32 s30, s30, 12
	s_add_u32 s28, s26, s30
	s_addc_u32 s29, s27, 0
	global_load_dwordx2 v[40:41], v162, s[28:29]
	s_waitcnt vmcnt(32)
	v_cvt_f32_ubyte0_e32 v125, v42
	v_cvt_f32_ubyte1_e32 v127, v42
	v_cvt_f32_ubyte2_e32 v129, v42
	v_cvt_f32_ubyte3_e32 v131, v42
	v_cvt_f32_ubyte0_e32 v133, v43
	v_cvt_f32_ubyte1_e32 v135, v43
	v_cvt_f32_ubyte2_e32 v137, v43
	v_cvt_f32_ubyte3_e32 v139, v43
	v_readlane_b32 s30, v121, 41
	s_lshl_b32 s30, s30, 12
	s_add_u32 s28, s26, s30
	s_addc_u32 s29, s27, 0
	global_load_dwordx2 v[42:43], v162, s[28:29]
	s_waitcnt vmcnt(32)
	v_cvt_f32_ubyte0_e32 v140, v44
	v_cvt_f32_ubyte1_e32 v142, v44
	v_cvt_f32_ubyte2_e32 v144, v44
	v_cvt_f32_ubyte3_e32 v146, v44
	v_cvt_f32_ubyte0_e32 v148, v45
	v_cvt_f32_ubyte1_e32 v150, v45
	v_cvt_f32_ubyte2_e32 v152, v45
	v_cvt_f32_ubyte3_e32 v154, v45
	v_readlane_b32 s30, v121, 42
	s_lshl_b32 s30, s30, 12
	s_add_u32 s28, s26, s30
	s_addc_u32 s29, s27, 0
	global_load_dwordx2 v[44:45], v162, s[28:29]
	s_waitcnt vmcnt(32)
	v_cvt_f32_ubyte0_e32 v141, v46
	v_cvt_f32_ubyte1_e32 v143, v46
	v_cvt_f32_ubyte2_e32 v145, v46
	v_cvt_f32_ubyte3_e32 v147, v46
	v_cvt_f32_ubyte0_e32 v149, v47
	v_cvt_f32_ubyte1_e32 v151, v47
	v_cvt_f32_ubyte2_e32 v153, v47
	v_cvt_f32_ubyte3_e32 v155, v47
	v_readlane_b32 s30, v121, 43
	s_lshl_b32 s30, s30, 12
	s_add_u32 s28, s26, s30
	s_addc_u32 s29, s27, 0
	global_load_dwordx2 v[46:47], v162, s[28:29]
	v_mul_f32_e32 v186, v124, v108
	v_mul_f32_e32 v187, v125, v108
	v_mul_f32_e32 v188, v140, v108
	v_mul_f32_e32 v189, v141, v108
	v_fmac_f32_e32 v186, v126, v109
	v_fmac_f32_e32 v187, v127, v109
	v_fmac_f32_e32 v188, v142, v109
	v_fmac_f32_e32 v189, v143, v109
	v_fmac_f32_e32 v186, v128, v110
	v_fmac_f32_e32 v187, v129, v110
	v_fmac_f32_e32 v188, v144, v110
	v_fmac_f32_e32 v189, v145, v110
	v_fmac_f32_e32 v186, v130, v111
	v_fmac_f32_e32 v187, v131, v111
	v_fmac_f32_e32 v188, v146, v111
	v_fmac_f32_e32 v189, v147, v111
	v_fmac_f32_e32 v186, v132, v112
	v_fmac_f32_e32 v187, v133, v112
	v_fmac_f32_e32 v188, v148, v112
	v_fmac_f32_e32 v189, v149, v112
	v_fmac_f32_e32 v186, v134, v113
	v_fmac_f32_e32 v187, v135, v113
	v_fmac_f32_e32 v188, v150, v113
	v_fmac_f32_e32 v189, v151, v113
	v_fmac_f32_e32 v186, v136, v114
	v_fmac_f32_e32 v187, v137, v114
	v_fmac_f32_e32 v188, v152, v114
	v_fmac_f32_e32 v189, v153, v114
	v_fmac_f32_e32 v186, v138, v115
	v_fmac_f32_e32 v187, v139, v115
	v_fmac_f32_e32 v188, v154, v115
	v_fmac_f32_e32 v189, v155, v115
	s_waitcnt vmcnt(32)
	v_cvt_f32_ubyte0_e32 v124, v48
	v_cvt_f32_ubyte1_e32 v126, v48
	v_cvt_f32_ubyte2_e32 v128, v48
	v_cvt_f32_ubyte3_e32 v130, v48
	v_cvt_f32_ubyte0_e32 v132, v49
	v_cvt_f32_ubyte1_e32 v134, v49
	v_cvt_f32_ubyte2_e32 v136, v49
	v_cvt_f32_ubyte3_e32 v138, v49
	v_readlane_b32 s30, v121, 44
	s_lshl_b32 s30, s30, 12
	s_add_u32 s28, s26, s30
	s_addc_u32 s29, s27, 0
	global_load_dwordx2 v[48:49], v162, s[28:29]
	s_waitcnt vmcnt(32)
	v_cvt_f32_ubyte0_e32 v125, v50
	v_cvt_f32_ubyte1_e32 v127, v50
	v_cvt_f32_ubyte2_e32 v129, v50
	v_cvt_f32_ubyte3_e32 v131, v50
	v_cvt_f32_ubyte0_e32 v133, v51
	v_cvt_f32_ubyte1_e32 v135, v51
	v_cvt_f32_ubyte2_e32 v137, v51
	v_cvt_f32_ubyte3_e32 v139, v51
	v_readlane_b32 s30, v121, 45
	s_lshl_b32 s30, s30, 12
	s_add_u32 s28, s26, s30
	s_addc_u32 s29, s27, 0
	global_load_dwordx2 v[50:51], v162, s[28:29]
	s_waitcnt vmcnt(32)
	v_cvt_f32_ubyte0_e32 v140, v52
	v_cvt_f32_ubyte1_e32 v142, v52
	v_cvt_f32_ubyte2_e32 v144, v52
	v_cvt_f32_ubyte3_e32 v146, v52
	v_cvt_f32_ubyte0_e32 v148, v53
	v_cvt_f32_ubyte1_e32 v150, v53
	v_cvt_f32_ubyte2_e32 v152, v53
	v_cvt_f32_ubyte3_e32 v154, v53
	v_readlane_b32 s30, v121, 46
	s_lshl_b32 s30, s30, 12
	s_add_u32 s28, s26, s30
	s_addc_u32 s29, s27, 0
	global_load_dwordx2 v[52:53], v162, s[28:29]
	s_waitcnt vmcnt(32)
	v_cvt_f32_ubyte0_e32 v141, v54
	v_cvt_f32_ubyte1_e32 v143, v54
	v_cvt_f32_ubyte2_e32 v145, v54
	v_cvt_f32_ubyte3_e32 v147, v54
	v_cvt_f32_ubyte0_e32 v149, v55
	v_cvt_f32_ubyte1_e32 v151, v55
	v_cvt_f32_ubyte2_e32 v153, v55
	v_cvt_f32_ubyte3_e32 v155, v55
	v_readlane_b32 s30, v121, 47
	s_lshl_b32 s30, s30, 12
	s_add_u32 s28, s26, s30
	s_addc_u32 s29, s27, 0
	global_load_dwordx2 v[54:55], v162, s[28:29]
	v_mul_f32_e32 v190, v124, v108
	v_mul_f32_e32 v191, v125, v108
	v_mul_f32_e32 v192, v140, v108
	v_mul_f32_e32 v193, v141, v108
	v_fmac_f32_e32 v190, v126, v109
	v_fmac_f32_e32 v191, v127, v109
	v_fmac_f32_e32 v192, v142, v109
	v_fmac_f32_e32 v193, v143, v109
	v_fmac_f32_e32 v190, v128, v110
	v_fmac_f32_e32 v191, v129, v110
	v_fmac_f32_e32 v192, v144, v110
	v_fmac_f32_e32 v193, v145, v110
	v_fmac_f32_e32 v190, v130, v111
	v_fmac_f32_e32 v191, v131, v111
	v_fmac_f32_e32 v192, v146, v111
	v_fmac_f32_e32 v193, v147, v111
	v_fmac_f32_e32 v190, v132, v112
	v_fmac_f32_e32 v191, v133, v112
	v_fmac_f32_e32 v192, v148, v112
	v_fmac_f32_e32 v193, v149, v112
	v_fmac_f32_e32 v190, v134, v113
	v_fmac_f32_e32 v191, v135, v113
	v_fmac_f32_e32 v192, v150, v113
	v_fmac_f32_e32 v193, v151, v113
	v_fmac_f32_e32 v190, v136, v114
	v_fmac_f32_e32 v191, v137, v114
	v_fmac_f32_e32 v192, v152, v114
	v_fmac_f32_e32 v193, v153, v114
	v_fmac_f32_e32 v190, v138, v115
	v_fmac_f32_e32 v191, v139, v115
	v_fmac_f32_e32 v192, v154, v115
	v_fmac_f32_e32 v193, v155, v115
	s_waitcnt vmcnt(32)
	v_cvt_f32_ubyte0_e32 v124, v56
	v_cvt_f32_ubyte1_e32 v126, v56
	v_cvt_f32_ubyte2_e32 v128, v56
	v_cvt_f32_ubyte3_e32 v130, v56
	v_cvt_f32_ubyte0_e32 v132, v57
	v_cvt_f32_ubyte1_e32 v134, v57
	v_cvt_f32_ubyte2_e32 v136, v57
	v_cvt_f32_ubyte3_e32 v138, v57
	v_readlane_b32 s30, v121, 48
	s_lshl_b32 s30, s30, 12
	s_add_u32 s28, s26, s30
	s_addc_u32 s29, s27, 0
	global_load_dwordx2 v[56:57], v162, s[28:29]
	s_waitcnt vmcnt(32)
	v_cvt_f32_ubyte0_e32 v125, v58
	v_cvt_f32_ubyte1_e32 v127, v58
	v_cvt_f32_ubyte2_e32 v129, v58
	v_cvt_f32_ubyte3_e32 v131, v58
	v_cvt_f32_ubyte0_e32 v133, v59
	v_cvt_f32_ubyte1_e32 v135, v59
	v_cvt_f32_ubyte2_e32 v137, v59
	v_cvt_f32_ubyte3_e32 v139, v59
	v_readlane_b32 s30, v121, 49
	s_lshl_b32 s30, s30, 12
	s_add_u32 s28, s26, s30
	s_addc_u32 s29, s27, 0
	global_load_dwordx2 v[58:59], v162, s[28:29]
	s_waitcnt vmcnt(32)
	v_cvt_f32_ubyte0_e32 v140, v60
	v_cvt_f32_ubyte1_e32 v142, v60
	v_cvt_f32_ubyte2_e32 v144, v60
	v_cvt_f32_ubyte3_e32 v146, v60
	v_cvt_f32_ubyte0_e32 v148, v61
	v_cvt_f32_ubyte1_e32 v150, v61
	v_cvt_f32_ubyte2_e32 v152, v61
	v_cvt_f32_ubyte3_e32 v154, v61
	v_readlane_b32 s30, v121, 50
	s_lshl_b32 s30, s30, 12
	s_add_u32 s28, s26, s30
	s_addc_u32 s29, s27, 0
	global_load_dwordx2 v[60:61], v162, s[28:29]
	s_waitcnt vmcnt(32)
	v_cvt_f32_ubyte0_e32 v141, v62
	v_cvt_f32_ubyte1_e32 v143, v62
	v_cvt_f32_ubyte2_e32 v145, v62
	v_cvt_f32_ubyte3_e32 v147, v62
	v_cvt_f32_ubyte0_e32 v149, v63
	v_cvt_f32_ubyte1_e32 v151, v63
	v_cvt_f32_ubyte2_e32 v153, v63
	v_cvt_f32_ubyte3_e32 v155, v63
	v_readlane_b32 s30, v121, 51
	s_lshl_b32 s30, s30, 12
	s_add_u32 s28, s26, s30
	s_addc_u32 s29, s27, 0
	global_load_dwordx2 v[62:63], v162, s[28:29]
	v_mul_f32_e32 v194, v124, v108
	v_mul_f32_e32 v195, v125, v108
	v_mul_f32_e32 v196, v140, v108
	v_mul_f32_e32 v197, v141, v108
	v_fmac_f32_e32 v194, v126, v109
	v_fmac_f32_e32 v195, v127, v109
	v_fmac_f32_e32 v196, v142, v109
	v_fmac_f32_e32 v197, v143, v109
	v_fmac_f32_e32 v194, v128, v110
	v_fmac_f32_e32 v195, v129, v110
	v_fmac_f32_e32 v196, v144, v110
	v_fmac_f32_e32 v197, v145, v110
	v_fmac_f32_e32 v194, v130, v111
	v_fmac_f32_e32 v195, v131, v111
	v_fmac_f32_e32 v196, v146, v111
	v_fmac_f32_e32 v197, v147, v111
	v_fmac_f32_e32 v194, v132, v112
	v_fmac_f32_e32 v195, v133, v112
	v_fmac_f32_e32 v196, v148, v112
	v_fmac_f32_e32 v197, v149, v112
	v_fmac_f32_e32 v194, v134, v113
	v_fmac_f32_e32 v195, v135, v113
	v_fmac_f32_e32 v196, v150, v113
	v_fmac_f32_e32 v197, v151, v113
	v_fmac_f32_e32 v194, v136, v114
	v_fmac_f32_e32 v195, v137, v114
	v_fmac_f32_e32 v196, v152, v114
	v_fmac_f32_e32 v197, v153, v114
	v_fmac_f32_e32 v194, v138, v115
	v_fmac_f32_e32 v195, v139, v115
	v_fmac_f32_e32 v196, v154, v115
	v_fmac_f32_e32 v197, v155, v115
	s_waitcnt vmcnt(32)
	v_cvt_f32_ubyte0_e32 v124, v64
	v_cvt_f32_ubyte1_e32 v126, v64
	v_cvt_f32_ubyte2_e32 v128, v64
	v_cvt_f32_ubyte3_e32 v130, v64
	v_cvt_f32_ubyte0_e32 v132, v65
	v_cvt_f32_ubyte1_e32 v134, v65
	v_cvt_f32_ubyte2_e32 v136, v65
	v_cvt_f32_ubyte3_e32 v138, v65
	v_readlane_b32 s30, v121, 52
	s_lshl_b32 s30, s30, 12
	s_add_u32 s28, s26, s30
	s_addc_u32 s29, s27, 0
	global_load_dwordx2 v[64:65], v162, s[28:29]
	s_waitcnt vmcnt(32)
	v_cvt_f32_ubyte0_e32 v125, v66
	v_cvt_f32_ubyte1_e32 v127, v66
	v_cvt_f32_ubyte2_e32 v129, v66
	v_cvt_f32_ubyte3_e32 v131, v66
	v_cvt_f32_ubyte0_e32 v133, v67
	v_cvt_f32_ubyte1_e32 v135, v67
	v_cvt_f32_ubyte2_e32 v137, v67
	v_cvt_f32_ubyte3_e32 v139, v67
	v_readlane_b32 s30, v121, 53
	s_lshl_b32 s30, s30, 12
	s_add_u32 s28, s26, s30
	s_addc_u32 s29, s27, 0
	global_load_dwordx2 v[66:67], v162, s[28:29]
	s_waitcnt vmcnt(32)
	v_cvt_f32_ubyte0_e32 v140, v68
	v_cvt_f32_ubyte1_e32 v142, v68
	v_cvt_f32_ubyte2_e32 v144, v68
	v_cvt_f32_ubyte3_e32 v146, v68
	v_cvt_f32_ubyte0_e32 v148, v69
	v_cvt_f32_ubyte1_e32 v150, v69
	v_cvt_f32_ubyte2_e32 v152, v69
	v_cvt_f32_ubyte3_e32 v154, v69
	v_readlane_b32 s30, v121, 54
	s_lshl_b32 s30, s30, 12
	s_add_u32 s28, s26, s30
	s_addc_u32 s29, s27, 0
	global_load_dwordx2 v[68:69], v162, s[28:29]
	s_waitcnt vmcnt(32)
	v_cvt_f32_ubyte0_e32 v141, v70
	v_cvt_f32_ubyte1_e32 v143, v70
	v_cvt_f32_ubyte2_e32 v145, v70
	v_cvt_f32_ubyte3_e32 v147, v70
	v_cvt_f32_ubyte0_e32 v149, v71
	v_cvt_f32_ubyte1_e32 v151, v71
	v_cvt_f32_ubyte2_e32 v153, v71
	v_cvt_f32_ubyte3_e32 v155, v71
	v_readlane_b32 s30, v121, 55
	s_lshl_b32 s30, s30, 12
	s_add_u32 s28, s26, s30
	s_addc_u32 s29, s27, 0
	global_load_dwordx2 v[70:71], v162, s[28:29]
	v_mul_f32_e32 v198, v124, v108
	v_mul_f32_e32 v199, v125, v108
	v_mul_f32_e32 v200, v140, v108
	v_mul_f32_e32 v201, v141, v108
	v_fmac_f32_e32 v198, v126, v109
	v_fmac_f32_e32 v199, v127, v109
	v_fmac_f32_e32 v200, v142, v109
	v_fmac_f32_e32 v201, v143, v109
	v_fmac_f32_e32 v198, v128, v110
	v_fmac_f32_e32 v199, v129, v110
	v_fmac_f32_e32 v200, v144, v110
	v_fmac_f32_e32 v201, v145, v110
	v_fmac_f32_e32 v198, v130, v111
	v_fmac_f32_e32 v199, v131, v111
	v_fmac_f32_e32 v200, v146, v111
	v_fmac_f32_e32 v201, v147, v111
	v_fmac_f32_e32 v198, v132, v112
	v_fmac_f32_e32 v199, v133, v112
	v_fmac_f32_e32 v200, v148, v112
	v_fmac_f32_e32 v201, v149, v112
	v_fmac_f32_e32 v198, v134, v113
	v_fmac_f32_e32 v199, v135, v113
	v_fmac_f32_e32 v200, v150, v113
	v_fmac_f32_e32 v201, v151, v113
	v_fmac_f32_e32 v198, v136, v114
	v_fmac_f32_e32 v199, v137, v114
	v_fmac_f32_e32 v200, v152, v114
	v_fmac_f32_e32 v201, v153, v114
	v_fmac_f32_e32 v198, v138, v115
	v_fmac_f32_e32 v199, v139, v115
	v_fmac_f32_e32 v200, v154, v115
	v_fmac_f32_e32 v201, v155, v115
	s_waitcnt vmcnt(32)
	v_cvt_f32_ubyte0_e32 v124, v72
	v_cvt_f32_ubyte1_e32 v126, v72
	v_cvt_f32_ubyte2_e32 v128, v72
	v_cvt_f32_ubyte3_e32 v130, v72
	v_cvt_f32_ubyte0_e32 v132, v73
	v_cvt_f32_ubyte1_e32 v134, v73
	v_cvt_f32_ubyte2_e32 v136, v73
	v_cvt_f32_ubyte3_e32 v138, v73
	v_readlane_b32 s30, v121, 56
	s_lshl_b32 s30, s30, 12
	s_add_u32 s28, s26, s30
	s_addc_u32 s29, s27, 0
	global_load_dwordx2 v[72:73], v162, s[28:29]
	s_waitcnt vmcnt(32)
	v_cvt_f32_ubyte0_e32 v125, v74
	v_cvt_f32_ubyte1_e32 v127, v74
	v_cvt_f32_ubyte2_e32 v129, v74
	v_cvt_f32_ubyte3_e32 v131, v74
	v_cvt_f32_ubyte0_e32 v133, v75
	v_cvt_f32_ubyte1_e32 v135, v75
	v_cvt_f32_ubyte2_e32 v137, v75
	v_cvt_f32_ubyte3_e32 v139, v75
	v_readlane_b32 s30, v121, 57
	s_lshl_b32 s30, s30, 12
	s_add_u32 s28, s26, s30
	s_addc_u32 s29, s27, 0
	global_load_dwordx2 v[74:75], v162, s[28:29]
	s_waitcnt vmcnt(32)
	v_cvt_f32_ubyte0_e32 v140, v76
	v_cvt_f32_ubyte1_e32 v142, v76
	v_cvt_f32_ubyte2_e32 v144, v76
	v_cvt_f32_ubyte3_e32 v146, v76
	v_cvt_f32_ubyte0_e32 v148, v77
	v_cvt_f32_ubyte1_e32 v150, v77
	v_cvt_f32_ubyte2_e32 v152, v77
	v_cvt_f32_ubyte3_e32 v154, v77
	v_readlane_b32 s30, v121, 58
	s_lshl_b32 s30, s30, 12
	s_add_u32 s28, s26, s30
	s_addc_u32 s29, s27, 0
	global_load_dwordx2 v[76:77], v162, s[28:29]
	s_waitcnt vmcnt(32)
	v_cvt_f32_ubyte0_e32 v141, v78
	v_cvt_f32_ubyte1_e32 v143, v78
	v_cvt_f32_ubyte2_e32 v145, v78
	v_cvt_f32_ubyte3_e32 v147, v78
	v_cvt_f32_ubyte0_e32 v149, v79
	v_cvt_f32_ubyte1_e32 v151, v79
	v_cvt_f32_ubyte2_e32 v153, v79
	v_cvt_f32_ubyte3_e32 v155, v79
	v_readlane_b32 s30, v121, 59
	s_lshl_b32 s30, s30, 12
	s_add_u32 s28, s26, s30
	s_addc_u32 s29, s27, 0
	global_load_dwordx2 v[78:79], v162, s[28:29]
	v_mul_f32_e32 v202, v124, v108
	v_mul_f32_e32 v203, v125, v108
	v_mul_f32_e32 v204, v140, v108
	v_mul_f32_e32 v205, v141, v108
	v_fmac_f32_e32 v202, v126, v109
	v_fmac_f32_e32 v203, v127, v109
	v_fmac_f32_e32 v204, v142, v109
	v_fmac_f32_e32 v205, v143, v109
	v_fmac_f32_e32 v202, v128, v110
	v_fmac_f32_e32 v203, v129, v110
	v_fmac_f32_e32 v204, v144, v110
	v_fmac_f32_e32 v205, v145, v110
	v_fmac_f32_e32 v202, v130, v111
	v_fmac_f32_e32 v203, v131, v111
	v_fmac_f32_e32 v204, v146, v111
	v_fmac_f32_e32 v205, v147, v111
	v_fmac_f32_e32 v202, v132, v112
	v_fmac_f32_e32 v203, v133, v112
	v_fmac_f32_e32 v204, v148, v112
	v_fmac_f32_e32 v205, v149, v112
	v_fmac_f32_e32 v202, v134, v113
	v_fmac_f32_e32 v203, v135, v113
	v_fmac_f32_e32 v204, v150, v113
	v_fmac_f32_e32 v205, v151, v113
	v_fmac_f32_e32 v202, v136, v114
	v_fmac_f32_e32 v203, v137, v114
	v_fmac_f32_e32 v204, v152, v114
	v_fmac_f32_e32 v205, v153, v114
	v_fmac_f32_e32 v202, v138, v115
	v_fmac_f32_e32 v203, v139, v115
	v_fmac_f32_e32 v204, v154, v115
	v_fmac_f32_e32 v205, v155, v115
	s_waitcnt vmcnt(32)
	v_cvt_f32_ubyte0_e32 v124, v80
	v_cvt_f32_ubyte1_e32 v126, v80
	v_cvt_f32_ubyte2_e32 v128, v80
	v_cvt_f32_ubyte3_e32 v130, v80
	v_cvt_f32_ubyte0_e32 v132, v81
	v_cvt_f32_ubyte1_e32 v134, v81
	v_cvt_f32_ubyte2_e32 v136, v81
	v_cvt_f32_ubyte3_e32 v138, v81
	v_readlane_b32 s30, v121, 60
	s_lshl_b32 s30, s30, 12
	s_add_u32 s28, s26, s30
	s_addc_u32 s29, s27, 0
	global_load_dwordx2 v[80:81], v162, s[28:29]
	s_waitcnt vmcnt(32)
	v_cvt_f32_ubyte0_e32 v125, v82
	v_cvt_f32_ubyte1_e32 v127, v82
	v_cvt_f32_ubyte2_e32 v129, v82
	v_cvt_f32_ubyte3_e32 v131, v82
	v_cvt_f32_ubyte0_e32 v133, v83
	v_cvt_f32_ubyte1_e32 v135, v83
	v_cvt_f32_ubyte2_e32 v137, v83
	v_cvt_f32_ubyte3_e32 v139, v83
	v_readlane_b32 s30, v121, 61
	s_lshl_b32 s30, s30, 12
	s_add_u32 s28, s26, s30
	s_addc_u32 s29, s27, 0
	global_load_dwordx2 v[82:83], v162, s[28:29]
	s_waitcnt vmcnt(32)
	v_cvt_f32_ubyte0_e32 v140, v84
	v_cvt_f32_ubyte1_e32 v142, v84
	v_cvt_f32_ubyte2_e32 v144, v84
	v_cvt_f32_ubyte3_e32 v146, v84
	v_cvt_f32_ubyte0_e32 v148, v85
	v_cvt_f32_ubyte1_e32 v150, v85
	v_cvt_f32_ubyte2_e32 v152, v85
	v_cvt_f32_ubyte3_e32 v154, v85
	v_readlane_b32 s30, v121, 62
	s_lshl_b32 s30, s30, 12
	s_add_u32 s28, s26, s30
	s_addc_u32 s29, s27, 0
	global_load_dwordx2 v[84:85], v162, s[28:29]
	s_waitcnt vmcnt(32)
	v_cvt_f32_ubyte0_e32 v141, v86
	v_cvt_f32_ubyte1_e32 v143, v86
	v_cvt_f32_ubyte2_e32 v145, v86
	v_cvt_f32_ubyte3_e32 v147, v86
	v_cvt_f32_ubyte0_e32 v149, v87
	v_cvt_f32_ubyte1_e32 v151, v87
	v_cvt_f32_ubyte2_e32 v153, v87
	v_cvt_f32_ubyte3_e32 v155, v87
	v_readlane_b32 s30, v121, 63
	s_lshl_b32 s30, s30, 12
	s_add_u32 s28, s26, s30
	s_addc_u32 s29, s27, 0
	global_load_dwordx2 v[86:87], v162, s[28:29]
	v_mul_f32_e32 v206, v124, v108
	v_mul_f32_e32 v207, v125, v108
	v_mul_f32_e32 v208, v140, v108
	v_mul_f32_e32 v209, v141, v108
	v_fmac_f32_e32 v206, v126, v109
	v_fmac_f32_e32 v207, v127, v109
	v_fmac_f32_e32 v208, v142, v109
	v_fmac_f32_e32 v209, v143, v109
	v_fmac_f32_e32 v206, v128, v110
	v_fmac_f32_e32 v207, v129, v110
	v_fmac_f32_e32 v208, v144, v110
	v_fmac_f32_e32 v209, v145, v110
	v_fmac_f32_e32 v206, v130, v111
	v_fmac_f32_e32 v207, v131, v111
	v_fmac_f32_e32 v208, v146, v111
	v_fmac_f32_e32 v209, v147, v111
	v_fmac_f32_e32 v206, v132, v112
	v_fmac_f32_e32 v207, v133, v112
	v_fmac_f32_e32 v208, v148, v112
	v_fmac_f32_e32 v209, v149, v112
	v_fmac_f32_e32 v206, v134, v113
	v_fmac_f32_e32 v207, v135, v113
	v_fmac_f32_e32 v208, v150, v113
	v_fmac_f32_e32 v209, v151, v113
	v_fmac_f32_e32 v206, v136, v114
	v_fmac_f32_e32 v207, v137, v114
	v_fmac_f32_e32 v208, v152, v114
	v_fmac_f32_e32 v209, v153, v114
	v_fmac_f32_e32 v206, v138, v115
	v_fmac_f32_e32 v207, v139, v115
	v_fmac_f32_e32 v208, v154, v115
	v_fmac_f32_e32 v209, v155, v115
	v_permlane32_swap_b32_e32 v178, v194
	v_permlane32_swap_b32_e32 v179, v195
	v_permlane32_swap_b32_e32 v180, v196
	v_permlane32_swap_b32_e32 v181, v197
	v_permlane32_swap_b32_e32 v182, v198
	v_permlane32_swap_b32_e32 v183, v199
	v_permlane32_swap_b32_e32 v184, v200
	v_permlane32_swap_b32_e32 v185, v201
	v_permlane32_swap_b32_e32 v186, v202
	v_permlane32_swap_b32_e32 v187, v203
	v_permlane32_swap_b32_e32 v188, v204
	v_permlane32_swap_b32_e32 v189, v205
	v_permlane32_swap_b32_e32 v190, v206
	v_permlane32_swap_b32_e32 v191, v207
	v_permlane32_swap_b32_e32 v192, v208
	v_permlane32_swap_b32_e32 v193, v209
	v_add_f32_e32 v178, v178, v194
	v_add_f32_e32 v179, v179, v195
	v_add_f32_e32 v180, v180, v196
	v_add_f32_e32 v181, v181, v197
	v_add_f32_e32 v182, v182, v198
	v_add_f32_e32 v183, v183, v199
	v_add_f32_e32 v184, v184, v200
	v_add_f32_e32 v185, v185, v201
	v_add_f32_e32 v186, v186, v202
	v_add_f32_e32 v187, v187, v203
	v_add_f32_e32 v188, v188, v204
	v_add_f32_e32 v189, v189, v205
	v_add_f32_e32 v190, v190, v206
	v_add_f32_e32 v191, v191, v207
	v_add_f32_e32 v192, v192, v208
	v_add_f32_e32 v193, v193, v209
	v_permlane16_swap_b32_e32 v178, v186
	v_permlane16_swap_b32_e32 v179, v187
	v_permlane16_swap_b32_e32 v180, v188
	v_permlane16_swap_b32_e32 v181, v189
	v_permlane16_swap_b32_e32 v182, v190
	v_permlane16_swap_b32_e32 v183, v191
	v_permlane16_swap_b32_e32 v184, v192
	v_permlane16_swap_b32_e32 v185, v193
	v_add_f32_e32 v178, v178, v186
	v_add_f32_e32 v179, v179, v187
	v_add_f32_e32 v180, v180, v188
	v_add_f32_e32 v181, v181, v189
	v_add_f32_e32 v182, v182, v190
	v_add_f32_e32 v183, v183, v191
	v_add_f32_e32 v184, v184, v192
	v_add_f32_e32 v185, v185, v193
	v_cndmask_b32_e64 v2, v178, v182, s[8:9]
	v_cndmask_b32_e64 v3, v179, v183, s[8:9]
	v_cndmask_b32_e64 v4, v180, v184, s[8:9]
	v_cndmask_b32_e64 v5, v181, v185, s[8:9]
	v_cndmask_b32_e64 v6, v182, v178, s[8:9]
	v_cndmask_b32_e64 v7, v183, v179, s[8:9]
	v_cndmask_b32_e64 v8, v184, v180, s[8:9]
	v_cndmask_b32_e64 v9, v185, v181, s[8:9]
	v_add_f32_dpp v6, v2, v6 row_ror:8 row_mask:0xf bank_mask:0xf
	v_add_f32_dpp v7, v3, v7 row_ror:8 row_mask:0xf bank_mask:0xf
	v_add_f32_dpp v8, v4, v8 row_ror:8 row_mask:0xf bank_mask:0xf
	v_add_f32_dpp v9, v5, v9 row_ror:8 row_mask:0xf bank_mask:0xf
	v_cndmask_b32_e64 v2, v6, v8, s[10:11]
	v_cndmask_b32_e64 v3, v7, v9, s[10:11]
	v_cndmask_b32_e64 v4, v8, v6, s[10:11]
	v_cndmask_b32_e64 v5, v9, v7, s[10:11]
	v_add_f32_dpp v4, v2, v4 row_half_mirror row_mask:0xf bank_mask:0xf
	v_add_f32_dpp v5, v3, v5 row_half_mirror row_mask:0xf bank_mask:0xf
	v_cndmask_b32_e64 v2, v4, v5, s[14:15]
	v_cndmask_b32_e64 v3, v5, v4, s[14:15]
	s_nop 0
	v_add_f32_dpp v3, v2, v3 quad_perm:[2,3,0,1] row_mask:0xf bank_mask:0xf
	s_nop 1
	v_add_f32_dpp v11, v3, v3 quad_perm:[1,0,3,2] row_mask:0xf bank_mask:0xf
	s_mov_b64 exec, s[2:3]
	global_store_dword v[22:23], v11, off offset:256
	s_mov_b64 exec, -1
	s_waitcnt vmcnt(32)
	v_cvt_f32_ubyte0_e32 v124, v24
	v_cvt_f32_ubyte1_e32 v126, v24
	v_cvt_f32_ubyte2_e32 v128, v24
	v_cvt_f32_ubyte3_e32 v130, v24
	v_cvt_f32_ubyte0_e32 v132, v25
	v_cvt_f32_ubyte1_e32 v134, v25
	v_cvt_f32_ubyte2_e32 v136, v25
	v_cvt_f32_ubyte3_e32 v138, v25
	s_waitcnt vmcnt(31)
	v_cvt_f32_ubyte0_e32 v125, v26
	v_cvt_f32_ubyte1_e32 v127, v26
	v_cvt_f32_ubyte2_e32 v129, v26
	v_cvt_f32_ubyte3_e32 v131, v26
	v_cvt_f32_ubyte0_e32 v133, v27
	v_cvt_f32_ubyte1_e32 v135, v27
	v_cvt_f32_ubyte2_e32 v137, v27
	v_cvt_f32_ubyte3_e32 v139, v27
	s_waitcnt vmcnt(30)
	v_cvt_f32_ubyte0_e32 v140, v28
	v_cvt_f32_ubyte1_e32 v142, v28
	v_cvt_f32_ubyte2_e32 v144, v28
	v_cvt_f32_ubyte3_e32 v146, v28
	v_cvt_f32_ubyte0_e32 v148, v29
	v_cvt_f32_ubyte1_e32 v150, v29
	v_cvt_f32_ubyte2_e32 v152, v29
	v_cvt_f32_ubyte3_e32 v154, v29
	s_waitcnt vmcnt(29)
	v_cvt_f32_ubyte0_e32 v141, v30
	v_cvt_f32_ubyte1_e32 v143, v30
	v_cvt_f32_ubyte2_e32 v145, v30
	v_cvt_f32_ubyte3_e32 v147, v30
	v_cvt_f32_ubyte0_e32 v149, v31
	v_cvt_f32_ubyte1_e32 v151, v31
	v_cvt_f32_ubyte2_e32 v153, v31
	v_cvt_f32_ubyte3_e32 v155, v31
	v_mul_f32_e32 v178, v124, v108
	v_mul_f32_e32 v179, v125, v108
	v_mul_f32_e32 v180, v140, v108
	v_mul_f32_e32 v181, v141, v108
	v_fmac_f32_e32 v178, v126, v109
	v_fmac_f32_e32 v179, v127, v109
	v_fmac_f32_e32 v180, v142, v109
	v_fmac_f32_e32 v181, v143, v109
	v_fmac_f32_e32 v178, v128, v110
	v_fmac_f32_e32 v179, v129, v110
	v_fmac_f32_e32 v180, v144, v110
	v_fmac_f32_e32 v181, v145, v110
	v_fmac_f32_e32 v178, v130, v111
	v_fmac_f32_e32 v179, v131, v111
	v_fmac_f32_e32 v180, v146, v111
	v_fmac_f32_e32 v181, v147, v111
	v_fmac_f32_e32 v178, v132, v112
	v_fmac_f32_e32 v179, v133, v112
	v_fmac_f32_e32 v180, v148, v112
	v_fmac_f32_e32 v181, v149, v112
	v_fmac_f32_e32 v178, v134, v113
	v_fmac_f32_e32 v179, v135, v113
	v_fmac_f32_e32 v180, v150, v113
	v_fmac_f32_e32 v181, v151, v113
	v_fmac_f32_e32 v178, v136, v114
	v_fmac_f32_e32 v179, v137, v114
	v_fmac_f32_e32 v180, v152, v114
	v_fmac_f32_e32 v181, v153, v114
	v_fmac_f32_e32 v178, v138, v115
	v_fmac_f32_e32 v179, v139, v115
	v_fmac_f32_e32 v180, v154, v115
	v_fmac_f32_e32 v181, v155, v115
	s_waitcnt vmcnt(28)
	v_cvt_f32_ubyte0_e32 v124, v32
	v_cvt_f32_ubyte1_e32 v126, v32
	v_cvt_f32_ubyte2_e32 v128, v32
	v_cvt_f32_ubyte3_e32 v130, v32
	v_cvt_f32_ubyte0_e32 v132, v33
	v_cvt_f32_ubyte1_e32 v134, v33
	v_cvt_f32_ubyte2_e32 v136, v33
	v_cvt_f32_ubyte3_e32 v138, v33
	s_waitcnt vmcnt(27)
	v_cvt_f32_ubyte0_e32 v125, v34
	v_cvt_f32_ubyte1_e32 v127, v34
	v_cvt_f32_ubyte2_e32 v129, v34
	v_cvt_f32_ubyte3_e32 v131, v34
	v_cvt_f32_ubyte0_e32 v133, v35
	v_cvt_f32_ubyte1_e32 v135, v35
	v_cvt_f32_ubyte2_e32 v137, v35
	v_cvt_f32_ubyte3_e32 v139, v35
	s_waitcnt vmcnt(26)
	v_cvt_f32_ubyte0_e32 v140, v36
	v_cvt_f32_ubyte1_e32 v142, v36
	v_cvt_f32_ubyte2_e32 v144, v36
	v_cvt_f32_ubyte3_e32 v146, v36
	v_cvt_f32_ubyte0_e32 v148, v37
	v_cvt_f32_ubyte1_e32 v150, v37
	v_cvt_f32_ubyte2_e32 v152, v37
	v_cvt_f32_ubyte3_e32 v154, v37
	s_waitcnt vmcnt(25)
	v_cvt_f32_ubyte0_e32 v141, v38
	v_cvt_f32_ubyte1_e32 v143, v38
	v_cvt_f32_ubyte2_e32 v145, v38
	v_cvt_f32_ubyte3_e32 v147, v38
	v_cvt_f32_ubyte0_e32 v149, v39
	v_cvt_f32_ubyte1_e32 v151, v39
	v_cvt_f32_ubyte2_e32 v153, v39
	v_cvt_f32_ubyte3_e32 v155, v39
	v_mul_f32_e32 v182, v124, v108
	v_mul_f32_e32 v183, v125, v108
	v_mul_f32_e32 v184, v140, v108
	v_mul_f32_e32 v185, v141, v108
	v_fmac_f32_e32 v182, v126, v109
	v_fmac_f32_e32 v183, v127, v109
	v_fmac_f32_e32 v184, v142, v109
	v_fmac_f32_e32 v185, v143, v109
	v_fmac_f32_e32 v182, v128, v110
	v_fmac_f32_e32 v183, v129, v110
	v_fmac_f32_e32 v184, v144, v110
	v_fmac_f32_e32 v185, v145, v110
	v_fmac_f32_e32 v182, v130, v111
	v_fmac_f32_e32 v183, v131, v111
	v_fmac_f32_e32 v184, v146, v111
	v_fmac_f32_e32 v185, v147, v111
	v_fmac_f32_e32 v182, v132, v112
	v_fmac_f32_e32 v183, v133, v112
	v_fmac_f32_e32 v184, v148, v112
	v_fmac_f32_e32 v185, v149, v112
	v_fmac_f32_e32 v182, v134, v113
	v_fmac_f32_e32 v183, v135, v113
	v_fmac_f32_e32 v184, v150, v113
	v_fmac_f32_e32 v185, v151, v113
	v_fmac_f32_e32 v182, v136, v114
	v_fmac_f32_e32 v183, v137, v114
	v_fmac_f32_e32 v184, v152, v114
	v_fmac_f32_e32 v185, v153, v114
	v_fmac_f32_e32 v182, v138, v115
	v_fmac_f32_e32 v183, v139, v115
	v_fmac_f32_e32 v184, v154, v115
	v_fmac_f32_e32 v185, v155, v115
	s_waitcnt vmcnt(24)
	v_cvt_f32_ubyte0_e32 v124, v40
	v_cvt_f32_ubyte1_e32 v126, v40
	v_cvt_f32_ubyte2_e32 v128, v40
	v_cvt_f32_ubyte3_e32 v130, v40
	v_cvt_f32_ubyte0_e32 v132, v41
	v_cvt_f32_ubyte1_e32 v134, v41
	v_cvt_f32_ubyte2_e32 v136, v41
	v_cvt_f32_ubyte3_e32 v138, v41
	s_waitcnt vmcnt(23)
	v_cvt_f32_ubyte0_e32 v125, v42
	v_cvt_f32_ubyte1_e32 v127, v42
	v_cvt_f32_ubyte2_e32 v129, v42
	v_cvt_f32_ubyte3_e32 v131, v42
	v_cvt_f32_ubyte0_e32 v133, v43
	v_cvt_f32_ubyte1_e32 v135, v43
	v_cvt_f32_ubyte2_e32 v137, v43
	v_cvt_f32_ubyte3_e32 v139, v43
	s_waitcnt vmcnt(22)
	v_cvt_f32_ubyte0_e32 v140, v44
	v_cvt_f32_ubyte1_e32 v142, v44
	v_cvt_f32_ubyte2_e32 v144, v44
	v_cvt_f32_ubyte3_e32 v146, v44
	v_cvt_f32_ubyte0_e32 v148, v45
	v_cvt_f32_ubyte1_e32 v150, v45
	v_cvt_f32_ubyte2_e32 v152, v45
	v_cvt_f32_ubyte3_e32 v154, v45
	s_waitcnt vmcnt(21)
	v_cvt_f32_ubyte0_e32 v141, v46
	v_cvt_f32_ubyte1_e32 v143, v46
	v_cvt_f32_ubyte2_e32 v145, v46
	v_cvt_f32_ubyte3_e32 v147, v46
	v_cvt_f32_ubyte0_e32 v149, v47
	v_cvt_f32_ubyte1_e32 v151, v47
	v_cvt_f32_ubyte2_e32 v153, v47
	v_cvt_f32_ubyte3_e32 v155, v47
	v_mul_f32_e32 v186, v124, v108
	v_mul_f32_e32 v187, v125, v108
	v_mul_f32_e32 v188, v140, v108
	v_mul_f32_e32 v189, v141, v108
	v_fmac_f32_e32 v186, v126, v109
	v_fmac_f32_e32 v187, v127, v109
	v_fmac_f32_e32 v188, v142, v109
	v_fmac_f32_e32 v189, v143, v109
	v_fmac_f32_e32 v186, v128, v110
	v_fmac_f32_e32 v187, v129, v110
	v_fmac_f32_e32 v188, v144, v110
	v_fmac_f32_e32 v189, v145, v110
	v_fmac_f32_e32 v186, v130, v111
	v_fmac_f32_e32 v187, v131, v111
	v_fmac_f32_e32 v188, v146, v111
	v_fmac_f32_e32 v189, v147, v111
	v_fmac_f32_e32 v186, v132, v112
	v_fmac_f32_e32 v187, v133, v112
	v_fmac_f32_e32 v188, v148, v112
	v_fmac_f32_e32 v189, v149, v112
	v_fmac_f32_e32 v186, v134, v113
	v_fmac_f32_e32 v187, v135, v113
	v_fmac_f32_e32 v188, v150, v113
	v_fmac_f32_e32 v189, v151, v113
	v_fmac_f32_e32 v186, v136, v114
	v_fmac_f32_e32 v187, v137, v114
	v_fmac_f32_e32 v188, v152, v114
	v_fmac_f32_e32 v189, v153, v114
	v_fmac_f32_e32 v186, v138, v115
	v_fmac_f32_e32 v187, v139, v115
	v_fmac_f32_e32 v188, v154, v115
	v_fmac_f32_e32 v189, v155, v115
	s_waitcnt vmcnt(20)
	v_cvt_f32_ubyte0_e32 v124, v48
	v_cvt_f32_ubyte1_e32 v126, v48
	v_cvt_f32_ubyte2_e32 v128, v48
	v_cvt_f32_ubyte3_e32 v130, v48
	v_cvt_f32_ubyte0_e32 v132, v49
	v_cvt_f32_ubyte1_e32 v134, v49
	v_cvt_f32_ubyte2_e32 v136, v49
	v_cvt_f32_ubyte3_e32 v138, v49
	s_waitcnt vmcnt(19)
	v_cvt_f32_ubyte0_e32 v125, v50
	v_cvt_f32_ubyte1_e32 v127, v50
	v_cvt_f32_ubyte2_e32 v129, v50
	v_cvt_f32_ubyte3_e32 v131, v50
	v_cvt_f32_ubyte0_e32 v133, v51
	v_cvt_f32_ubyte1_e32 v135, v51
	v_cvt_f32_ubyte2_e32 v137, v51
	v_cvt_f32_ubyte3_e32 v139, v51
	s_waitcnt vmcnt(18)
	v_cvt_f32_ubyte0_e32 v140, v52
	v_cvt_f32_ubyte1_e32 v142, v52
	v_cvt_f32_ubyte2_e32 v144, v52
	v_cvt_f32_ubyte3_e32 v146, v52
	v_cvt_f32_ubyte0_e32 v148, v53
	v_cvt_f32_ubyte1_e32 v150, v53
	v_cvt_f32_ubyte2_e32 v152, v53
	v_cvt_f32_ubyte3_e32 v154, v53
	s_waitcnt vmcnt(17)
	v_cvt_f32_ubyte0_e32 v141, v54
	v_cvt_f32_ubyte1_e32 v143, v54
	v_cvt_f32_ubyte2_e32 v145, v54
	v_cvt_f32_ubyte3_e32 v147, v54
	v_cvt_f32_ubyte0_e32 v149, v55
	v_cvt_f32_ubyte1_e32 v151, v55
	v_cvt_f32_ubyte2_e32 v153, v55
	v_cvt_f32_ubyte3_e32 v155, v55
	v_mul_f32_e32 v190, v124, v108
	v_mul_f32_e32 v191, v125, v108
	v_mul_f32_e32 v192, v140, v108
	v_mul_f32_e32 v193, v141, v108
	v_fmac_f32_e32 v190, v126, v109
	v_fmac_f32_e32 v191, v127, v109
	v_fmac_f32_e32 v192, v142, v109
	v_fmac_f32_e32 v193, v143, v109
	v_fmac_f32_e32 v190, v128, v110
	v_fmac_f32_e32 v191, v129, v110
	v_fmac_f32_e32 v192, v144, v110
	v_fmac_f32_e32 v193, v145, v110
	v_fmac_f32_e32 v190, v130, v111
	v_fmac_f32_e32 v191, v131, v111
	v_fmac_f32_e32 v192, v146, v111
	v_fmac_f32_e32 v193, v147, v111
	v_fmac_f32_e32 v190, v132, v112
	v_fmac_f32_e32 v191, v133, v112
	v_fmac_f32_e32 v192, v148, v112
	v_fmac_f32_e32 v193, v149, v112
	v_fmac_f32_e32 v190, v134, v113
	v_fmac_f32_e32 v191, v135, v113
	v_fmac_f32_e32 v192, v150, v113
	v_fmac_f32_e32 v193, v151, v113
	v_fmac_f32_e32 v190, v136, v114
	v_fmac_f32_e32 v191, v137, v114
	v_fmac_f32_e32 v192, v152, v114
	v_fmac_f32_e32 v193, v153, v114
	v_fmac_f32_e32 v190, v138, v115
	v_fmac_f32_e32 v191, v139, v115
	v_fmac_f32_e32 v192, v154, v115
	v_fmac_f32_e32 v193, v155, v115
	s_waitcnt vmcnt(16)
	v_cvt_f32_ubyte0_e32 v124, v56
	v_cvt_f32_ubyte1_e32 v126, v56
	v_cvt_f32_ubyte2_e32 v128, v56
	v_cvt_f32_ubyte3_e32 v130, v56
	v_cvt_f32_ubyte0_e32 v132, v57
	v_cvt_f32_ubyte1_e32 v134, v57
	v_cvt_f32_ubyte2_e32 v136, v57
	v_cvt_f32_ubyte3_e32 v138, v57
	s_waitcnt vmcnt(15)
	v_cvt_f32_ubyte0_e32 v125, v58
	v_cvt_f32_ubyte1_e32 v127, v58
	v_cvt_f32_ubyte2_e32 v129, v58
	v_cvt_f32_ubyte3_e32 v131, v58
	v_cvt_f32_ubyte0_e32 v133, v59
	v_cvt_f32_ubyte1_e32 v135, v59
	v_cvt_f32_ubyte2_e32 v137, v59
	v_cvt_f32_ubyte3_e32 v139, v59
	s_waitcnt vmcnt(14)
	v_cvt_f32_ubyte0_e32 v140, v60
	v_cvt_f32_ubyte1_e32 v142, v60
	v_cvt_f32_ubyte2_e32 v144, v60
	v_cvt_f32_ubyte3_e32 v146, v60
	v_cvt_f32_ubyte0_e32 v148, v61
	v_cvt_f32_ubyte1_e32 v150, v61
	v_cvt_f32_ubyte2_e32 v152, v61
	v_cvt_f32_ubyte3_e32 v154, v61
	s_waitcnt vmcnt(13)
	v_cvt_f32_ubyte0_e32 v141, v62
	v_cvt_f32_ubyte1_e32 v143, v62
	v_cvt_f32_ubyte2_e32 v145, v62
	v_cvt_f32_ubyte3_e32 v147, v62
	v_cvt_f32_ubyte0_e32 v149, v63
	v_cvt_f32_ubyte1_e32 v151, v63
	v_cvt_f32_ubyte2_e32 v153, v63
	v_cvt_f32_ubyte3_e32 v155, v63
	v_mul_f32_e32 v194, v124, v108
	v_mul_f32_e32 v195, v125, v108
	v_mul_f32_e32 v196, v140, v108
	v_mul_f32_e32 v197, v141, v108
	v_fmac_f32_e32 v194, v126, v109
	v_fmac_f32_e32 v195, v127, v109
	v_fmac_f32_e32 v196, v142, v109
	v_fmac_f32_e32 v197, v143, v109
	v_fmac_f32_e32 v194, v128, v110
	v_fmac_f32_e32 v195, v129, v110
	v_fmac_f32_e32 v196, v144, v110
	v_fmac_f32_e32 v197, v145, v110
	v_fmac_f32_e32 v194, v130, v111
	v_fmac_f32_e32 v195, v131, v111
	v_fmac_f32_e32 v196, v146, v111
	v_fmac_f32_e32 v197, v147, v111
	v_fmac_f32_e32 v194, v132, v112
	v_fmac_f32_e32 v195, v133, v112
	v_fmac_f32_e32 v196, v148, v112
	v_fmac_f32_e32 v197, v149, v112
	v_fmac_f32_e32 v194, v134, v113
	v_fmac_f32_e32 v195, v135, v113
	v_fmac_f32_e32 v196, v150, v113
	v_fmac_f32_e32 v197, v151, v113
	v_fmac_f32_e32 v194, v136, v114
	v_fmac_f32_e32 v195, v137, v114
	v_fmac_f32_e32 v196, v152, v114
	v_fmac_f32_e32 v197, v153, v114
	v_fmac_f32_e32 v194, v138, v115
	v_fmac_f32_e32 v195, v139, v115
	v_fmac_f32_e32 v196, v154, v115
	v_fmac_f32_e32 v197, v155, v115
	s_waitcnt vmcnt(12)
	v_cvt_f32_ubyte0_e32 v124, v64
	v_cvt_f32_ubyte1_e32 v126, v64
	v_cvt_f32_ubyte2_e32 v128, v64
	v_cvt_f32_ubyte3_e32 v130, v64
	v_cvt_f32_ubyte0_e32 v132, v65
	v_cvt_f32_ubyte1_e32 v134, v65
	v_cvt_f32_ubyte2_e32 v136, v65
	v_cvt_f32_ubyte3_e32 v138, v65
	s_waitcnt vmcnt(11)
	v_cvt_f32_ubyte0_e32 v125, v66
	v_cvt_f32_ubyte1_e32 v127, v66
	v_cvt_f32_ubyte2_e32 v129, v66
	v_cvt_f32_ubyte3_e32 v131, v66
	v_cvt_f32_ubyte0_e32 v133, v67
	v_cvt_f32_ubyte1_e32 v135, v67
	v_cvt_f32_ubyte2_e32 v137, v67
	v_cvt_f32_ubyte3_e32 v139, v67
	s_waitcnt vmcnt(10)
	v_cvt_f32_ubyte0_e32 v140, v68
	v_cvt_f32_ubyte1_e32 v142, v68
	v_cvt_f32_ubyte2_e32 v144, v68
	v_cvt_f32_ubyte3_e32 v146, v68
	v_cvt_f32_ubyte0_e32 v148, v69
	v_cvt_f32_ubyte1_e32 v150, v69
	v_cvt_f32_ubyte2_e32 v152, v69
	v_cvt_f32_ubyte3_e32 v154, v69
	s_waitcnt vmcnt(9)
	v_cvt_f32_ubyte0_e32 v141, v70
	v_cvt_f32_ubyte1_e32 v143, v70
	v_cvt_f32_ubyte2_e32 v145, v70
	v_cvt_f32_ubyte3_e32 v147, v70
	v_cvt_f32_ubyte0_e32 v149, v71
	v_cvt_f32_ubyte1_e32 v151, v71
	v_cvt_f32_ubyte2_e32 v153, v71
	v_cvt_f32_ubyte3_e32 v155, v71
	v_mul_f32_e32 v198, v124, v108
	v_mul_f32_e32 v199, v125, v108
	v_mul_f32_e32 v200, v140, v108
	v_mul_f32_e32 v201, v141, v108
	v_fmac_f32_e32 v198, v126, v109
	v_fmac_f32_e32 v199, v127, v109
	v_fmac_f32_e32 v200, v142, v109
	v_fmac_f32_e32 v201, v143, v109
	v_fmac_f32_e32 v198, v128, v110
	v_fmac_f32_e32 v199, v129, v110
	v_fmac_f32_e32 v200, v144, v110
	v_fmac_f32_e32 v201, v145, v110
	v_fmac_f32_e32 v198, v130, v111
	v_fmac_f32_e32 v199, v131, v111
	v_fmac_f32_e32 v200, v146, v111
	v_fmac_f32_e32 v201, v147, v111
	v_fmac_f32_e32 v198, v132, v112
	v_fmac_f32_e32 v199, v133, v112
	v_fmac_f32_e32 v200, v148, v112
	v_fmac_f32_e32 v201, v149, v112
	v_fmac_f32_e32 v198, v134, v113
	v_fmac_f32_e32 v199, v135, v113
	v_fmac_f32_e32 v200, v150, v113
	v_fmac_f32_e32 v201, v151, v113
	v_fmac_f32_e32 v198, v136, v114
	v_fmac_f32_e32 v199, v137, v114
	v_fmac_f32_e32 v200, v152, v114
	v_fmac_f32_e32 v201, v153, v114
	v_fmac_f32_e32 v198, v138, v115
	v_fmac_f32_e32 v199, v139, v115
	v_fmac_f32_e32 v200, v154, v115
	v_fmac_f32_e32 v201, v155, v115
	s_waitcnt vmcnt(8)
	v_cvt_f32_ubyte0_e32 v124, v72
	v_cvt_f32_ubyte1_e32 v126, v72
	v_cvt_f32_ubyte2_e32 v128, v72
	v_cvt_f32_ubyte3_e32 v130, v72
	v_cvt_f32_ubyte0_e32 v132, v73
	v_cvt_f32_ubyte1_e32 v134, v73
	v_cvt_f32_ubyte2_e32 v136, v73
	v_cvt_f32_ubyte3_e32 v138, v73
	s_waitcnt vmcnt(7)
	v_cvt_f32_ubyte0_e32 v125, v74
	v_cvt_f32_ubyte1_e32 v127, v74
	v_cvt_f32_ubyte2_e32 v129, v74
	v_cvt_f32_ubyte3_e32 v131, v74
	v_cvt_f32_ubyte0_e32 v133, v75
	v_cvt_f32_ubyte1_e32 v135, v75
	v_cvt_f32_ubyte2_e32 v137, v75
	v_cvt_f32_ubyte3_e32 v139, v75
	s_waitcnt vmcnt(6)
	v_cvt_f32_ubyte0_e32 v140, v76
	v_cvt_f32_ubyte1_e32 v142, v76
	v_cvt_f32_ubyte2_e32 v144, v76
	v_cvt_f32_ubyte3_e32 v146, v76
	v_cvt_f32_ubyte0_e32 v148, v77
	v_cvt_f32_ubyte1_e32 v150, v77
	v_cvt_f32_ubyte2_e32 v152, v77
	v_cvt_f32_ubyte3_e32 v154, v77
	s_waitcnt vmcnt(5)
	v_cvt_f32_ubyte0_e32 v141, v78
	v_cvt_f32_ubyte1_e32 v143, v78
	v_cvt_f32_ubyte2_e32 v145, v78
	v_cvt_f32_ubyte3_e32 v147, v78
	v_cvt_f32_ubyte0_e32 v149, v79
	v_cvt_f32_ubyte1_e32 v151, v79
	v_cvt_f32_ubyte2_e32 v153, v79
	v_cvt_f32_ubyte3_e32 v155, v79
	v_mul_f32_e32 v202, v124, v108
	v_mul_f32_e32 v203, v125, v108
	v_mul_f32_e32 v204, v140, v108
	v_mul_f32_e32 v205, v141, v108
	v_fmac_f32_e32 v202, v126, v109
	v_fmac_f32_e32 v203, v127, v109
	v_fmac_f32_e32 v204, v142, v109
	v_fmac_f32_e32 v205, v143, v109
	v_fmac_f32_e32 v202, v128, v110
	v_fmac_f32_e32 v203, v129, v110
	v_fmac_f32_e32 v204, v144, v110
	v_fmac_f32_e32 v205, v145, v110
	v_fmac_f32_e32 v202, v130, v111
	v_fmac_f32_e32 v203, v131, v111
	v_fmac_f32_e32 v204, v146, v111
	v_fmac_f32_e32 v205, v147, v111
	v_fmac_f32_e32 v202, v132, v112
	v_fmac_f32_e32 v203, v133, v112
	v_fmac_f32_e32 v204, v148, v112
	v_fmac_f32_e32 v205, v149, v112
	v_fmac_f32_e32 v202, v134, v113
	v_fmac_f32_e32 v203, v135, v113
	v_fmac_f32_e32 v204, v150, v113
	v_fmac_f32_e32 v205, v151, v113
	v_fmac_f32_e32 v202, v136, v114
	v_fmac_f32_e32 v203, v137, v114
	v_fmac_f32_e32 v204, v152, v114
	v_fmac_f32_e32 v205, v153, v114
	v_fmac_f32_e32 v202, v138, v115
	v_fmac_f32_e32 v203, v139, v115
	v_fmac_f32_e32 v204, v154, v115
	v_fmac_f32_e32 v205, v155, v115
	s_waitcnt vmcnt(4)
	v_cvt_f32_ubyte0_e32 v124, v80
	v_cvt_f32_ubyte1_e32 v126, v80
	v_cvt_f32_ubyte2_e32 v128, v80
	v_cvt_f32_ubyte3_e32 v130, v80
	v_cvt_f32_ubyte0_e32 v132, v81
	v_cvt_f32_ubyte1_e32 v134, v81
	v_cvt_f32_ubyte2_e32 v136, v81
	v_cvt_f32_ubyte3_e32 v138, v81
	s_waitcnt vmcnt(3)
	v_cvt_f32_ubyte0_e32 v125, v82
	v_cvt_f32_ubyte1_e32 v127, v82
	v_cvt_f32_ubyte2_e32 v129, v82
	v_cvt_f32_ubyte3_e32 v131, v82
	v_cvt_f32_ubyte0_e32 v133, v83
	v_cvt_f32_ubyte1_e32 v135, v83
	v_cvt_f32_ubyte2_e32 v137, v83
	v_cvt_f32_ubyte3_e32 v139, v83
	s_waitcnt vmcnt(2)
	v_cvt_f32_ubyte0_e32 v140, v84
	v_cvt_f32_ubyte1_e32 v142, v84
	v_cvt_f32_ubyte2_e32 v144, v84
	v_cvt_f32_ubyte3_e32 v146, v84
	v_cvt_f32_ubyte0_e32 v148, v85
	v_cvt_f32_ubyte1_e32 v150, v85
	v_cvt_f32_ubyte2_e32 v152, v85
	v_cvt_f32_ubyte3_e32 v154, v85
	s_waitcnt vmcnt(1)
	v_cvt_f32_ubyte0_e32 v141, v86
	v_cvt_f32_ubyte1_e32 v143, v86
	v_cvt_f32_ubyte2_e32 v145, v86
	v_cvt_f32_ubyte3_e32 v147, v86
	v_cvt_f32_ubyte0_e32 v149, v87
	v_cvt_f32_ubyte1_e32 v151, v87
	v_cvt_f32_ubyte2_e32 v153, v87
	v_cvt_f32_ubyte3_e32 v155, v87
	v_mul_f32_e32 v206, v124, v108
	v_mul_f32_e32 v207, v125, v108
	v_mul_f32_e32 v208, v140, v108
	v_mul_f32_e32 v209, v141, v108
	v_fmac_f32_e32 v206, v126, v109
	v_fmac_f32_e32 v207, v127, v109
	v_fmac_f32_e32 v208, v142, v109
	v_fmac_f32_e32 v209, v143, v109
	v_fmac_f32_e32 v206, v128, v110
	v_fmac_f32_e32 v207, v129, v110
	v_fmac_f32_e32 v208, v144, v110
	v_fmac_f32_e32 v209, v145, v110
	v_fmac_f32_e32 v206, v130, v111
	v_fmac_f32_e32 v207, v131, v111
	v_fmac_f32_e32 v208, v146, v111
	v_fmac_f32_e32 v209, v147, v111
	v_fmac_f32_e32 v206, v132, v112
	v_fmac_f32_e32 v207, v133, v112
	v_fmac_f32_e32 v208, v148, v112
	v_fmac_f32_e32 v209, v149, v112
	v_fmac_f32_e32 v206, v134, v113
	v_fmac_f32_e32 v207, v135, v113
	v_fmac_f32_e32 v208, v150, v113
	v_fmac_f32_e32 v209, v151, v113
	v_fmac_f32_e32 v206, v136, v114
	v_fmac_f32_e32 v207, v137, v114
	v_fmac_f32_e32 v208, v152, v114
	v_fmac_f32_e32 v209, v153, v114
	v_fmac_f32_e32 v206, v138, v115
	v_fmac_f32_e32 v207, v139, v115
	v_fmac_f32_e32 v208, v154, v115
	v_fmac_f32_e32 v209, v155, v115
	v_readlane_b32 s30, v122, 0
	s_lshl_b32 s30, s30, 12
	s_add_u32 s28, s26, s30
	s_addc_u32 s29, s27, 0
	global_load_dwordx2 v[24:25], v162, s[28:29]
	v_readlane_b32 s30, v122, 1
	s_lshl_b32 s30, s30, 12
	s_add_u32 s28, s26, s30
	s_addc_u32 s29, s27, 0
	global_load_dwordx2 v[26:27], v162, s[28:29]
	v_readlane_b32 s30, v122, 2
	s_lshl_b32 s30, s30, 12
	s_add_u32 s28, s26, s30
	s_addc_u32 s29, s27, 0
	global_load_dwordx2 v[28:29], v162, s[28:29]
	v_readlane_b32 s30, v122, 3
	s_lshl_b32 s30, s30, 12
	s_add_u32 s28, s26, s30
	s_addc_u32 s29, s27, 0
	global_load_dwordx2 v[30:31], v162, s[28:29]
	v_readlane_b32 s30, v122, 4
	s_lshl_b32 s30, s30, 12
	s_add_u32 s28, s26, s30
	s_addc_u32 s29, s27, 0
	global_load_dwordx2 v[32:33], v162, s[28:29]
	v_readlane_b32 s30, v122, 5
	s_lshl_b32 s30, s30, 12
	s_add_u32 s28, s26, s30
	s_addc_u32 s29, s27, 0
	global_load_dwordx2 v[34:35], v162, s[28:29]
	v_readlane_b32 s30, v122, 6
	s_lshl_b32 s30, s30, 12
	s_add_u32 s28, s26, s30
	s_addc_u32 s29, s27, 0
	global_load_dwordx2 v[36:37], v162, s[28:29]
	v_readlane_b32 s30, v122, 7
	s_lshl_b32 s30, s30, 12
	s_add_u32 s28, s26, s30
	s_addc_u32 s29, s27, 0
	global_load_dwordx2 v[38:39], v162, s[28:29]
	v_readlane_b32 s30, v122, 8
	s_lshl_b32 s30, s30, 12
	s_add_u32 s28, s26, s30
	s_addc_u32 s29, s27, 0
	global_load_dwordx2 v[40:41], v162, s[28:29]
	v_readlane_b32 s30, v122, 9
	s_lshl_b32 s30, s30, 12
	s_add_u32 s28, s26, s30
	s_addc_u32 s29, s27, 0
	global_load_dwordx2 v[42:43], v162, s[28:29]
	v_readlane_b32 s30, v122, 10
	s_lshl_b32 s30, s30, 12
	s_add_u32 s28, s26, s30
	s_addc_u32 s29, s27, 0
	global_load_dwordx2 v[44:45], v162, s[28:29]
	v_readlane_b32 s30, v122, 11
	s_lshl_b32 s30, s30, 12
	s_add_u32 s28, s26, s30
	s_addc_u32 s29, s27, 0
	global_load_dwordx2 v[46:47], v162, s[28:29]
	v_readlane_b32 s30, v122, 12
	s_lshl_b32 s30, s30, 12
	s_add_u32 s28, s26, s30
	s_addc_u32 s29, s27, 0
	global_load_dwordx2 v[48:49], v162, s[28:29]
	v_readlane_b32 s30, v122, 13
	s_lshl_b32 s30, s30, 12
	s_add_u32 s28, s26, s30
	s_addc_u32 s29, s27, 0
	global_load_dwordx2 v[50:51], v162, s[28:29]
	v_readlane_b32 s30, v122, 14
	s_lshl_b32 s30, s30, 12
	s_add_u32 s28, s26, s30
	s_addc_u32 s29, s27, 0
	global_load_dwordx2 v[52:53], v162, s[28:29]
	v_readlane_b32 s30, v122, 15
	s_lshl_b32 s30, s30, 12
	s_add_u32 s28, s26, s30
	s_addc_u32 s29, s27, 0
	global_load_dwordx2 v[54:55], v162, s[28:29]
	v_readlane_b32 s30, v122, 16
	s_lshl_b32 s30, s30, 12
	s_add_u32 s28, s26, s30
	s_addc_u32 s29, s27, 0
	global_load_dwordx2 v[56:57], v162, s[28:29]
	v_readlane_b32 s30, v122, 17
	s_lshl_b32 s30, s30, 12
	s_add_u32 s28, s26, s30
	s_addc_u32 s29, s27, 0
	global_load_dwordx2 v[58:59], v162, s[28:29]
	v_readlane_b32 s30, v122, 18
	s_lshl_b32 s30, s30, 12
	s_add_u32 s28, s26, s30
	s_addc_u32 s29, s27, 0
	global_load_dwordx2 v[60:61], v162, s[28:29]
	v_readlane_b32 s30, v122, 19
	s_lshl_b32 s30, s30, 12
	s_add_u32 s28, s26, s30
	s_addc_u32 s29, s27, 0
	global_load_dwordx2 v[62:63], v162, s[28:29]
	v_readlane_b32 s30, v122, 20
	s_lshl_b32 s30, s30, 12
	s_add_u32 s28, s26, s30
	s_addc_u32 s29, s27, 0
	global_load_dwordx2 v[64:65], v162, s[28:29]
	v_readlane_b32 s30, v122, 21
	s_lshl_b32 s30, s30, 12
	s_add_u32 s28, s26, s30
	s_addc_u32 s29, s27, 0
	global_load_dwordx2 v[66:67], v162, s[28:29]
	v_readlane_b32 s30, v122, 22
	s_lshl_b32 s30, s30, 12
	s_add_u32 s28, s26, s30
	s_addc_u32 s29, s27, 0
	global_load_dwordx2 v[68:69], v162, s[28:29]
	v_readlane_b32 s30, v122, 23
	s_lshl_b32 s30, s30, 12
	s_add_u32 s28, s26, s30
	s_addc_u32 s29, s27, 0
	global_load_dwordx2 v[70:71], v162, s[28:29]
	v_readlane_b32 s30, v122, 24
	s_lshl_b32 s30, s30, 12
	s_add_u32 s28, s26, s30
	s_addc_u32 s29, s27, 0
	global_load_dwordx2 v[72:73], v162, s[28:29]
	v_readlane_b32 s30, v122, 25
	s_lshl_b32 s30, s30, 12
	s_add_u32 s28, s26, s30
	s_addc_u32 s29, s27, 0
	global_load_dwordx2 v[74:75], v162, s[28:29]
	v_readlane_b32 s30, v122, 26
	s_lshl_b32 s30, s30, 12
	s_add_u32 s28, s26, s30
	s_addc_u32 s29, s27, 0
	global_load_dwordx2 v[76:77], v162, s[28:29]
	v_readlane_b32 s30, v122, 27
	s_lshl_b32 s30, s30, 12
	s_add_u32 s28, s26, s30
	s_addc_u32 s29, s27, 0
	global_load_dwordx2 v[78:79], v162, s[28:29]
	v_readlane_b32 s30, v122, 28
	s_lshl_b32 s30, s30, 12
	s_add_u32 s28, s26, s30
	s_addc_u32 s29, s27, 0
	global_load_dwordx2 v[80:81], v162, s[28:29]
	v_readlane_b32 s30, v122, 29
	s_lshl_b32 s30, s30, 12
	s_add_u32 s28, s26, s30
	s_addc_u32 s29, s27, 0
	global_load_dwordx2 v[82:83], v162, s[28:29]
	v_readlane_b32 s30, v122, 30
	s_lshl_b32 s30, s30, 12
	s_add_u32 s28, s26, s30
	s_addc_u32 s29, s27, 0
	global_load_dwordx2 v[84:85], v162, s[28:29]
	v_readlane_b32 s30, v122, 31
	s_lshl_b32 s30, s30, 12
	s_add_u32 s28, s26, s30
	s_addc_u32 s29, s27, 0
	global_load_dwordx2 v[86:87], v162, s[28:29]
	v_permlane32_swap_b32_e32 v178, v194
	v_permlane32_swap_b32_e32 v179, v195
	v_permlane32_swap_b32_e32 v180, v196
	v_permlane32_swap_b32_e32 v181, v197
	v_permlane32_swap_b32_e32 v182, v198
	v_permlane32_swap_b32_e32 v183, v199
	v_permlane32_swap_b32_e32 v184, v200
	v_permlane32_swap_b32_e32 v185, v201
	v_permlane32_swap_b32_e32 v186, v202
	v_permlane32_swap_b32_e32 v187, v203
	v_permlane32_swap_b32_e32 v188, v204
	v_permlane32_swap_b32_e32 v189, v205
	v_permlane32_swap_b32_e32 v190, v206
	v_permlane32_swap_b32_e32 v191, v207
	v_permlane32_swap_b32_e32 v192, v208
	v_permlane32_swap_b32_e32 v193, v209
	v_add_f32_e32 v178, v178, v194
	v_add_f32_e32 v179, v179, v195
	v_add_f32_e32 v180, v180, v196
	v_add_f32_e32 v181, v181, v197
	v_add_f32_e32 v182, v182, v198
	v_add_f32_e32 v183, v183, v199
	v_add_f32_e32 v184, v184, v200
	v_add_f32_e32 v185, v185, v201
	v_add_f32_e32 v186, v186, v202
	v_add_f32_e32 v187, v187, v203
	v_add_f32_e32 v188, v188, v204
	v_add_f32_e32 v189, v189, v205
	v_add_f32_e32 v190, v190, v206
	v_add_f32_e32 v191, v191, v207
	v_add_f32_e32 v192, v192, v208
	v_add_f32_e32 v193, v193, v209
	v_permlane16_swap_b32_e32 v178, v186
	v_permlane16_swap_b32_e32 v179, v187
	v_permlane16_swap_b32_e32 v180, v188
	v_permlane16_swap_b32_e32 v181, v189
	v_permlane16_swap_b32_e32 v182, v190
	v_permlane16_swap_b32_e32 v183, v191
	v_permlane16_swap_b32_e32 v184, v192
	v_permlane16_swap_b32_e32 v185, v193
	v_add_f32_e32 v178, v178, v186
	v_add_f32_e32 v179, v179, v187
	v_add_f32_e32 v180, v180, v188
	v_add_f32_e32 v181, v181, v189
	v_add_f32_e32 v182, v182, v190
	v_add_f32_e32 v183, v183, v191
	v_add_f32_e32 v184, v184, v192
	v_add_f32_e32 v185, v185, v193
	v_cndmask_b32_e64 v2, v178, v182, s[8:9]
	v_cndmask_b32_e64 v3, v179, v183, s[8:9]
	v_cndmask_b32_e64 v4, v180, v184, s[8:9]
	v_cndmask_b32_e64 v5, v181, v185, s[8:9]
	v_cndmask_b32_e64 v6, v182, v178, s[8:9]
	v_cndmask_b32_e64 v7, v183, v179, s[8:9]
	v_cndmask_b32_e64 v8, v184, v180, s[8:9]
	v_cndmask_b32_e64 v9, v185, v181, s[8:9]
	v_add_f32_dpp v6, v2, v6 row_ror:8 row_mask:0xf bank_mask:0xf
	v_add_f32_dpp v7, v3, v7 row_ror:8 row_mask:0xf bank_mask:0xf
	v_add_f32_dpp v8, v4, v8 row_ror:8 row_mask:0xf bank_mask:0xf
	v_add_f32_dpp v9, v5, v9 row_ror:8 row_mask:0xf bank_mask:0xf
	v_cndmask_b32_e64 v2, v6, v8, s[10:11]
	v_cndmask_b32_e64 v3, v7, v9, s[10:11]
	v_cndmask_b32_e64 v4, v8, v6, s[10:11]
	v_cndmask_b32_e64 v5, v9, v7, s[10:11]
	v_add_f32_dpp v4, v2, v4 row_half_mirror row_mask:0xf bank_mask:0xf
	v_add_f32_dpp v5, v3, v5 row_half_mirror row_mask:0xf bank_mask:0xf
	v_cndmask_b32_e64 v2, v4, v5, s[14:15]
	v_cndmask_b32_e64 v3, v5, v4, s[14:15]
	s_nop 0
	v_add_f32_dpp v3, v2, v3 quad_perm:[2,3,0,1] row_mask:0xf bank_mask:0xf
	s_nop 1
	v_add_f32_dpp v11, v3, v3 quad_perm:[1,0,3,2] row_mask:0xf bank_mask:0xf
	s_mov_b64 exec, s[2:3]
	global_store_dword v[22:23], v11, off offset:384
	s_mov_b64 exec, -1
	s_add_i32 s16, s16, 1
	s_cmp_lt_i32 s16, s17
	s_cbranch_scc1 .Lpa_tok
	s_waitcnt vmcnt(0)
	s_waitcnt vmcnt(0)
	v_cmp_eq_u32_e32 vcc, 0, v0
	s_waitcnt vmcnt(0) lgkmcnt(0)
	s_barrier
	s_and_saveexec_b64 s[2:3], vcc
	s_cbranch_execz .Lgbb_1444
	v_readlane_b32 s4, v237, 5
	s_waitcnt vmcnt(0) expcnt(0) lgkmcnt(0)
	s_nop 0
	v_mov_b32_e32 v1, s4
	ds_read_b32 v3, v1
	ds_read_b32 v1, v1 offset:4
	s_waitcnt lgkmcnt(1)
	v_cmp_ne_u32_e32 vcc, 0, v3
	s_branch .Lgbb_1412
	v_readlane_b32 s4, v237, 2
	v_readlane_b32 s5, v237, 3
	s_load_dwordx2 s[8:9], s[6:7], 0x4
	s_lshl_b64 s[4:5], s[4:5], 2
	v_readlane_b32 s6, v237, 0
	s_add_u32 s4, s6, s4
	v_readlane_b32 s6, v237, 1
	s_addc_u32 s5, s6, s5
	s_add_u32 s6, s4, 0x1000
	s_addc_u32 s7, s5, 0
	s_waitcnt lgkmcnt(0)
	s_mul_i32 s20, s8, s38
	s_add_u32 s8, s4, 0x1100
	s_mul_i32 s20, s20, s9
	s_addc_u32 s9, s5, 0
	s_add_u32 s10, s4, 0x1200
	s_addc_u32 s11, s5, 0
	s_add_u32 s12, s4, 0x1300
	s_addc_u32 s13, s5, 0
	s_mov_b32 s21, 1
	v_mov_b32_e32 v17, 0
	s_branch .Lgbb_1400

.Lgbb_1444:
	s_or_b64 exec, exec, s[2:3]
	s_waitcnt lgkmcnt(0)
	s_barrier
	s_mov_b64 exec, -1
	v_and_b32_e32 v1, 63, v0
	v_readfirstlane_b32 s16, v0
	s_load_dwordx2 s[12:13], s[0:1], 0xc0
	s_lshr_b32 s16, s16, 6
	s_and_b32 s18, s33, 7
	s_lshr_b32 s19, s33, 3
	s_lshl_b32 s19, s19, 8
	s_lshl_b32 s16, s16, 5
	s_add_i32 s16, s16, s19
	s_add_i32 s17, s16, 32
	s_add_i32 s24, s17, -1
	s_lshl_b32 s19, s18, 9
	v_lshl_add_u32 v162, v1, 3, s19
	v_mov_b32_e32 v163, 0
	s_mov_b32 s31, 0
	v_mov_b32_e32 v4, v1
	v_mov_b32_e32 v5, 0
	s_mov_b32 s69, 0
	s_mov_b32 s68, 0x400000
	s_mov_b32 s41, 0x378e98ab
	s_mov_b32 s42, 0x3b7cd369
	s_mov_b32 s43, 0xbcc618b2
	s_mov_b32 s44, 0x3dda74e4
	s_mov_b32 s45, 0x3f228afd
	s_mov_b32 s46, 0x3e03c728
	s_mov_b32 s47, 0xbfb8aa3b
	s_mov_b32 s48, 0x42ce8ed0
	s_mov_b32 s49, 0xc2b17218
	s_mov_b32 s50, 0x7fffffff
	v_mov_b32_e32 v97, 0x43000000
	v_mov_b32_e32 v172, 0x3ba10414
	v_mov_b32_e32 v175, 0xb9c68948
	v_mov_b32_e32 v176, 0x7f800000
	s_load_dwordx2 s[4:5], s[0:1], 0xb8
	s_waitcnt lgkmcnt(0)
	s_add_u32 s26, s12, 0x17c00000
	s_addc_u32 s27, s13, 0
	s_add_u32 s20, s12, 0x100000
	s_addc_u32 s21, s13, 0
	v_lshl_add_u64 v[172:173], v[162:163], 1, s[20:21]
	s_add_u32 s20, s12, 0x4da00000
	s_addc_u32 s21, s13, 0
	v_lshl_add_u64 v[174:175], v[4:5], 2, s[20:21]
	s_add_u32 s20, s12, 0x4de00000
	s_addc_u32 s21, s13, 0
	v_lshl_add_u64 v[176:177], v[4:5], 2, s[20:21]
	s_add_u32 s20, s12, 0x23c00000
	s_addc_u32 s21, s13, 0
	v_lshl_add_u64 v[210:211], v[4:5], 2, s[20:21]
	s_add_u32 s20, s12, 0x25c00000
	s_addc_u32 s21, s13, 0
	v_and_b32_e32 v6, 7, v1
	v_mov_b32_e32 v7, 0
	v_lshl_add_u64 v[212:213], v[6:7], 2, s[20:21]
	v_lshl_add_u64 v[214:215], v[162:163], 2, s[4:5]
	s_add_u32 s66, s12, 0x1fe00000
	s_addc_u32 s67, s13, 0
	s_add_u32 s64, s12, 0x38d80000
	s_addc_u32 s65, s13, 0
	s_add_u32 s60, s12, 0x38d90000
	s_addc_u32 s61, s13, 0
	s_lshl_b32 s19, s18, 2
	s_add_u32 s62, s12, 0x25d00000
	s_addc_u32 s63, s13, 0
	s_add_u32 s62, s62, s19
	s_addc_u32 s63, s63, 0
	v_mov_b32_e32 v19, 0
	s_lshl_b32 s30, s16, 13
	v_lshl_add_u64 v[160:161], v[172:173], 0, s[30:31]
	global_load_dwordx4 v[116:119], v[160:161], off
	s_lshl_b32 s30, s16, 9
	v_lshl_add_u64 v[160:161], v[174:175], 0, s[30:31]
	global_load_dword v122, v[160:161], off
	global_load_dword v123, v[160:161], off offset:256
	v_lshl_add_u64 v[160:161], v[176:177], 0, s[30:31]
	global_load_dword v216, v[160:161], off
	global_load_dword v217, v[160:161], off offset:256
	v_lshl_add_u64 v[160:161], v[210:211], 0, s[30:31]
	global_load_dword v218, v[160:161], off
	global_load_dword v226, v[160:161], off offset:256
	v_lshl_add_u64 v[160:161], v[160:161], 0, s[68:69]
	global_load_dword v219, v[160:161], off
	global_load_dword v227, v[160:161], off offset:256
	v_lshl_add_u64 v[160:161], v[160:161], 0, s[68:69]
	global_load_dword v220, v[160:161], off
	global_load_dword v228, v[160:161], off offset:256
	v_lshl_add_u64 v[160:161], v[160:161], 0, s[68:69]
	global_load_dword v221, v[160:161], off
	global_load_dword v229, v[160:161], off offset:256
	v_lshl_add_u64 v[160:161], v[160:161], 0, s[68:69]
	global_load_dword v222, v[160:161], off
	global_load_dword v230, v[160:161], off offset:256
	v_lshl_add_u64 v[160:161], v[160:161], 0, s[68:69]
	global_load_dword v223, v[160:161], off
	global_load_dword v231, v[160:161], off offset:256
	v_lshl_add_u64 v[160:161], v[160:161], 0, s[68:69]
	global_load_dword v224, v[160:161], off
	global_load_dword v232, v[160:161], off offset:256
	v_lshl_add_u64 v[160:161], v[160:161], 0, s[68:69]
	global_load_dword v225, v[160:161], off
	global_load_dword v233, v[160:161], off offset:256
	s_lshl_b32 s30, s16, 5
	v_lshl_add_u64 v[160:161], v[212:213], 0, s[30:31]
	global_load_dword v234, v[160:161], off
	s_lshl_b32 s30, s16, 2
	s_add_u32 s28, s66, s30
	s_addc_u32 s29, s67, 0
	global_load_dword v235, v19, s[28:29]
	s_waitcnt vmcnt(0)
	v_lshlrev_b32_e32 v16, 2, v122
	v_lshlrev_b32_e32 v17, 2, v123
	global_load_dword v238, v16, s[64:65]
	global_load_dword v240, v16, s[60:61]
	global_load_dword v239, v17, s[64:65]
	global_load_dword v241, v17, s[60:61]
	s_waitcnt vmcnt(0)
	v_readlane_b32 s30, v122, 0
	s_lshl_b32 s30, s30, 12
	s_add_u32 s28, s26, s30
	s_addc_u32 s29, s27, 0
	global_load_dwordx2 v[24:25], v162, s[28:29]
	v_readlane_b32 s30, v122, 1
	s_lshl_b32 s30, s30, 12
	s_add_u32 s28, s26, s30
	s_addc_u32 s29, s27, 0
	global_load_dwordx2 v[26:27], v162, s[28:29]
	v_readlane_b32 s30, v122, 2
	s_lshl_b32 s30, s30, 12
	s_add_u32 s28, s26, s30
	s_addc_u32 s29, s27, 0
	global_load_dwordx2 v[28:29], v162, s[28:29]
	v_readlane_b32 s30, v122, 3
	s_lshl_b32 s30, s30, 12
	s_add_u32 s28, s26, s30
	s_addc_u32 s29, s27, 0
	global_load_dwordx2 v[30:31], v162, s[28:29]
	v_readlane_b32 s30, v122, 4
	s_lshl_b32 s30, s30, 12
	s_add_u32 s28, s26, s30
	s_addc_u32 s29, s27, 0
	global_load_dwordx2 v[32:33], v162, s[28:29]
	v_readlane_b32 s30, v122, 5
	s_lshl_b32 s30, s30, 12
	s_add_u32 s28, s26, s30
	s_addc_u32 s29, s27, 0
	global_load_dwordx2 v[34:35], v162, s[28:29]
	v_readlane_b32 s30, v122, 6
	s_lshl_b32 s30, s30, 12
	s_add_u32 s28, s26, s30
	s_addc_u32 s29, s27, 0
	global_load_dwordx2 v[36:37], v162, s[28:29]
	v_readlane_b32 s30, v122, 7
	s_lshl_b32 s30, s30, 12
	s_add_u32 s28, s26, s30
	s_addc_u32 s29, s27, 0
	global_load_dwordx2 v[38:39], v162, s[28:29]
	v_readlane_b32 s30, v122, 8
	s_lshl_b32 s30, s30, 12
	s_add_u32 s28, s26, s30
	s_addc_u32 s29, s27, 0
	global_load_dwordx2 v[40:41], v162, s[28:29]
	v_readlane_b32 s30, v122, 9
	s_lshl_b32 s30, s30, 12
	s_add_u32 s28, s26, s30
	s_addc_u32 s29, s27, 0
	global_load_dwordx2 v[42:43], v162, s[28:29]
	v_readlane_b32 s30, v122, 10
	s_lshl_b32 s30, s30, 12
	s_add_u32 s28, s26, s30
	s_addc_u32 s29, s27, 0
	global_load_dwordx2 v[44:45], v162, s[28:29]
	v_readlane_b32 s30, v122, 11
	s_lshl_b32 s30, s30, 12
	s_add_u32 s28, s26, s30
	s_addc_u32 s29, s27, 0
	global_load_dwordx2 v[46:47], v162, s[28:29]
	v_readlane_b32 s30, v122, 12
	s_lshl_b32 s30, s30, 12
	s_add_u32 s28, s26, s30
	s_addc_u32 s29, s27, 0
	global_load_dwordx2 v[48:49], v162, s[28:29]
	v_readlane_b32 s30, v122, 13
	s_lshl_b32 s30, s30, 12
	s_add_u32 s28, s26, s30
	s_addc_u32 s29, s27, 0
	global_load_dwordx2 v[50:51], v162, s[28:29]
	v_readlane_b32 s30, v122, 14
	s_lshl_b32 s30, s30, 12
	s_add_u32 s28, s26, s30
	s_addc_u32 s29, s27, 0
	global_load_dwordx2 v[52:53], v162, s[28:29]
	v_readlane_b32 s30, v122, 15
	s_lshl_b32 s30, s30, 12
	s_add_u32 s28, s26, s30
	s_addc_u32 s29, s27, 0
	global_load_dwordx2 v[54:55], v162, s[28:29]
	v_readlane_b32 s30, v122, 16
	s_lshl_b32 s30, s30, 12
	s_add_u32 s28, s26, s30
	s_addc_u32 s29, s27, 0
	global_load_dwordx2 v[56:57], v162, s[28:29]
	v_readlane_b32 s30, v122, 17
	s_lshl_b32 s30, s30, 12
	s_add_u32 s28, s26, s30
	s_addc_u32 s29, s27, 0
	global_load_dwordx2 v[58:59], v162, s[28:29]
	v_readlane_b32 s30, v122, 18
	s_lshl_b32 s30, s30, 12
	s_add_u32 s28, s26, s30
	s_addc_u32 s29, s27, 0
	global_load_dwordx2 v[60:61], v162, s[28:29]
	v_readlane_b32 s30, v122, 19
	s_lshl_b32 s30, s30, 12
	s_add_u32 s28, s26, s30
	s_addc_u32 s29, s27, 0
	global_load_dwordx2 v[62:63], v162, s[28:29]
	v_readlane_b32 s30, v122, 20
	s_lshl_b32 s30, s30, 12
	s_add_u32 s28, s26, s30
	s_addc_u32 s29, s27, 0
	global_load_dwordx2 v[64:65], v162, s[28:29]
	v_readlane_b32 s30, v122, 21
	s_lshl_b32 s30, s30, 12
	s_add_u32 s28, s26, s30
	s_addc_u32 s29, s27, 0
	global_load_dwordx2 v[66:67], v162, s[28:29]
	v_readlane_b32 s30, v122, 22
	s_lshl_b32 s30, s30, 12
	s_add_u32 s28, s26, s30
	s_addc_u32 s29, s27, 0
	global_load_dwordx2 v[68:69], v162, s[28:29]
	v_readlane_b32 s30, v122, 23
	s_lshl_b32 s30, s30, 12
	s_add_u32 s28, s26, s30
	s_addc_u32 s29, s27, 0
	global_load_dwordx2 v[70:71], v162, s[28:29]
	v_readlane_b32 s30, v122, 24
	s_lshl_b32 s30, s30, 12
	s_add_u32 s28, s26, s30
	s_addc_u32 s29, s27, 0
	global_load_dwordx2 v[72:73], v162, s[28:29]
	v_readlane_b32 s30, v122, 25
	s_lshl_b32 s30, s30, 12
	s_add_u32 s28, s26, s30
	s_addc_u32 s29, s27, 0
	global_load_dwordx2 v[74:75], v162, s[28:29]
	v_readlane_b32 s30, v122, 26
	s_lshl_b32 s30, s30, 12
	s_add_u32 s28, s26, s30
	s_addc_u32 s29, s27, 0
	global_load_dwordx2 v[76:77], v162, s[28:29]
	v_readlane_b32 s30, v122, 27
	s_lshl_b32 s30, s30, 12
	s_add_u32 s28, s26, s30
	s_addc_u32 s29, s27, 0
	global_load_dwordx2 v[78:79], v162, s[28:29]
	v_readlane_b32 s30, v122, 28
	s_lshl_b32 s30, s30, 12
	s_add_u32 s28, s26, s30
	s_addc_u32 s29, s27, 0
	global_load_dwordx2 v[80:81], v162, s[28:29]
	v_readlane_b32 s30, v122, 29
	s_lshl_b32 s30, s30, 12
	s_add_u32 s28, s26, s30
	s_addc_u32 s29, s27, 0
	global_load_dwordx2 v[82:83], v162, s[28:29]
	v_readlane_b32 s30, v122, 30
	s_lshl_b32 s30, s30, 12
	s_add_u32 s28, s26, s30
	s_addc_u32 s29, s27, 0
	global_load_dwordx2 v[84:85], v162, s[28:29]
	v_readlane_b32 s30, v122, 31
	s_lshl_b32 s30, s30, 12
	s_add_u32 s28, s26, s30
	s_addc_u32 s29, s27, 0
	global_load_dwordx2 v[86:87], v162, s[28:29]
.Lpb_tok:
	v_mov_b32_e32 v99, v234
	s_nop 1
	v_add_f32_dpp v16, v99, v99 quad_perm:[1,0,3,2] row_mask:0xf bank_mask:0xf
	s_nop 1
	v_add_f32_dpp v99, v16, v16 quad_perm:[2,3,0,1] row_mask:0xf bank_mask:0xf
	s_nop 1
	v_add_f32_dpp v99, v99, v99 row_half_mirror row_mask:0xf bank_mask:0xf
	v_mov_b32_e32 v98, v235
	v_mul_f32_e32 v15, v99, v97
	v_add_f32_e32 v10, v218, v219
	v_add_f32_e32 v12, v220, v221
	v_add_f32_e32 v13, v222, v223
	v_add_f32_e32 v14, v224, v225
	v_add_f32_e32 v10, v10, v12
	v_add_f32_e32 v13, v13, v14
	v_add_f32_e32 v11, v10, v13
	v_mov_b32_e32 v96, v238
	v_mov_b32_e32 v249, v240
	v_mov_b32_e32 v164, v216
	v_mul_f32_e32 v12, v98, v96
	v_mul_f32_e32 v13, v99, v97
	v_sub_f32_e32 v10, v11, v13
	v_mul_f32_e32 v10, v12, v10
	v_mul_f32_e32 v11, 0x3f3504f3, v10
	v_cmp_nlt_f32_e64 s[34:35], |v11|, 1.0
	s_and_saveexec_b64 s[52:53], s[34:35]
	s_xor_b64 s[34:35], exec, s[52:53]
	s_cbranch_execz .Lerfa0_1476
	v_fma_f32 v12, |v11|, s41, v175
	v_fma_f32 v12, |v11|, v12, s42
	v_fma_f32 v12, |v11|, v12, s43
	v_fma_f32 v12, |v11|, v12, s44
	v_fma_f32 v12, |v11|, v12, s45
	v_fma_f32 v12, |v11|, v12, s46
	v_fma_f32 v12, |v11|, v12, |v11|
	v_mul_f32_e32 v13, 0xbfb8aa3b, v12
	v_fma_f32 v14, v12, s47, -v13
	v_rndne_f32_e32 v15, v13
	v_fmac_f32_e32 v14, 0xb2a5705f, v12
	v_sub_f32_e32 v13, v13, v15
	v_add_f32_e32 v13, v13, v14
	v_cvt_i32_f32_e32 v14, v15
	v_exp_f32_e32 v13, v13
	v_cmp_nlt_f32_e32 vcc, s48, v12
	v_ldexp_f32 v13, v13, v14
	s_nop 0
	v_cndmask_b32_e32 v13, 0, v13, vcc
	v_cmp_ngt_f32_e32 vcc, s49, v12
	s_nop 1
	v_cndmask_b32_e32 v12, v176, v13, vcc
	v_sub_f32_e32 v12, 1.0, v12
.Lerfa0_1476:
	s_andn2_saveexec_b64 s[34:35], s[34:35]
	v_mul_f32_e32 v12, v11, v11
	v_fmamk_f32 v13, v12, 0xba1345e1, v172
	v_fmaak_f32 v13, v12, v13, 0xbcdac9b8
	v_fmaak_f32 v13, v12, v13, 0x3de703be
	v_fmaak_f32 v13, v12, v13, 0xbec09330
	v_fmaak_f32 v12, v12, v13, 0x3e0375d0
	v_fma_f32 v12, |v11|, v12, |v11|
	s_or_b64 exec, exec, s[34:35]
	v_bfi_b32 v11, s50, v12, v11
	v_mul_f32_e32 v10, 0.5, v10
	v_add_f32_e32 v11, 1.0, v11
	v_mul_f32_e32 v10, v10, v11
	v_mul_f32_e32 v10, v164, v10
	v_mul_f32_e32 v10, v249, v10
	v_mov_b32_e32 v246, v10
	v_add_f32_e32 v10, v226, v227
	v_add_f32_e32 v12, v228, v229
	v_add_f32_e32 v13, v230, v231
	v_add_f32_e32 v14, v232, v233
	v_add_f32_e32 v10, v10, v12
	v_add_f32_e32 v13, v13, v14
	v_add_f32_e32 v11, v10, v13
	v_mov_b32_e32 v96, v239
	v_mov_b32_e32 v249, v241
	v_mov_b32_e32 v164, v217
	v_mul_f32_e32 v12, v98, v96
	v_mul_f32_e32 v13, v99, v97
	v_sub_f32_e32 v10, v11, v13
	v_mul_f32_e32 v10, v12, v10
	v_mul_f32_e32 v11, 0x3f3504f3, v10
	v_cmp_nlt_f32_e64 s[34:35], |v11|, 1.0
	s_and_saveexec_b64 s[52:53], s[34:35]
	s_xor_b64 s[34:35], exec, s[52:53]
	s_cbranch_execz .Lerfa1_1476
	v_fma_f32 v12, |v11|, s41, v175
	v_fma_f32 v12, |v11|, v12, s42
	v_fma_f32 v12, |v11|, v12, s43
	v_fma_f32 v12, |v11|, v12, s44
	v_fma_f32 v12, |v11|, v12, s45
	v_fma_f32 v12, |v11|, v12, s46
	v_fma_f32 v12, |v11|, v12, |v11|
	v_mul_f32_e32 v13, 0xbfb8aa3b, v12
	v_fma_f32 v14, v12, s47, -v13
	v_rndne_f32_e32 v15, v13
	v_fmac_f32_e32 v14, 0xb2a5705f, v12
	v_sub_f32_e32 v13, v13, v15
	v_add_f32_e32 v13, v13, v14
	v_cvt_i32_f32_e32 v14, v15
	v_exp_f32_e32 v13, v13
	v_cmp_nlt_f32_e32 vcc, s48, v12
	v_ldexp_f32 v13, v13, v14
	s_nop 0
	v_cndmask_b32_e32 v13, 0, v13, vcc
	v_cmp_ngt_f32_e32 vcc, s49, v12
	s_nop 1
	v_cndmask_b32_e32 v12, v176, v13, vcc
	v_sub_f32_e32 v12, 1.0, v12
.Lerfa1_1476:
	s_andn2_saveexec_b64 s[34:35], s[34:35]
	v_mul_f32_e32 v12, v11, v11
	v_fmamk_f32 v13, v12, 0xba1345e1, v172
	v_fmaak_f32 v13, v12, v13, 0xbcdac9b8
	v_fmaak_f32 v13, v12, v13, 0x3de703be
	v_fmaak_f32 v13, v12, v13, 0xbec09330
	v_fmaak_f32 v12, v12, v13, 0x3e0375d0
	v_fma_f32 v12, |v11|, v12, |v11|
	s_or_b64 exec, exec, s[34:35]
	v_bfi_b32 v11, s50, v12, v11
	v_mul_f32_e32 v10, 0.5, v10
	v_add_f32_e32 v11, 1.0, v11
	v_mul_f32_e32 v10, v10, v11
	v_mul_f32_e32 v10, v164, v10
	v_mul_f32_e32 v10, v249, v10
	v_mov_b32_e32 v247, v10
	v_add_f32_e32 v16, v246, v247
	s_nop 1
	v_add_f32_dpp v17, v16, v16 quad_perm:[1,0,3,2] row_mask:0xf bank_mask:0xf
	s_nop 1
	v_add_f32_dpp v16, v17, v17 quad_perm:[2,3,0,1] row_mask:0xf bank_mask:0xf
	s_nop 1
	v_add_f32_dpp v17, v16, v16 row_half_mirror row_mask:0xf bank_mask:0xf
	s_nop 1
	v_add_f32_dpp v16, v17, v17 row_ror:8 row_mask:0xf bank_mask:0xf
	v_mov_b32_e32 v17, v16
	s_nop 1
	v_permlane16_swap_b32_e32 v16, v17
	v_add_f32_e32 v16, v16, v17
	v_mov_b32_e32 v17, v16
	s_nop 1
	v_permlane32_swap_b32_e32 v16, v17
	v_add_f32_e32 v16, v16, v17
	v_mul_f32_e32 v248, 0xc3000000, v16
	v_mov_b32_e32 v242, v116
	v_mov_b32_e32 v243, v117
	v_mov_b32_e32 v244, v118
	v_mov_b32_e32 v245, v119
	v_mov_b32_e32 v120, v122
	v_mov_b32_e32 v121, v123
	s_lshl_b32 s30, s16, 14
	v_lshl_add_u64 v[20:21], v[214:215], 0, s[30:31]
	s_add_i32 s18, s16, 1
	s_min_i32 s18, s18, s24
	s_lshl_b32 s30, s18, 13
	v_lshl_add_u64 v[160:161], v[172:173], 0, s[30:31]
	global_load_dwordx4 v[116:119], v[160:161], off
	s_lshl_b32 s30, s18, 9
	v_lshl_add_u64 v[160:161], v[174:175], 0, s[30:31]
	global_load_dword v122, v[160:161], off
	global_load_dword v123, v[160:161], off offset:256
	v_lshl_add_u64 v[160:161], v[176:177], 0, s[30:31]
	global_load_dword v216, v[160:161], off
	global_load_dword v217, v[160:161], off offset:256
	v_lshl_add_u64 v[160:161], v[210:211], 0, s[30:31]
	global_load_dword v218, v[160:161], off
	global_load_dword v226, v[160:161], off offset:256
	v_lshl_add_u64 v[160:161], v[160:161], 0, s[68:69]
	global_load_dword v219, v[160:161], off
	global_load_dword v227, v[160:161], off offset:256
	v_lshl_add_u64 v[160:161], v[160:161], 0, s[68:69]
	global_load_dword v220, v[160:161], off
	global_load_dword v228, v[160:161], off offset:256
	v_lshl_add_u64 v[160:161], v[160:161], 0, s[68:69]
	global_load_dword v221, v[160:161], off
	global_load_dword v229, v[160:161], off offset:256
	v_lshl_add_u64 v[160:161], v[160:161], 0, s[68:69]
	global_load_dword v222, v[160:161], off
	global_load_dword v230, v[160:161], off offset:256
	v_lshl_add_u64 v[160:161], v[160:161], 0, s[68:69]
	global_load_dword v223, v[160:161], off
	global_load_dword v231, v[160:161], off offset:256
	v_lshl_add_u64 v[160:161], v[160:161], 0, s[68:69]
	global_load_dword v224, v[160:161], off
	global_load_dword v232, v[160:161], off offset:256
	v_lshl_add_u64 v[160:161], v[160:161], 0, s[68:69]
	global_load_dword v225, v[160:161], off
	global_load_dword v233, v[160:161], off offset:256
	s_lshl_b32 s30, s18, 5
	v_lshl_add_u64 v[160:161], v[212:213], 0, s[30:31]
	global_load_dword v234, v[160:161], off
	s_lshl_b32 s30, s18, 2
	s_add_u32 s28, s66, s30
	s_addc_u32 s29, s67, 0
	global_load_dword v235, v19, s[28:29]
	v_mov_b32_e32 v178, 0
	v_mov_b32_e32 v179, 0
	v_mov_b32_e32 v180, 0
	v_mov_b32_e32 v181, 0
	v_mov_b32_e32 v182, 0
	v_mov_b32_e32 v183, 0
	v_mov_b32_e32 v184, 0
	v_mov_b32_e32 v185, 0
	s_waitcnt vmcnt(54)
	v_readlane_b32 s25, v246, 0
	v_cvt_f32_ubyte0_e32 v124, v24
	v_cvt_f32_ubyte1_e32 v125, v24
	v_cvt_f32_ubyte2_e32 v126, v24
	v_cvt_f32_ubyte3_e32 v127, v24
	v_cvt_f32_ubyte0_e32 v128, v25
	v_cvt_f32_ubyte1_e32 v129, v25
	v_cvt_f32_ubyte2_e32 v130, v25
	v_cvt_f32_ubyte3_e32 v131, v25
	v_readlane_b32 s30, v120, 32
	s_lshl_b32 s30, s30, 12
	s_add_u32 s28, s26, s30
	s_addc_u32 s29, s27, 0
	global_load_dwordx2 v[24:25], v162, s[28:29]
	v_fmac_f32_e32 v178, s25, v124
	v_fmac_f32_e32 v179, s25, v125
	v_fmac_f32_e32 v180, s25, v126
	v_fmac_f32_e32 v181, s25, v127
	v_fmac_f32_e32 v182, s25, v128
	v_fmac_f32_e32 v183, s25, v129
	v_fmac_f32_e32 v184, s25, v130
	v_fmac_f32_e32 v185, s25, v131
	s_waitcnt vmcnt(54)
	v_readlane_b32 s25, v246, 1
	v_cvt_f32_ubyte0_e32 v132, v26
	v_cvt_f32_ubyte1_e32 v133, v26
	v_cvt_f32_ubyte2_e32 v134, v26
	v_cvt_f32_ubyte3_e32 v135, v26
	v_cvt_f32_ubyte0_e32 v136, v27
	v_cvt_f32_ubyte1_e32 v137, v27
	v_cvt_f32_ubyte2_e32 v138, v27
	v_cvt_f32_ubyte3_e32 v139, v27
	v_readlane_b32 s30, v120, 33
	s_lshl_b32 s30, s30, 12
	s_add_u32 s28, s26, s30
	s_addc_u32 s29, s27, 0
	global_load_dwordx2 v[26:27], v162, s[28:29]
	v_fmac_f32_e32 v178, s25, v132
	v_fmac_f32_e32 v179, s25, v133
	v_fmac_f32_e32 v180, s25, v134
	v_fmac_f32_e32 v181, s25, v135
	v_fmac_f32_e32 v182, s25, v136
	v_fmac_f32_e32 v183, s25, v137
	v_fmac_f32_e32 v184, s25, v138
	v_fmac_f32_e32 v185, s25, v139
	s_waitcnt vmcnt(54)
	v_readlane_b32 s25, v246, 2
	v_cvt_f32_ubyte0_e32 v124, v28
	v_cvt_f32_ubyte1_e32 v125, v28
	v_cvt_f32_ubyte2_e32 v126, v28
	v_cvt_f32_ubyte3_e32 v127, v28
	v_cvt_f32_ubyte0_e32 v128, v29
	v_cvt_f32_ubyte1_e32 v129, v29
	v_cvt_f32_ubyte2_e32 v130, v29
	v_cvt_f32_ubyte3_e32 v131, v29
	v_readlane_b32 s30, v120, 34
	s_lshl_b32 s30, s30, 12
	s_add_u32 s28, s26, s30
	s_addc_u32 s29, s27, 0
	global_load_dwordx2 v[28:29], v162, s[28:29]
	v_fmac_f32_e32 v178, s25, v124
	v_fmac_f32_e32 v179, s25, v125
	v_fmac_f32_e32 v180, s25, v126
	v_fmac_f32_e32 v181, s25, v127
	v_fmac_f32_e32 v182, s25, v128
	v_fmac_f32_e32 v183, s25, v129
	v_fmac_f32_e32 v184, s25, v130
	v_fmac_f32_e32 v185, s25, v131
	s_waitcnt vmcnt(54)
	v_readlane_b32 s25, v246, 3
	v_cvt_f32_ubyte0_e32 v132, v30
	v_cvt_f32_ubyte1_e32 v133, v30
	v_cvt_f32_ubyte2_e32 v134, v30
	v_cvt_f32_ubyte3_e32 v135, v30
	v_cvt_f32_ubyte0_e32 v136, v31
	v_cvt_f32_ubyte1_e32 v137, v31
	v_cvt_f32_ubyte2_e32 v138, v31
	v_cvt_f32_ubyte3_e32 v139, v31
	v_readlane_b32 s30, v120, 35
	s_lshl_b32 s30, s30, 12
	s_add_u32 s28, s26, s30
	s_addc_u32 s29, s27, 0
	global_load_dwordx2 v[30:31], v162, s[28:29]
	v_fmac_f32_e32 v178, s25, v132
	v_fmac_f32_e32 v179, s25, v133
	v_fmac_f32_e32 v180, s25, v134
	v_fmac_f32_e32 v181, s25, v135
	v_fmac_f32_e32 v182, s25, v136
	v_fmac_f32_e32 v183, s25, v137
	v_fmac_f32_e32 v184, s25, v138
	v_fmac_f32_e32 v185, s25, v139
	s_waitcnt vmcnt(54)
	v_readlane_b32 s25, v246, 4
	v_cvt_f32_ubyte0_e32 v124, v32
	v_cvt_f32_ubyte1_e32 v125, v32
	v_cvt_f32_ubyte2_e32 v126, v32
	v_cvt_f32_ubyte3_e32 v127, v32
	v_cvt_f32_ubyte0_e32 v128, v33
	v_cvt_f32_ubyte1_e32 v129, v33
	v_cvt_f32_ubyte2_e32 v130, v33
	v_cvt_f32_ubyte3_e32 v131, v33
	v_readlane_b32 s30, v120, 36
	s_lshl_b32 s30, s30, 12
	s_add_u32 s28, s26, s30
	s_addc_u32 s29, s27, 0
	global_load_dwordx2 v[32:33], v162, s[28:29]
	v_fmac_f32_e32 v178, s25, v124
	v_fmac_f32_e32 v179, s25, v125
	v_fmac_f32_e32 v180, s25, v126
	v_fmac_f32_e32 v181, s25, v127
	v_fmac_f32_e32 v182, s25, v128
	v_fmac_f32_e32 v183, s25, v129
	v_fmac_f32_e32 v184, s25, v130
	v_fmac_f32_e32 v185, s25, v131
	s_waitcnt vmcnt(54)
	v_readlane_b32 s25, v246, 5
	v_cvt_f32_ubyte0_e32 v132, v34
	v_cvt_f32_ubyte1_e32 v133, v34
	v_cvt_f32_ubyte2_e32 v134, v34
	v_cvt_f32_ubyte3_e32 v135, v34
	v_cvt_f32_ubyte0_e32 v136, v35
	v_cvt_f32_ubyte1_e32 v137, v35
	v_cvt_f32_ubyte2_e32 v138, v35
	v_cvt_f32_ubyte3_e32 v139, v35
	v_readlane_b32 s30, v120, 37
	s_lshl_b32 s30, s30, 12
	s_add_u32 s28, s26, s30
	s_addc_u32 s29, s27, 0
	global_load_dwordx2 v[34:35], v162, s[28:29]
	v_fmac_f32_e32 v178, s25, v132
	v_fmac_f32_e32 v179, s25, v133
	v_fmac_f32_e32 v180, s25, v134
	v_fmac_f32_e32 v181, s25, v135
	v_fmac_f32_e32 v182, s25, v136
	v_fmac_f32_e32 v183, s25, v137
	v_fmac_f32_e32 v184, s25, v138
	v_fmac_f32_e32 v185, s25, v139
	s_waitcnt vmcnt(54)
	v_readlane_b32 s25, v246, 6
	v_cvt_f32_ubyte0_e32 v124, v36
	v_cvt_f32_ubyte1_e32 v125, v36
	v_cvt_f32_ubyte2_e32 v126, v36
	v_cvt_f32_ubyte3_e32 v127, v36
	v_cvt_f32_ubyte0_e32 v128, v37
	v_cvt_f32_ubyte1_e32 v129, v37
	v_cvt_f32_ubyte2_e32 v130, v37
	v_cvt_f32_ubyte3_e32 v131, v37
	v_readlane_b32 s30, v120, 38
	s_lshl_b32 s30, s30, 12
	s_add_u32 s28, s26, s30
	s_addc_u32 s29, s27, 0
	global_load_dwordx2 v[36:37], v162, s[28:29]
	v_fmac_f32_e32 v178, s25, v124
	v_fmac_f32_e32 v179, s25, v125
	v_fmac_f32_e32 v180, s25, v126
	v_fmac_f32_e32 v181, s25, v127
	v_fmac_f32_e32 v182, s25, v128
	v_fmac_f32_e32 v183, s25, v129
	v_fmac_f32_e32 v184, s25, v130
	v_fmac_f32_e32 v185, s25, v131
	s_waitcnt vmcnt(54)
	v_readlane_b32 s25, v246, 7
	v_cvt_f32_ubyte0_e32 v132, v38
	v_cvt_f32_ubyte1_e32 v133, v38
	v_cvt_f32_ubyte2_e32 v134, v38
	v_cvt_f32_ubyte3_e32 v135, v38
	v_cvt_f32_ubyte0_e32 v136, v39
	v_cvt_f32_ubyte1_e32 v137, v39
	v_cvt_f32_ubyte2_e32 v138, v39
	v_cvt_f32_ubyte3_e32 v139, v39
	v_readlane_b32 s30, v120, 39
	s_lshl_b32 s30, s30, 12
	s_add_u32 s28, s26, s30
	s_addc_u32 s29, s27, 0
	global_load_dwordx2 v[38:39], v162, s[28:29]
	v_fmac_f32_e32 v178, s25, v132
	v_fmac_f32_e32 v179, s25, v133
	v_fmac_f32_e32 v180, s25, v134
	v_fmac_f32_e32 v181, s25, v135
	v_fmac_f32_e32 v182, s25, v136
	v_fmac_f32_e32 v183, s25, v137
	v_fmac_f32_e32 v184, s25, v138
	v_fmac_f32_e32 v185, s25, v139
	s_waitcnt vmcnt(54)
	v_readlane_b32 s25, v246, 8
	v_cvt_f32_ubyte0_e32 v124, v40
	v_cvt_f32_ubyte1_e32 v125, v40
	v_cvt_f32_ubyte2_e32 v126, v40
	v_cvt_f32_ubyte3_e32 v127, v40
	v_cvt_f32_ubyte0_e32 v128, v41
	v_cvt_f32_ubyte1_e32 v129, v41
	v_cvt_f32_ubyte2_e32 v130, v41
	v_cvt_f32_ubyte3_e32 v131, v41
	v_readlane_b32 s30, v120, 40
	s_lshl_b32 s30, s30, 12
	s_add_u32 s28, s26, s30
	s_addc_u32 s29, s27, 0
	global_load_dwordx2 v[40:41], v162, s[28:29]
	v_fmac_f32_e32 v178, s25, v124
	v_fmac_f32_e32 v179, s25, v125
	v_fmac_f32_e32 v180, s25, v126
	v_fmac_f32_e32 v181, s25, v127
	v_fmac_f32_e32 v182, s25, v128
	v_fmac_f32_e32 v183, s25, v129
	v_fmac_f32_e32 v184, s25, v130
	v_fmac_f32_e32 v185, s25, v131
	s_waitcnt vmcnt(54)
	v_readlane_b32 s25, v246, 9
	v_cvt_f32_ubyte0_e32 v132, v42
	v_cvt_f32_ubyte1_e32 v133, v42
	v_cvt_f32_ubyte2_e32 v134, v42
	v_cvt_f32_ubyte3_e32 v135, v42
	v_cvt_f32_ubyte0_e32 v136, v43
	v_cvt_f32_ubyte1_e32 v137, v43
	v_cvt_f32_ubyte2_e32 v138, v43
	v_cvt_f32_ubyte3_e32 v139, v43
	v_readlane_b32 s30, v120, 41
	s_lshl_b32 s30, s30, 12
	s_add_u32 s28, s26, s30
	s_addc_u32 s29, s27, 0
	global_load_dwordx2 v[42:43], v162, s[28:29]
	v_fmac_f32_e32 v178, s25, v132
	v_fmac_f32_e32 v179, s25, v133
	v_fmac_f32_e32 v180, s25, v134
	v_fmac_f32_e32 v181, s25, v135
	v_fmac_f32_e32 v182, s25, v136
	v_fmac_f32_e32 v183, s25, v137
	v_fmac_f32_e32 v184, s25, v138
	v_fmac_f32_e32 v185, s25, v139
	s_waitcnt vmcnt(54)
	v_readlane_b32 s25, v246, 10
	v_cvt_f32_ubyte0_e32 v124, v44
	v_cvt_f32_ubyte1_e32 v125, v44
	v_cvt_f32_ubyte2_e32 v126, v44
	v_cvt_f32_ubyte3_e32 v127, v44
	v_cvt_f32_ubyte0_e32 v128, v45
	v_cvt_f32_ubyte1_e32 v129, v45
	v_cvt_f32_ubyte2_e32 v130, v45
	v_cvt_f32_ubyte3_e32 v131, v45
	v_readlane_b32 s30, v120, 42
	s_lshl_b32 s30, s30, 12
	s_add_u32 s28, s26, s30
	s_addc_u32 s29, s27, 0
	global_load_dwordx2 v[44:45], v162, s[28:29]
	v_fmac_f32_e32 v178, s25, v124
	v_fmac_f32_e32 v179, s25, v125
	v_fmac_f32_e32 v180, s25, v126
	v_fmac_f32_e32 v181, s25, v127
	v_fmac_f32_e32 v182, s25, v128
	v_fmac_f32_e32 v183, s25, v129
	v_fmac_f32_e32 v184, s25, v130
	v_fmac_f32_e32 v185, s25, v131
	s_waitcnt vmcnt(54)
	v_readlane_b32 s25, v246, 11
	v_cvt_f32_ubyte0_e32 v132, v46
	v_cvt_f32_ubyte1_e32 v133, v46
	v_cvt_f32_ubyte2_e32 v134, v46
	v_cvt_f32_ubyte3_e32 v135, v46
	v_cvt_f32_ubyte0_e32 v136, v47
	v_cvt_f32_ubyte1_e32 v137, v47
	v_cvt_f32_ubyte2_e32 v138, v47
	v_cvt_f32_ubyte3_e32 v139, v47
	v_readlane_b32 s30, v120, 43
	s_lshl_b32 s30, s30, 12
	s_add_u32 s28, s26, s30
	s_addc_u32 s29, s27, 0
	global_load_dwordx2 v[46:47], v162, s[28:29]
	v_fmac_f32_e32 v178, s25, v132
	v_fmac_f32_e32 v179, s25, v133
	v_fmac_f32_e32 v180, s25, v134
	v_fmac_f32_e32 v181, s25, v135
	v_fmac_f32_e32 v182, s25, v136
	v_fmac_f32_e32 v183, s25, v137
	v_fmac_f32_e32 v184, s25, v138
	v_fmac_f32_e32 v185, s25, v139
	s_waitcnt vmcnt(54)
	v_readlane_b32 s25, v246, 12
	v_cvt_f32_ubyte0_e32 v124, v48
	v_cvt_f32_ubyte1_e32 v125, v48
	v_cvt_f32_ubyte2_e32 v126, v48
	v_cvt_f32_ubyte3_e32 v127, v48
	v_cvt_f32_ubyte0_e32 v128, v49
	v_cvt_f32_ubyte1_e32 v129, v49
	v_cvt_f32_ubyte2_e32 v130, v49
	v_cvt_f32_ubyte3_e32 v131, v49
	v_readlane_b32 s30, v120, 44
	s_lshl_b32 s30, s30, 12
	s_add_u32 s28, s26, s30
	s_addc_u32 s29, s27, 0
	global_load_dwordx2 v[48:49], v162, s[28:29]
	v_fmac_f32_e32 v178, s25, v124
	v_fmac_f32_e32 v179, s25, v125
	v_fmac_f32_e32 v180, s25, v126
	v_fmac_f32_e32 v181, s25, v127
	v_fmac_f32_e32 v182, s25, v128
	v_fmac_f32_e32 v183, s25, v129
	v_fmac_f32_e32 v184, s25, v130
	v_fmac_f32_e32 v185, s25, v131
	s_waitcnt vmcnt(54)
	v_readlane_b32 s25, v246, 13
	v_cvt_f32_ubyte0_e32 v132, v50
	v_cvt_f32_ubyte1_e32 v133, v50
	v_cvt_f32_ubyte2_e32 v134, v50
	v_cvt_f32_ubyte3_e32 v135, v50
	v_cvt_f32_ubyte0_e32 v136, v51
	v_cvt_f32_ubyte1_e32 v137, v51
	v_cvt_f32_ubyte2_e32 v138, v51
	v_cvt_f32_ubyte3_e32 v139, v51
	v_readlane_b32 s30, v120, 45
	s_lshl_b32 s30, s30, 12
	s_add_u32 s28, s26, s30
	s_addc_u32 s29, s27, 0
	global_load_dwordx2 v[50:51], v162, s[28:29]
	v_fmac_f32_e32 v178, s25, v132
	v_fmac_f32_e32 v179, s25, v133
	v_fmac_f32_e32 v180, s25, v134
	v_fmac_f32_e32 v181, s25, v135
	v_fmac_f32_e32 v182, s25, v136
	v_fmac_f32_e32 v183, s25, v137
	v_fmac_f32_e32 v184, s25, v138
	v_fmac_f32_e32 v185, s25, v139
	s_waitcnt vmcnt(54)
	v_readlane_b32 s25, v246, 14
	v_cvt_f32_ubyte0_e32 v124, v52
	v_cvt_f32_ubyte1_e32 v125, v52
	v_cvt_f32_ubyte2_e32 v126, v52
	v_cvt_f32_ubyte3_e32 v127, v52
	v_cvt_f32_ubyte0_e32 v128, v53
	v_cvt_f32_ubyte1_e32 v129, v53
	v_cvt_f32_ubyte2_e32 v130, v53
	v_cvt_f32_ubyte3_e32 v131, v53
	v_readlane_b32 s30, v120, 46
	s_lshl_b32 s30, s30, 12
	s_add_u32 s28, s26, s30
	s_addc_u32 s29, s27, 0
	global_load_dwordx2 v[52:53], v162, s[28:29]
	v_fmac_f32_e32 v178, s25, v124
	v_fmac_f32_e32 v179, s25, v125
	v_fmac_f32_e32 v180, s25, v126
	v_fmac_f32_e32 v181, s25, v127
	v_fmac_f32_e32 v182, s25, v128
	v_fmac_f32_e32 v183, s25, v129
	v_fmac_f32_e32 v184, s25, v130
	v_fmac_f32_e32 v185, s25, v131
	s_waitcnt vmcnt(54)
	v_readlane_b32 s25, v246, 15
	v_cvt_f32_ubyte0_e32 v132, v54
	v_cvt_f32_ubyte1_e32 v133, v54
	v_cvt_f32_ubyte2_e32 v134, v54
	v_cvt_f32_ubyte3_e32 v135, v54
	v_cvt_f32_ubyte0_e32 v136, v55
	v_cvt_f32_ubyte1_e32 v137, v55
	v_cvt_f32_ubyte2_e32 v138, v55
	v_cvt_f32_ubyte3_e32 v139, v55
	v_readlane_b32 s30, v120, 47
	s_lshl_b32 s30, s30, 12
	s_add_u32 s28, s26, s30
	s_addc_u32 s29, s27, 0
	global_load_dwordx2 v[54:55], v162, s[28:29]
	v_fmac_f32_e32 v178, s25, v132
	v_fmac_f32_e32 v179, s25, v133
	v_fmac_f32_e32 v180, s25, v134
	v_fmac_f32_e32 v181, s25, v135
	v_fmac_f32_e32 v182, s25, v136
	v_fmac_f32_e32 v183, s25, v137
	v_fmac_f32_e32 v184, s25, v138
	v_fmac_f32_e32 v185, s25, v139
	s_waitcnt vmcnt(54)
	v_readlane_b32 s25, v246, 16
	v_cvt_f32_ubyte0_e32 v124, v56
	v_cvt_f32_ubyte1_e32 v125, v56
	v_cvt_f32_ubyte2_e32 v126, v56
	v_cvt_f32_ubyte3_e32 v127, v56
	v_cvt_f32_ubyte0_e32 v128, v57
	v_cvt_f32_ubyte1_e32 v129, v57
	v_cvt_f32_ubyte2_e32 v130, v57
	v_cvt_f32_ubyte3_e32 v131, v57
	v_readlane_b32 s30, v120, 48
	s_lshl_b32 s30, s30, 12
	s_add_u32 s28, s26, s30
	s_addc_u32 s29, s27, 0
	global_load_dwordx2 v[56:57], v162, s[28:29]
	v_fmac_f32_e32 v178, s25, v124
	v_fmac_f32_e32 v179, s25, v125
	v_fmac_f32_e32 v180, s25, v126
	v_fmac_f32_e32 v181, s25, v127
	v_fmac_f32_e32 v182, s25, v128
	v_fmac_f32_e32 v183, s25, v129
	v_fmac_f32_e32 v184, s25, v130
	v_fmac_f32_e32 v185, s25, v131
	s_waitcnt vmcnt(54)
	v_readlane_b32 s25, v246, 17
	v_cvt_f32_ubyte0_e32 v132, v58
	v_cvt_f32_ubyte1_e32 v133, v58
	v_cvt_f32_ubyte2_e32 v134, v58
	v_cvt_f32_ubyte3_e32 v135, v58
	v_cvt_f32_ubyte0_e32 v136, v59
	v_cvt_f32_ubyte1_e32 v137, v59
	v_cvt_f32_ubyte2_e32 v138, v59
	v_cvt_f32_ubyte3_e32 v139, v59
	v_readlane_b32 s30, v120, 49
	s_lshl_b32 s30, s30, 12
	s_add_u32 s28, s26, s30
	s_addc_u32 s29, s27, 0
	global_load_dwordx2 v[58:59], v162, s[28:29]
	v_fmac_f32_e32 v178, s25, v132
	v_fmac_f32_e32 v179, s25, v133
	v_fmac_f32_e32 v180, s25, v134
	v_fmac_f32_e32 v181, s25, v135
	v_fmac_f32_e32 v182, s25, v136
	v_fmac_f32_e32 v183, s25, v137
	v_fmac_f32_e32 v184, s25, v138
	v_fmac_f32_e32 v185, s25, v139
	s_waitcnt vmcnt(54)
	v_readlane_b32 s25, v246, 18
	v_cvt_f32_ubyte0_e32 v124, v60
	v_cvt_f32_ubyte1_e32 v125, v60
	v_cvt_f32_ubyte2_e32 v126, v60
	v_cvt_f32_ubyte3_e32 v127, v60
	v_cvt_f32_ubyte0_e32 v128, v61
	v_cvt_f32_ubyte1_e32 v129, v61
	v_cvt_f32_ubyte2_e32 v130, v61
	v_cvt_f32_ubyte3_e32 v131, v61
	v_readlane_b32 s30, v120, 50
	s_lshl_b32 s30, s30, 12
	s_add_u32 s28, s26, s30
	s_addc_u32 s29, s27, 0
	global_load_dwordx2 v[60:61], v162, s[28:29]
	v_fmac_f32_e32 v178, s25, v124
	v_fmac_f32_e32 v179, s25, v125
	v_fmac_f32_e32 v180, s25, v126
	v_fmac_f32_e32 v181, s25, v127
	v_fmac_f32_e32 v182, s25, v128
	v_fmac_f32_e32 v183, s25, v129
	v_fmac_f32_e32 v184, s25, v130
	v_fmac_f32_e32 v185, s25, v131
	s_waitcnt vmcnt(54)
	v_readlane_b32 s25, v246, 19
	v_cvt_f32_ubyte0_e32 v132, v62
	v_cvt_f32_ubyte1_e32 v133, v62
	v_cvt_f32_ubyte2_e32 v134, v62
	v_cvt_f32_ubyte3_e32 v135, v62
	v_cvt_f32_ubyte0_e32 v136, v63
	v_cvt_f32_ubyte1_e32 v137, v63
	v_cvt_f32_ubyte2_e32 v138, v63
	v_cvt_f32_ubyte3_e32 v139, v63
	v_readlane_b32 s30, v120, 51
	s_lshl_b32 s30, s30, 12
	s_add_u32 s28, s26, s30
	s_addc_u32 s29, s27, 0
	global_load_dwordx2 v[62:63], v162, s[28:29]
	v_fmac_f32_e32 v178, s25, v132
	v_fmac_f32_e32 v179, s25, v133
	v_fmac_f32_e32 v180, s25, v134
	v_fmac_f32_e32 v181, s25, v135
	v_fmac_f32_e32 v182, s25, v136
	v_fmac_f32_e32 v183, s25, v137
	v_fmac_f32_e32 v184, s25, v138
	v_fmac_f32_e32 v185, s25, v139
	s_waitcnt vmcnt(54)
	v_readlane_b32 s25, v246, 20
	v_cvt_f32_ubyte0_e32 v124, v64
	v_cvt_f32_ubyte1_e32 v125, v64
	v_cvt_f32_ubyte2_e32 v126, v64
	v_cvt_f32_ubyte3_e32 v127, v64
	v_cvt_f32_ubyte0_e32 v128, v65
	v_cvt_f32_ubyte1_e32 v129, v65
	v_cvt_f32_ubyte2_e32 v130, v65
	v_cvt_f32_ubyte3_e32 v131, v65
	v_readlane_b32 s30, v120, 52
	s_lshl_b32 s30, s30, 12
	s_add_u32 s28, s26, s30
	s_addc_u32 s29, s27, 0
	global_load_dwordx2 v[64:65], v162, s[28:29]
	v_fmac_f32_e32 v178, s25, v124
	v_fmac_f32_e32 v179, s25, v125
	v_fmac_f32_e32 v180, s25, v126
	v_fmac_f32_e32 v181, s25, v127
	v_fmac_f32_e32 v182, s25, v128
	v_fmac_f32_e32 v183, s25, v129
	v_fmac_f32_e32 v184, s25, v130
	v_fmac_f32_e32 v185, s25, v131
	s_waitcnt vmcnt(54)
	v_readlane_b32 s25, v246, 21
	v_cvt_f32_ubyte0_e32 v132, v66
	v_cvt_f32_ubyte1_e32 v133, v66
	v_cvt_f32_ubyte2_e32 v134, v66
	v_cvt_f32_ubyte3_e32 v135, v66
	v_cvt_f32_ubyte0_e32 v136, v67
	v_cvt_f32_ubyte1_e32 v137, v67
	v_cvt_f32_ubyte2_e32 v138, v67
	v_cvt_f32_ubyte3_e32 v139, v67
	v_readlane_b32 s30, v120, 53
	s_lshl_b32 s30, s30, 12
	s_add_u32 s28, s26, s30
	s_addc_u32 s29, s27, 0
	global_load_dwordx2 v[66:67], v162, s[28:29]
	v_fmac_f32_e32 v178, s25, v132
	v_fmac_f32_e32 v179, s25, v133
	v_fmac_f32_e32 v180, s25, v134
	v_fmac_f32_e32 v181, s25, v135
	v_fmac_f32_e32 v182, s25, v136
	v_fmac_f32_e32 v183, s25, v137
	v_fmac_f32_e32 v184, s25, v138
	v_fmac_f32_e32 v185, s25, v139
	s_waitcnt vmcnt(54)
	v_readlane_b32 s25, v246, 22
	v_cvt_f32_ubyte0_e32 v124, v68
	v_cvt_f32_ubyte1_e32 v125, v68
	v_cvt_f32_ubyte2_e32 v126, v68
	v_cvt_f32_ubyte3_e32 v127, v68
	v_cvt_f32_ubyte0_e32 v128, v69
	v_cvt_f32_ubyte1_e32 v129, v69
	v_cvt_f32_ubyte2_e32 v130, v69
	v_cvt_f32_ubyte3_e32 v131, v69
	v_readlane_b32 s30, v120, 54
	s_lshl_b32 s30, s30, 12
	s_add_u32 s28, s26, s30
	s_addc_u32 s29, s27, 0
	global_load_dwordx2 v[68:69], v162, s[28:29]
	v_fmac_f32_e32 v178, s25, v124
	v_fmac_f32_e32 v179, s25, v125
	v_fmac_f32_e32 v180, s25, v126
	v_fmac_f32_e32 v181, s25, v127
	v_fmac_f32_e32 v182, s25, v128
	v_fmac_f32_e32 v183, s25, v129
	v_fmac_f32_e32 v184, s25, v130
	v_fmac_f32_e32 v185, s25, v131
	s_waitcnt vmcnt(54)
	v_readlane_b32 s25, v246, 23
	v_cvt_f32_ubyte0_e32 v132, v70
	v_cvt_f32_ubyte1_e32 v133, v70
	v_cvt_f32_ubyte2_e32 v134, v70
	v_cvt_f32_ubyte3_e32 v135, v70
	v_cvt_f32_ubyte0_e32 v136, v71
	v_cvt_f32_ubyte1_e32 v137, v71
	v_cvt_f32_ubyte2_e32 v138, v71
	v_cvt_f32_ubyte3_e32 v139, v71
	v_readlane_b32 s30, v120, 55
	s_lshl_b32 s30, s30, 12
	s_add_u32 s28, s26, s30
	s_addc_u32 s29, s27, 0
	global_load_dwordx2 v[70:71], v162, s[28:29]
	v_fmac_f32_e32 v178, s25, v132
	v_fmac_f32_e32 v179, s25, v133
	v_fmac_f32_e32 v180, s25, v134
	v_fmac_f32_e32 v181, s25, v135
	v_fmac_f32_e32 v182, s25, v136
	v_fmac_f32_e32 v183, s25, v137
	v_fmac_f32_e32 v184, s25, v138
	v_fmac_f32_e32 v185, s25, v139
	s_waitcnt vmcnt(54)
	v_readlane_b32 s25, v246, 24
	v_cvt_f32_ubyte0_e32 v124, v72
	v_cvt_f32_ubyte1_e32 v125, v72
	v_cvt_f32_ubyte2_e32 v126, v72
	v_cvt_f32_ubyte3_e32 v127, v72
	v_cvt_f32_ubyte0_e32 v128, v73
	v_cvt_f32_ubyte1_e32 v129, v73
	v_cvt_f32_ubyte2_e32 v130, v73
	v_cvt_f32_ubyte3_e32 v131, v73
	v_readlane_b32 s30, v120, 56
	s_lshl_b32 s30, s30, 12
	s_add_u32 s28, s26, s30
	s_addc_u32 s29, s27, 0
	global_load_dwordx2 v[72:73], v162, s[28:29]
	v_fmac_f32_e32 v178, s25, v124
	v_fmac_f32_e32 v179, s25, v125
	v_fmac_f32_e32 v180, s25, v126
	v_fmac_f32_e32 v181, s25, v127
	v_fmac_f32_e32 v182, s25, v128
	v_fmac_f32_e32 v183, s25, v129
	v_fmac_f32_e32 v184, s25, v130
	v_fmac_f32_e32 v185, s25, v131
	s_waitcnt vmcnt(54)
	v_readlane_b32 s25, v246, 25
	v_cvt_f32_ubyte0_e32 v132, v74
	v_cvt_f32_ubyte1_e32 v133, v74
	v_cvt_f32_ubyte2_e32 v134, v74
	v_cvt_f32_ubyte3_e32 v135, v74
	v_cvt_f32_ubyte0_e32 v136, v75
	v_cvt_f32_ubyte1_e32 v137, v75
	v_cvt_f32_ubyte2_e32 v138, v75
	v_cvt_f32_ubyte3_e32 v139, v75
	v_readlane_b32 s30, v120, 57
	s_lshl_b32 s30, s30, 12
	s_add_u32 s28, s26, s30
	s_addc_u32 s29, s27, 0
	global_load_dwordx2 v[74:75], v162, s[28:29]
	v_fmac_f32_e32 v178, s25, v132
	v_fmac_f32_e32 v179, s25, v133
	v_fmac_f32_e32 v180, s25, v134
	v_fmac_f32_e32 v181, s25, v135
	v_fmac_f32_e32 v182, s25, v136
	v_fmac_f32_e32 v183, s25, v137
	v_fmac_f32_e32 v184, s25, v138
	v_fmac_f32_e32 v185, s25, v139
	s_waitcnt vmcnt(54)
	v_readlane_b32 s25, v246, 26
	v_cvt_f32_ubyte0_e32 v124, v76
	v_cvt_f32_ubyte1_e32 v125, v76
	v_cvt_f32_ubyte2_e32 v126, v76
	v_cvt_f32_ubyte3_e32 v127, v76
	v_cvt_f32_ubyte0_e32 v128, v77
	v_cvt_f32_ubyte1_e32 v129, v77
	v_cvt_f32_ubyte2_e32 v130, v77
	v_cvt_f32_ubyte3_e32 v131, v77
	v_readlane_b32 s30, v120, 58
	s_lshl_b32 s30, s30, 12
	s_add_u32 s28, s26, s30
	s_addc_u32 s29, s27, 0
	global_load_dwordx2 v[76:77], v162, s[28:29]
	v_fmac_f32_e32 v178, s25, v124
	v_fmac_f32_e32 v179, s25, v125
	v_fmac_f32_e32 v180, s25, v126
	v_fmac_f32_e32 v181, s25, v127
	v_fmac_f32_e32 v182, s25, v128
	v_fmac_f32_e32 v183, s25, v129
	v_fmac_f32_e32 v184, s25, v130
	v_fmac_f32_e32 v185, s25, v131
	s_waitcnt vmcnt(54)
	v_readlane_b32 s25, v246, 27
	v_cvt_f32_ubyte0_e32 v132, v78
	v_cvt_f32_ubyte1_e32 v133, v78
	v_cvt_f32_ubyte2_e32 v134, v78
	v_cvt_f32_ubyte3_e32 v135, v78
	v_cvt_f32_ubyte0_e32 v136, v79
	v_cvt_f32_ubyte1_e32 v137, v79
	v_cvt_f32_ubyte2_e32 v138, v79
	v_cvt_f32_ubyte3_e32 v139, v79
	v_readlane_b32 s30, v120, 59
	s_lshl_b32 s30, s30, 12
	s_add_u32 s28, s26, s30
	s_addc_u32 s29, s27, 0
	global_load_dwordx2 v[78:79], v162, s[28:29]
	v_fmac_f32_e32 v178, s25, v132
	v_fmac_f32_e32 v179, s25, v133
	v_fmac_f32_e32 v180, s25, v134
	v_fmac_f32_e32 v181, s25, v135
	v_fmac_f32_e32 v182, s25, v136
	v_fmac_f32_e32 v183, s25, v137
	v_fmac_f32_e32 v184, s25, v138
	v_fmac_f32_e32 v185, s25, v139
	s_waitcnt vmcnt(54)
	v_readlane_b32 s25, v246, 28
	v_cvt_f32_ubyte0_e32 v124, v80
	v_cvt_f32_ubyte1_e32 v125, v80
	v_cvt_f32_ubyte2_e32 v126, v80
	v_cvt_f32_ubyte3_e32 v127, v80
	v_cvt_f32_ubyte0_e32 v128, v81
	v_cvt_f32_ubyte1_e32 v129, v81
	v_cvt_f32_ubyte2_e32 v130, v81
	v_cvt_f32_ubyte3_e32 v131, v81
	v_readlane_b32 s30, v120, 60
	s_lshl_b32 s30, s30, 12
	s_add_u32 s28, s26, s30
	s_addc_u32 s29, s27, 0
	global_load_dwordx2 v[80:81], v162, s[28:29]
	v_fmac_f32_e32 v178, s25, v124
	v_fmac_f32_e32 v179, s25, v125
	v_fmac_f32_e32 v180, s25, v126
	v_fmac_f32_e32 v181, s25, v127
	v_fmac_f32_e32 v182, s25, v128
	v_fmac_f32_e32 v183, s25, v129
	v_fmac_f32_e32 v184, s25, v130
	v_fmac_f32_e32 v185, s25, v131
	s_waitcnt vmcnt(54)
	v_readlane_b32 s25, v246, 29
	v_cvt_f32_ubyte0_e32 v132, v82
	v_cvt_f32_ubyte1_e32 v133, v82
	v_cvt_f32_ubyte2_e32 v134, v82
	v_cvt_f32_ubyte3_e32 v135, v82
	v_cvt_f32_ubyte0_e32 v136, v83
	v_cvt_f32_ubyte1_e32 v137, v83
	v_cvt_f32_ubyte2_e32 v138, v83
	v_cvt_f32_ubyte3_e32 v139, v83
	v_readlane_b32 s30, v120, 61
	s_lshl_b32 s30, s30, 12
	s_add_u32 s28, s26, s30
	s_addc_u32 s29, s27, 0
	global_load_dwordx2 v[82:83], v162, s[28:29]
	v_fmac_f32_e32 v178, s25, v132
	v_fmac_f32_e32 v179, s25, v133
	v_fmac_f32_e32 v180, s25, v134
	v_fmac_f32_e32 v181, s25, v135
	v_fmac_f32_e32 v182, s25, v136
	v_fmac_f32_e32 v183, s25, v137
	v_fmac_f32_e32 v184, s25, v138
	v_fmac_f32_e32 v185, s25, v139
	s_waitcnt vmcnt(54)
	v_readlane_b32 s25, v246, 30
	v_cvt_f32_ubyte0_e32 v124, v84
	v_cvt_f32_ubyte1_e32 v125, v84
	v_cvt_f32_ubyte2_e32 v126, v84
	v_cvt_f32_ubyte3_e32 v127, v84
	v_cvt_f32_ubyte0_e32 v128, v85
	v_cvt_f32_ubyte1_e32 v129, v85
	v_cvt_f32_ubyte2_e32 v130, v85
	v_cvt_f32_ubyte3_e32 v131, v85
	v_readlane_b32 s30, v120, 62
	s_lshl_b32 s30, s30, 12
	s_add_u32 s28, s26, s30
	s_addc_u32 s29, s27, 0
	global_load_dwordx2 v[84:85], v162, s[28:29]
	v_fmac_f32_e32 v178, s25, v124
	v_fmac_f32_e32 v179, s25, v125
	v_fmac_f32_e32 v180, s25, v126
	v_fmac_f32_e32 v181, s25, v127
	v_fmac_f32_e32 v182, s25, v128
	v_fmac_f32_e32 v183, s25, v129
	v_fmac_f32_e32 v184, s25, v130
	v_fmac_f32_e32 v185, s25, v131
	s_waitcnt vmcnt(54)
	v_readlane_b32 s25, v246, 31
	v_cvt_f32_ubyte0_e32 v132, v86
	v_cvt_f32_ubyte1_e32 v133, v86
	v_cvt_f32_ubyte2_e32 v134, v86
	v_cvt_f32_ubyte3_e32 v135, v86
	v_cvt_f32_ubyte0_e32 v136, v87
	v_cvt_f32_ubyte1_e32 v137, v87
	v_cvt_f32_ubyte2_e32 v138, v87
	v_cvt_f32_ubyte3_e32 v139, v87
	v_readlane_b32 s30, v120, 63
	s_lshl_b32 s30, s30, 12
	s_add_u32 s28, s26, s30
	s_addc_u32 s29, s27, 0
	global_load_dwordx2 v[86:87], v162, s[28:29]
	v_fmac_f32_e32 v178, s25, v132
	v_fmac_f32_e32 v179, s25, v133
	v_fmac_f32_e32 v180, s25, v134
	v_fmac_f32_e32 v181, s25, v135
	v_fmac_f32_e32 v182, s25, v136
	v_fmac_f32_e32 v183, s25, v137
	v_fmac_f32_e32 v184, s25, v138
	v_fmac_f32_e32 v185, s25, v139
	s_waitcnt vmcnt(31)
	v_readlane_b32 s25, v246, 32
	v_cvt_f32_ubyte0_e32 v124, v24
	v_cvt_f32_ubyte1_e32 v125, v24
	v_cvt_f32_ubyte2_e32 v126, v24
	v_cvt_f32_ubyte3_e32 v127, v24
	v_cvt_f32_ubyte0_e32 v128, v25
	v_cvt_f32_ubyte1_e32 v129, v25
	v_cvt_f32_ubyte2_e32 v130, v25
	v_cvt_f32_ubyte3_e32 v131, v25
	v_readlane_b32 s30, v121, 0
	s_lshl_b32 s30, s30, 12
	s_add_u32 s28, s26, s30
	s_addc_u32 s29, s27, 0
	global_load_dwordx2 v[24:25], v162, s[28:29]
	v_fmac_f32_e32 v178, s25, v124
	v_fmac_f32_e32 v179, s25, v125
	v_fmac_f32_e32 v180, s25, v126
	v_fmac_f32_e32 v181, s25, v127
	v_fmac_f32_e32 v182, s25, v128
	v_fmac_f32_e32 v183, s25, v129
	v_fmac_f32_e32 v184, s25, v130
	v_fmac_f32_e32 v185, s25, v131
	s_waitcnt vmcnt(31)
	v_readlane_b32 s25, v246, 33
	v_cvt_f32_ubyte0_e32 v132, v26
	v_cvt_f32_ubyte1_e32 v133, v26
	v_cvt_f32_ubyte2_e32 v134, v26
	v_cvt_f32_ubyte3_e32 v135, v26
	v_cvt_f32_ubyte0_e32 v136, v27
	v_cvt_f32_ubyte1_e32 v137, v27
	v_cvt_f32_ubyte2_e32 v138, v27
	v_cvt_f32_ubyte3_e32 v139, v27
	v_readlane_b32 s30, v121, 1
	s_lshl_b32 s30, s30, 12
	s_add_u32 s28, s26, s30
	s_addc_u32 s29, s27, 0
	global_load_dwordx2 v[26:27], v162, s[28:29]
	v_fmac_f32_e32 v178, s25, v132
	v_fmac_f32_e32 v179, s25, v133
	v_fmac_f32_e32 v180, s25, v134
	v_fmac_f32_e32 v181, s25, v135
	v_fmac_f32_e32 v182, s25, v136
	v_fmac_f32_e32 v183, s25, v137
	v_fmac_f32_e32 v184, s25, v138
	v_fmac_f32_e32 v185, s25, v139
	s_waitcnt vmcnt(31)
	v_readlane_b32 s25, v246, 34
	v_cvt_f32_ubyte0_e32 v124, v28
	v_cvt_f32_ubyte1_e32 v125, v28
	v_cvt_f32_ubyte2_e32 v126, v28
	v_cvt_f32_ubyte3_e32 v127, v28
	v_cvt_f32_ubyte0_e32 v128, v29
	v_cvt_f32_ubyte1_e32 v129, v29
	v_cvt_f32_ubyte2_e32 v130, v29
	v_cvt_f32_ubyte3_e32 v131, v29
	v_readlane_b32 s30, v121, 2
	s_lshl_b32 s30, s30, 12
	s_add_u32 s28, s26, s30
	s_addc_u32 s29, s27, 0
	global_load_dwordx2 v[28:29], v162, s[28:29]
	v_fmac_f32_e32 v178, s25, v124
	v_fmac_f32_e32 v179, s25, v125
	v_fmac_f32_e32 v180, s25, v126
	v_fmac_f32_e32 v181, s25, v127
	v_fmac_f32_e32 v182, s25, v128
	v_fmac_f32_e32 v183, s25, v129
	v_fmac_f32_e32 v184, s25, v130
	v_fmac_f32_e32 v185, s25, v131
	s_waitcnt vmcnt(31)
	v_readlane_b32 s25, v246, 35
	v_cvt_f32_ubyte0_e32 v132, v30
	v_cvt_f32_ubyte1_e32 v133, v30
	v_cvt_f32_ubyte2_e32 v134, v30
	v_cvt_f32_ubyte3_e32 v135, v30
	v_cvt_f32_ubyte0_e32 v136, v31
	v_cvt_f32_ubyte1_e32 v137, v31
	v_cvt_f32_ubyte2_e32 v138, v31
	v_cvt_f32_ubyte3_e32 v139, v31
	v_readlane_b32 s30, v121, 3
	s_lshl_b32 s30, s30, 12
	s_add_u32 s28, s26, s30
	s_addc_u32 s29, s27, 0
	global_load_dwordx2 v[30:31], v162, s[28:29]
	v_fmac_f32_e32 v178, s25, v132
	v_fmac_f32_e32 v179, s25, v133
	v_fmac_f32_e32 v180, s25, v134
	v_fmac_f32_e32 v181, s25, v135
	v_fmac_f32_e32 v182, s25, v136
	v_fmac_f32_e32 v183, s25, v137
	v_fmac_f32_e32 v184, s25, v138
	v_fmac_f32_e32 v185, s25, v139
	s_waitcnt vmcnt(31)
	v_readlane_b32 s25, v246, 36
	v_cvt_f32_ubyte0_e32 v124, v32
	v_cvt_f32_ubyte1_e32 v125, v32
	v_cvt_f32_ubyte2_e32 v126, v32
	v_cvt_f32_ubyte3_e32 v127, v32
	v_cvt_f32_ubyte0_e32 v128, v33
	v_cvt_f32_ubyte1_e32 v129, v33
	v_cvt_f32_ubyte2_e32 v130, v33
	v_cvt_f32_ubyte3_e32 v131, v33
	v_readlane_b32 s30, v121, 4
	s_lshl_b32 s30, s30, 12
	s_add_u32 s28, s26, s30
	s_addc_u32 s29, s27, 0
	global_load_dwordx2 v[32:33], v162, s[28:29]
	v_fmac_f32_e32 v178, s25, v124
	v_fmac_f32_e32 v179, s25, v125
	v_fmac_f32_e32 v180, s25, v126
	v_fmac_f32_e32 v181, s25, v127
	v_fmac_f32_e32 v182, s25, v128
	v_fmac_f32_e32 v183, s25, v129
	v_fmac_f32_e32 v184, s25, v130
	v_fmac_f32_e32 v185, s25, v131
	s_waitcnt vmcnt(31)
	v_readlane_b32 s25, v246, 37
	v_cvt_f32_ubyte0_e32 v132, v34
	v_cvt_f32_ubyte1_e32 v133, v34
	v_cvt_f32_ubyte2_e32 v134, v34
	v_cvt_f32_ubyte3_e32 v135, v34
	v_cvt_f32_ubyte0_e32 v136, v35
	v_cvt_f32_ubyte1_e32 v137, v35
	v_cvt_f32_ubyte2_e32 v138, v35
	v_cvt_f32_ubyte3_e32 v139, v35
	v_readlane_b32 s30, v121, 5
	s_lshl_b32 s30, s30, 12
	s_add_u32 s28, s26, s30
	s_addc_u32 s29, s27, 0
	global_load_dwordx2 v[34:35], v162, s[28:29]
	v_fmac_f32_e32 v178, s25, v132
	v_fmac_f32_e32 v179, s25, v133
	v_fmac_f32_e32 v180, s25, v134
	v_fmac_f32_e32 v181, s25, v135
	v_fmac_f32_e32 v182, s25, v136
	v_fmac_f32_e32 v183, s25, v137
	v_fmac_f32_e32 v184, s25, v138
	v_fmac_f32_e32 v185, s25, v139
	s_waitcnt vmcnt(31)
	v_readlane_b32 s25, v246, 38
	v_cvt_f32_ubyte0_e32 v124, v36
	v_cvt_f32_ubyte1_e32 v125, v36
	v_cvt_f32_ubyte2_e32 v126, v36
	v_cvt_f32_ubyte3_e32 v127, v36
	v_cvt_f32_ubyte0_e32 v128, v37
	v_cvt_f32_ubyte1_e32 v129, v37
	v_cvt_f32_ubyte2_e32 v130, v37
	v_cvt_f32_ubyte3_e32 v131, v37
	v_readlane_b32 s30, v121, 6
	s_lshl_b32 s30, s30, 12
	s_add_u32 s28, s26, s30
	s_addc_u32 s29, s27, 0
	global_load_dwordx2 v[36:37], v162, s[28:29]
	v_fmac_f32_e32 v178, s25, v124
	v_fmac_f32_e32 v179, s25, v125
	v_fmac_f32_e32 v180, s25, v126
	v_fmac_f32_e32 v181, s25, v127
	v_fmac_f32_e32 v182, s25, v128
	v_fmac_f32_e32 v183, s25, v129
	v_fmac_f32_e32 v184, s25, v130
	v_fmac_f32_e32 v185, s25, v131
	s_waitcnt vmcnt(31)
	v_readlane_b32 s25, v246, 39
	v_cvt_f32_ubyte0_e32 v132, v38
	v_cvt_f32_ubyte1_e32 v133, v38
	v_cvt_f32_ubyte2_e32 v134, v38
	v_cvt_f32_ubyte3_e32 v135, v38
	v_cvt_f32_ubyte0_e32 v136, v39
	v_cvt_f32_ubyte1_e32 v137, v39
	v_cvt_f32_ubyte2_e32 v138, v39
	v_cvt_f32_ubyte3_e32 v139, v39
	v_readlane_b32 s30, v121, 7
	s_lshl_b32 s30, s30, 12
	s_add_u32 s28, s26, s30
	s_addc_u32 s29, s27, 0
	global_load_dwordx2 v[38:39], v162, s[28:29]
	v_fmac_f32_e32 v178, s25, v132
	v_fmac_f32_e32 v179, s25, v133
	v_fmac_f32_e32 v180, s25, v134
	v_fmac_f32_e32 v181, s25, v135
	v_fmac_f32_e32 v182, s25, v136
	v_fmac_f32_e32 v183, s25, v137
	v_fmac_f32_e32 v184, s25, v138
	v_fmac_f32_e32 v185, s25, v139
	s_waitcnt vmcnt(31)
	v_readlane_b32 s25, v246, 40
	v_cvt_f32_ubyte0_e32 v124, v40
	v_cvt_f32_ubyte1_e32 v125, v40
	v_cvt_f32_ubyte2_e32 v126, v40
	v_cvt_f32_ubyte3_e32 v127, v40
	v_cvt_f32_ubyte0_e32 v128, v41
	v_cvt_f32_ubyte1_e32 v129, v41
	v_cvt_f32_ubyte2_e32 v130, v41
	v_cvt_f32_ubyte3_e32 v131, v41
	v_readlane_b32 s30, v121, 8
	s_lshl_b32 s30, s30, 12
	s_add_u32 s28, s26, s30
	s_addc_u32 s29, s27, 0
	global_load_dwordx2 v[40:41], v162, s[28:29]
	v_fmac_f32_e32 v178, s25, v124
	v_fmac_f32_e32 v179, s25, v125
	v_fmac_f32_e32 v180, s25, v126
	v_fmac_f32_e32 v181, s25, v127
	v_fmac_f32_e32 v182, s25, v128
	v_fmac_f32_e32 v183, s25, v129
	v_fmac_f32_e32 v184, s25, v130
	v_fmac_f32_e32 v185, s25, v131
	s_waitcnt vmcnt(31)
	v_readlane_b32 s25, v246, 41
	v_cvt_f32_ubyte0_e32 v132, v42
	v_cvt_f32_ubyte1_e32 v133, v42
	v_cvt_f32_ubyte2_e32 v134, v42
	v_cvt_f32_ubyte3_e32 v135, v42
	v_cvt_f32_ubyte0_e32 v136, v43
	v_cvt_f32_ubyte1_e32 v137, v43
	v_cvt_f32_ubyte2_e32 v138, v43
	v_cvt_f32_ubyte3_e32 v139, v43
	v_readlane_b32 s30, v121, 9
	s_lshl_b32 s30, s30, 12
	s_add_u32 s28, s26, s30
	s_addc_u32 s29, s27, 0
	global_load_dwordx2 v[42:43], v162, s[28:29]
	v_fmac_f32_e32 v178, s25, v132
	v_fmac_f32_e32 v179, s25, v133
	v_fmac_f32_e32 v180, s25, v134
	v_fmac_f32_e32 v181, s25, v135
	v_fmac_f32_e32 v182, s25, v136
	v_fmac_f32_e32 v183, s25, v137
	v_fmac_f32_e32 v184, s25, v138
	v_fmac_f32_e32 v185, s25, v139
	s_waitcnt vmcnt(31)
	v_readlane_b32 s25, v246, 42
	v_cvt_f32_ubyte0_e32 v124, v44
	v_cvt_f32_ubyte1_e32 v125, v44
	v_cvt_f32_ubyte2_e32 v126, v44
	v_cvt_f32_ubyte3_e32 v127, v44
	v_cvt_f32_ubyte0_e32 v128, v45
	v_cvt_f32_ubyte1_e32 v129, v45
	v_cvt_f32_ubyte2_e32 v130, v45
	v_cvt_f32_ubyte3_e32 v131, v45
	v_readlane_b32 s30, v121, 10
	s_lshl_b32 s30, s30, 12
	s_add_u32 s28, s26, s30
	s_addc_u32 s29, s27, 0
	global_load_dwordx2 v[44:45], v162, s[28:29]
	v_fmac_f32_e32 v178, s25, v124
	v_fmac_f32_e32 v179, s25, v125
	v_fmac_f32_e32 v180, s25, v126
	v_fmac_f32_e32 v181, s25, v127
	v_fmac_f32_e32 v182, s25, v128
	v_fmac_f32_e32 v183, s25, v129
	v_fmac_f32_e32 v184, s25, v130
	v_fmac_f32_e32 v185, s25, v131
	s_waitcnt vmcnt(31)
	v_readlane_b32 s25, v246, 43
	v_cvt_f32_ubyte0_e32 v132, v46
	v_cvt_f32_ubyte1_e32 v133, v46
	v_cvt_f32_ubyte2_e32 v134, v46
	v_cvt_f32_ubyte3_e32 v135, v46
	v_cvt_f32_ubyte0_e32 v136, v47
	v_cvt_f32_ubyte1_e32 v137, v47
	v_cvt_f32_ubyte2_e32 v138, v47
	v_cvt_f32_ubyte3_e32 v139, v47
	v_readlane_b32 s30, v121, 11
	s_lshl_b32 s30, s30, 12
	s_add_u32 s28, s26, s30
	s_addc_u32 s29, s27, 0
	global_load_dwordx2 v[46:47], v162, s[28:29]
	v_fmac_f32_e32 v178, s25, v132
	v_fmac_f32_e32 v179, s25, v133
	v_fmac_f32_e32 v180, s25, v134
	v_fmac_f32_e32 v181, s25, v135
	v_fmac_f32_e32 v182, s25, v136
	v_fmac_f32_e32 v183, s25, v137
	v_fmac_f32_e32 v184, s25, v138
	v_fmac_f32_e32 v185, s25, v139
	s_waitcnt vmcnt(31)
	v_readlane_b32 s25, v246, 44
	v_cvt_f32_ubyte0_e32 v124, v48
	v_cvt_f32_ubyte1_e32 v125, v48
	v_cvt_f32_ubyte2_e32 v126, v48
	v_cvt_f32_ubyte3_e32 v127, v48
	v_cvt_f32_ubyte0_e32 v128, v49
	v_cvt_f32_ubyte1_e32 v129, v49
	v_cvt_f32_ubyte2_e32 v130, v49
	v_cvt_f32_ubyte3_e32 v131, v49
	v_readlane_b32 s30, v121, 12
	s_lshl_b32 s30, s30, 12
	s_add_u32 s28, s26, s30
	s_addc_u32 s29, s27, 0
	global_load_dwordx2 v[48:49], v162, s[28:29]
	v_fmac_f32_e32 v178, s25, v124
	v_fmac_f32_e32 v179, s25, v125
	v_fmac_f32_e32 v180, s25, v126
	v_fmac_f32_e32 v181, s25, v127
	v_fmac_f32_e32 v182, s25, v128
	v_fmac_f32_e32 v183, s25, v129
	v_fmac_f32_e32 v184, s25, v130
	v_fmac_f32_e32 v185, s25, v131
	s_waitcnt vmcnt(31)
	v_readlane_b32 s25, v246, 45
	v_cvt_f32_ubyte0_e32 v132, v50
	v_cvt_f32_ubyte1_e32 v133, v50
	v_cvt_f32_ubyte2_e32 v134, v50
	v_cvt_f32_ubyte3_e32 v135, v50
	v_cvt_f32_ubyte0_e32 v136, v51
	v_cvt_f32_ubyte1_e32 v137, v51
	v_cvt_f32_ubyte2_e32 v138, v51
	v_cvt_f32_ubyte3_e32 v139, v51
	v_readlane_b32 s30, v121, 13
	s_lshl_b32 s30, s30, 12
	s_add_u32 s28, s26, s30
	s_addc_u32 s29, s27, 0
	global_load_dwordx2 v[50:51], v162, s[28:29]
	v_fmac_f32_e32 v178, s25, v132
	v_fmac_f32_e32 v179, s25, v133
	v_fmac_f32_e32 v180, s25, v134
	v_fmac_f32_e32 v181, s25, v135
	v_fmac_f32_e32 v182, s25, v136
	v_fmac_f32_e32 v183, s25, v137
	v_fmac_f32_e32 v184, s25, v138
	v_fmac_f32_e32 v185, s25, v139
	s_waitcnt vmcnt(31)
	v_readlane_b32 s25, v246, 46
	v_cvt_f32_ubyte0_e32 v124, v52
	v_cvt_f32_ubyte1_e32 v125, v52
	v_cvt_f32_ubyte2_e32 v126, v52
	v_cvt_f32_ubyte3_e32 v127, v52
	v_cvt_f32_ubyte0_e32 v128, v53
	v_cvt_f32_ubyte1_e32 v129, v53
	v_cvt_f32_ubyte2_e32 v130, v53
	v_cvt_f32_ubyte3_e32 v131, v53
	v_readlane_b32 s30, v121, 14
	s_lshl_b32 s30, s30, 12
	s_add_u32 s28, s26, s30
	s_addc_u32 s29, s27, 0
	global_load_dwordx2 v[52:53], v162, s[28:29]
	v_fmac_f32_e32 v178, s25, v124
	v_fmac_f32_e32 v179, s25, v125
	v_fmac_f32_e32 v180, s25, v126
	v_fmac_f32_e32 v181, s25, v127
	v_fmac_f32_e32 v182, s25, v128
	v_fmac_f32_e32 v183, s25, v129
	v_fmac_f32_e32 v184, s25, v130
	v_fmac_f32_e32 v185, s25, v131
	s_waitcnt vmcnt(31)
	v_readlane_b32 s25, v246, 47
	v_cvt_f32_ubyte0_e32 v132, v54
	v_cvt_f32_ubyte1_e32 v133, v54
	v_cvt_f32_ubyte2_e32 v134, v54
	v_cvt_f32_ubyte3_e32 v135, v54
	v_cvt_f32_ubyte0_e32 v136, v55
	v_cvt_f32_ubyte1_e32 v137, v55
	v_cvt_f32_ubyte2_e32 v138, v55
	v_cvt_f32_ubyte3_e32 v139, v55
	v_readlane_b32 s30, v121, 15
	s_lshl_b32 s30, s30, 12
	s_add_u32 s28, s26, s30
	s_addc_u32 s29, s27, 0
	global_load_dwordx2 v[54:55], v162, s[28:29]
	v_fmac_f32_e32 v178, s25, v132
	v_fmac_f32_e32 v179, s25, v133
	v_fmac_f32_e32 v180, s25, v134
	v_fmac_f32_e32 v181, s25, v135
	v_fmac_f32_e32 v182, s25, v136
	v_fmac_f32_e32 v183, s25, v137
	v_fmac_f32_e32 v184, s25, v138
	v_fmac_f32_e32 v185, s25, v139
	s_waitcnt vmcnt(31)
	v_readlane_b32 s25, v246, 48
	v_cvt_f32_ubyte0_e32 v124, v56
	v_cvt_f32_ubyte1_e32 v125, v56
	v_cvt_f32_ubyte2_e32 v126, v56
	v_cvt_f32_ubyte3_e32 v127, v56
	v_cvt_f32_ubyte0_e32 v128, v57
	v_cvt_f32_ubyte1_e32 v129, v57
	v_cvt_f32_ubyte2_e32 v130, v57
	v_cvt_f32_ubyte3_e32 v131, v57
	v_readlane_b32 s30, v121, 16
	s_lshl_b32 s30, s30, 12
	s_add_u32 s28, s26, s30
	s_addc_u32 s29, s27, 0
	global_load_dwordx2 v[56:57], v162, s[28:29]
	v_fmac_f32_e32 v178, s25, v124
	v_fmac_f32_e32 v179, s25, v125
	v_fmac_f32_e32 v180, s25, v126
	v_fmac_f32_e32 v181, s25, v127
	v_fmac_f32_e32 v182, s25, v128
	v_fmac_f32_e32 v183, s25, v129
	v_fmac_f32_e32 v184, s25, v130
	v_fmac_f32_e32 v185, s25, v131
	s_waitcnt vmcnt(31)
	v_readlane_b32 s25, v246, 49
	v_cvt_f32_ubyte0_e32 v132, v58
	v_cvt_f32_ubyte1_e32 v133, v58
	v_cvt_f32_ubyte2_e32 v134, v58
	v_cvt_f32_ubyte3_e32 v135, v58
	v_cvt_f32_ubyte0_e32 v136, v59
	v_cvt_f32_ubyte1_e32 v137, v59
	v_cvt_f32_ubyte2_e32 v138, v59
	v_cvt_f32_ubyte3_e32 v139, v59
	v_readlane_b32 s30, v121, 17
	s_lshl_b32 s30, s30, 12
	s_add_u32 s28, s26, s30
	s_addc_u32 s29, s27, 0
	global_load_dwordx2 v[58:59], v162, s[28:29]
	v_fmac_f32_e32 v178, s25, v132
	v_fmac_f32_e32 v179, s25, v133
	v_fmac_f32_e32 v180, s25, v134
	v_fmac_f32_e32 v181, s25, v135
	v_fmac_f32_e32 v182, s25, v136
	v_fmac_f32_e32 v183, s25, v137
	v_fmac_f32_e32 v184, s25, v138
	v_fmac_f32_e32 v185, s25, v139
	s_waitcnt vmcnt(31)
	v_readlane_b32 s25, v246, 50
	v_cvt_f32_ubyte0_e32 v124, v60
	v_cvt_f32_ubyte1_e32 v125, v60
	v_cvt_f32_ubyte2_e32 v126, v60
	v_cvt_f32_ubyte3_e32 v127, v60
	v_cvt_f32_ubyte0_e32 v128, v61
	v_cvt_f32_ubyte1_e32 v129, v61
	v_cvt_f32_ubyte2_e32 v130, v61
	v_cvt_f32_ubyte3_e32 v131, v61
	v_readlane_b32 s30, v121, 18
	s_lshl_b32 s30, s30, 12
	s_add_u32 s28, s26, s30
	s_addc_u32 s29, s27, 0
	global_load_dwordx2 v[60:61], v162, s[28:29]
	v_fmac_f32_e32 v178, s25, v124
	v_fmac_f32_e32 v179, s25, v125
	v_fmac_f32_e32 v180, s25, v126
	v_fmac_f32_e32 v181, s25, v127
	v_fmac_f32_e32 v182, s25, v128
	v_fmac_f32_e32 v183, s25, v129
	v_fmac_f32_e32 v184, s25, v130
	v_fmac_f32_e32 v185, s25, v131
	s_waitcnt vmcnt(31)
	v_readlane_b32 s25, v246, 51
	v_cvt_f32_ubyte0_e32 v132, v62
	v_cvt_f32_ubyte1_e32 v133, v62
	v_cvt_f32_ubyte2_e32 v134, v62
	v_cvt_f32_ubyte3_e32 v135, v62
	v_cvt_f32_ubyte0_e32 v136, v63
	v_cvt_f32_ubyte1_e32 v137, v63
	v_cvt_f32_ubyte2_e32 v138, v63
	v_cvt_f32_ubyte3_e32 v139, v63
	v_readlane_b32 s30, v121, 19
	s_lshl_b32 s30, s30, 12
	s_add_u32 s28, s26, s30
	s_addc_u32 s29, s27, 0
	global_load_dwordx2 v[62:63], v162, s[28:29]
	v_fmac_f32_e32 v178, s25, v132
	v_fmac_f32_e32 v179, s25, v133
	v_fmac_f32_e32 v180, s25, v134
	v_fmac_f32_e32 v181, s25, v135
	v_fmac_f32_e32 v182, s25, v136
	v_fmac_f32_e32 v183, s25, v137
	v_fmac_f32_e32 v184, s25, v138
	v_fmac_f32_e32 v185, s25, v139
	s_waitcnt vmcnt(31)
	v_readlane_b32 s25, v246, 52
	v_cvt_f32_ubyte0_e32 v124, v64
	v_cvt_f32_ubyte1_e32 v125, v64
	v_cvt_f32_ubyte2_e32 v126, v64
	v_cvt_f32_ubyte3_e32 v127, v64
	v_cvt_f32_ubyte0_e32 v128, v65
	v_cvt_f32_ubyte1_e32 v129, v65
	v_cvt_f32_ubyte2_e32 v130, v65
	v_cvt_f32_ubyte3_e32 v131, v65
	v_readlane_b32 s30, v121, 20
	s_lshl_b32 s30, s30, 12
	s_add_u32 s28, s26, s30
	s_addc_u32 s29, s27, 0
	global_load_dwordx2 v[64:65], v162, s[28:29]
	v_fmac_f32_e32 v178, s25, v124
	v_fmac_f32_e32 v179, s25, v125
	v_fmac_f32_e32 v180, s25, v126
	v_fmac_f32_e32 v181, s25, v127
	v_fmac_f32_e32 v182, s25, v128
	v_fmac_f32_e32 v183, s25, v129
	v_fmac_f32_e32 v184, s25, v130
	v_fmac_f32_e32 v185, s25, v131
	s_waitcnt vmcnt(31)
	v_readlane_b32 s25, v246, 53
	v_cvt_f32_ubyte0_e32 v132, v66
	v_cvt_f32_ubyte1_e32 v133, v66
	v_cvt_f32_ubyte2_e32 v134, v66
	v_cvt_f32_ubyte3_e32 v135, v66
	v_cvt_f32_ubyte0_e32 v136, v67
	v_cvt_f32_ubyte1_e32 v137, v67
	v_cvt_f32_ubyte2_e32 v138, v67
	v_cvt_f32_ubyte3_e32 v139, v67
	v_readlane_b32 s30, v121, 21
	s_lshl_b32 s30, s30, 12
	s_add_u32 s28, s26, s30
	s_addc_u32 s29, s27, 0
	global_load_dwordx2 v[66:67], v162, s[28:29]
	v_fmac_f32_e32 v178, s25, v132
	v_fmac_f32_e32 v179, s25, v133
	v_fmac_f32_e32 v180, s25, v134
	v_fmac_f32_e32 v181, s25, v135
	v_fmac_f32_e32 v182, s25, v136
	v_fmac_f32_e32 v183, s25, v137
	v_fmac_f32_e32 v184, s25, v138
	v_fmac_f32_e32 v185, s25, v139
	s_waitcnt vmcnt(31)
	v_readlane_b32 s25, v246, 54
	v_cvt_f32_ubyte0_e32 v124, v68
	v_cvt_f32_ubyte1_e32 v125, v68
	v_cvt_f32_ubyte2_e32 v126, v68
	v_cvt_f32_ubyte3_e32 v127, v68
	v_cvt_f32_ubyte0_e32 v128, v69
	v_cvt_f32_ubyte1_e32 v129, v69
	v_cvt_f32_ubyte2_e32 v130, v69
	v_cvt_f32_ubyte3_e32 v131, v69
	v_readlane_b32 s30, v121, 22
	s_lshl_b32 s30, s30, 12
	s_add_u32 s28, s26, s30
	s_addc_u32 s29, s27, 0
	global_load_dwordx2 v[68:69], v162, s[28:29]
	v_fmac_f32_e32 v178, s25, v124
	v_fmac_f32_e32 v179, s25, v125
	v_fmac_f32_e32 v180, s25, v126
	v_fmac_f32_e32 v181, s25, v127
	v_fmac_f32_e32 v182, s25, v128
	v_fmac_f32_e32 v183, s25, v129
	v_fmac_f32_e32 v184, s25, v130
	v_fmac_f32_e32 v185, s25, v131
	s_waitcnt vmcnt(31)
	v_readlane_b32 s25, v246, 55
	v_cvt_f32_ubyte0_e32 v132, v70
	v_cvt_f32_ubyte1_e32 v133, v70
	v_cvt_f32_ubyte2_e32 v134, v70
	v_cvt_f32_ubyte3_e32 v135, v70
	v_cvt_f32_ubyte0_e32 v136, v71
	v_cvt_f32_ubyte1_e32 v137, v71
	v_cvt_f32_ubyte2_e32 v138, v71
	v_cvt_f32_ubyte3_e32 v139, v71
	v_readlane_b32 s30, v121, 23
	s_lshl_b32 s30, s30, 12
	s_add_u32 s28, s26, s30
	s_addc_u32 s29, s27, 0
	global_load_dwordx2 v[70:71], v162, s[28:29]
	v_fmac_f32_e32 v178, s25, v132
	v_fmac_f32_e32 v179, s25, v133
	v_fmac_f32_e32 v180, s25, v134
	v_fmac_f32_e32 v181, s25, v135
	v_fmac_f32_e32 v182, s25, v136
	v_fmac_f32_e32 v183, s25, v137
	v_fmac_f32_e32 v184, s25, v138
	v_fmac_f32_e32 v185, s25, v139
	s_waitcnt vmcnt(31)
	v_readlane_b32 s25, v246, 56
	v_cvt_f32_ubyte0_e32 v124, v72
	v_cvt_f32_ubyte1_e32 v125, v72
	v_cvt_f32_ubyte2_e32 v126, v72
	v_cvt_f32_ubyte3_e32 v127, v72
	v_cvt_f32_ubyte0_e32 v128, v73
	v_cvt_f32_ubyte1_e32 v129, v73
	v_cvt_f32_ubyte2_e32 v130, v73
	v_cvt_f32_ubyte3_e32 v131, v73
	v_readlane_b32 s30, v121, 24
	s_lshl_b32 s30, s30, 12
	s_add_u32 s28, s26, s30
	s_addc_u32 s29, s27, 0
	global_load_dwordx2 v[72:73], v162, s[28:29]
	v_fmac_f32_e32 v178, s25, v124
	v_fmac_f32_e32 v179, s25, v125
	v_fmac_f32_e32 v180, s25, v126
	v_fmac_f32_e32 v181, s25, v127
	v_fmac_f32_e32 v182, s25, v128
	v_fmac_f32_e32 v183, s25, v129
	v_fmac_f32_e32 v184, s25, v130
	v_fmac_f32_e32 v185, s25, v131
	s_waitcnt vmcnt(31)
	v_readlane_b32 s25, v246, 57
	v_cvt_f32_ubyte0_e32 v132, v74
	v_cvt_f32_ubyte1_e32 v133, v74
	v_cvt_f32_ubyte2_e32 v134, v74
	v_cvt_f32_ubyte3_e32 v135, v74
	v_cvt_f32_ubyte0_e32 v136, v75
	v_cvt_f32_ubyte1_e32 v137, v75
	v_cvt_f32_ubyte2_e32 v138, v75
	v_cvt_f32_ubyte3_e32 v139, v75
	v_readlane_b32 s30, v121, 25
	s_lshl_b32 s30, s30, 12
	s_add_u32 s28, s26, s30
	s_addc_u32 s29, s27, 0
	global_load_dwordx2 v[74:75], v162, s[28:29]
	v_fmac_f32_e32 v178, s25, v132
	v_fmac_f32_e32 v179, s25, v133
	v_fmac_f32_e32 v180, s25, v134
	v_fmac_f32_e32 v181, s25, v135
	v_fmac_f32_e32 v182, s25, v136
	v_fmac_f32_e32 v183, s25, v137
	v_fmac_f32_e32 v184, s25, v138
	v_fmac_f32_e32 v185, s25, v139
	s_waitcnt vmcnt(31)
	v_readlane_b32 s25, v246, 58
	v_cvt_f32_ubyte0_e32 v124, v76
	v_cvt_f32_ubyte1_e32 v125, v76
	v_cvt_f32_ubyte2_e32 v126, v76
	v_cvt_f32_ubyte3_e32 v127, v76
	v_cvt_f32_ubyte0_e32 v128, v77
	v_cvt_f32_ubyte1_e32 v129, v77
	v_cvt_f32_ubyte2_e32 v130, v77
	v_cvt_f32_ubyte3_e32 v131, v77
	v_readlane_b32 s30, v121, 26
	s_lshl_b32 s30, s30, 12
	s_add_u32 s28, s26, s30
	s_addc_u32 s29, s27, 0
	global_load_dwordx2 v[76:77], v162, s[28:29]
	v_fmac_f32_e32 v178, s25, v124
	v_fmac_f32_e32 v179, s25, v125
	v_fmac_f32_e32 v180, s25, v126
	v_fmac_f32_e32 v181, s25, v127
	v_fmac_f32_e32 v182, s25, v128
	v_fmac_f32_e32 v183, s25, v129
	v_fmac_f32_e32 v184, s25, v130
	v_fmac_f32_e32 v185, s25, v131
	s_waitcnt vmcnt(31)
	v_readlane_b32 s25, v246, 59
	v_cvt_f32_ubyte0_e32 v132, v78
	v_cvt_f32_ubyte1_e32 v133, v78
	v_cvt_f32_ubyte2_e32 v134, v78
	v_cvt_f32_ubyte3_e32 v135, v78
	v_cvt_f32_ubyte0_e32 v136, v79
	v_cvt_f32_ubyte1_e32 v137, v79
	v_cvt_f32_ubyte2_e32 v138, v79
	v_cvt_f32_ubyte3_e32 v139, v79
	v_readlane_b32 s30, v121, 27
	s_lshl_b32 s30, s30, 12
	s_add_u32 s28, s26, s30
	s_addc_u32 s29, s27, 0
	global_load_dwordx2 v[78:79], v162, s[28:29]
	v_fmac_f32_e32 v178, s25, v132
	v_fmac_f32_e32 v179, s25, v133
	v_fmac_f32_e32 v180, s25, v134
	v_fmac_f32_e32 v181, s25, v135
	v_fmac_f32_e32 v182, s25, v136
	v_fmac_f32_e32 v183, s25, v137
	v_fmac_f32_e32 v184, s25, v138
	v_fmac_f32_e32 v185, s25, v139
	s_waitcnt vmcnt(31)
	v_readlane_b32 s25, v246, 60
	v_cvt_f32_ubyte0_e32 v124, v80
	v_cvt_f32_ubyte1_e32 v125, v80
	v_cvt_f32_ubyte2_e32 v126, v80
	v_cvt_f32_ubyte3_e32 v127, v80
	v_cvt_f32_ubyte0_e32 v128, v81
	v_cvt_f32_ubyte1_e32 v129, v81
	v_cvt_f32_ubyte2_e32 v130, v81
	v_cvt_f32_ubyte3_e32 v131, v81
	v_readlane_b32 s30, v121, 28
	s_lshl_b32 s30, s30, 12
	s_add_u32 s28, s26, s30
	s_addc_u32 s29, s27, 0
	global_load_dwordx2 v[80:81], v162, s[28:29]
	v_fmac_f32_e32 v178, s25, v124
	v_fmac_f32_e32 v179, s25, v125
	v_fmac_f32_e32 v180, s25, v126
	v_fmac_f32_e32 v181, s25, v127
	v_fmac_f32_e32 v182, s25, v128
	v_fmac_f32_e32 v183, s25, v129
	v_fmac_f32_e32 v184, s25, v130
	v_fmac_f32_e32 v185, s25, v131
	s_waitcnt vmcnt(31)
	v_readlane_b32 s25, v246, 61
	v_cvt_f32_ubyte0_e32 v132, v82
	v_cvt_f32_ubyte1_e32 v133, v82
	v_cvt_f32_ubyte2_e32 v134, v82
	v_cvt_f32_ubyte3_e32 v135, v82
	v_cvt_f32_ubyte0_e32 v136, v83
	v_cvt_f32_ubyte1_e32 v137, v83
	v_cvt_f32_ubyte2_e32 v138, v83
	v_cvt_f32_ubyte3_e32 v139, v83
	v_readlane_b32 s30, v121, 29
	s_lshl_b32 s30, s30, 12
	s_add_u32 s28, s26, s30
	s_addc_u32 s29, s27, 0
	global_load_dwordx2 v[82:83], v162, s[28:29]
	v_fmac_f32_e32 v178, s25, v132
	v_fmac_f32_e32 v179, s25, v133
	v_fmac_f32_e32 v180, s25, v134
	v_fmac_f32_e32 v181, s25, v135
	v_fmac_f32_e32 v182, s25, v136
	v_fmac_f32_e32 v183, s25, v137
	v_fmac_f32_e32 v184, s25, v138
	v_fmac_f32_e32 v185, s25, v139
	s_waitcnt vmcnt(31)
	v_readlane_b32 s25, v246, 62
	v_cvt_f32_ubyte0_e32 v124, v84
	v_cvt_f32_ubyte1_e32 v125, v84
	v_cvt_f32_ubyte2_e32 v126, v84
	v_cvt_f32_ubyte3_e32 v127, v84
	v_cvt_f32_ubyte0_e32 v128, v85
	v_cvt_f32_ubyte1_e32 v129, v85
	v_cvt_f32_ubyte2_e32 v130, v85
	v_cvt_f32_ubyte3_e32 v131, v85
	v_readlane_b32 s30, v121, 30
	s_lshl_b32 s30, s30, 12
	s_add_u32 s28, s26, s30
	s_addc_u32 s29, s27, 0
	global_load_dwordx2 v[84:85], v162, s[28:29]
	v_fmac_f32_e32 v178, s25, v124
	v_fmac_f32_e32 v179, s25, v125
	v_fmac_f32_e32 v180, s25, v126
	v_fmac_f32_e32 v181, s25, v127
	v_fmac_f32_e32 v182, s25, v128
	v_fmac_f32_e32 v183, s25, v129
	v_fmac_f32_e32 v184, s25, v130
	v_fmac_f32_e32 v185, s25, v131
	s_waitcnt vmcnt(31)
	v_readlane_b32 s25, v246, 63
	v_cvt_f32_ubyte0_e32 v132, v86
	v_cvt_f32_ubyte1_e32 v133, v86
	v_cvt_f32_ubyte2_e32 v134, v86
	v_cvt_f32_ubyte3_e32 v135, v86
	v_cvt_f32_ubyte0_e32 v136, v87
	v_cvt_f32_ubyte1_e32 v137, v87
	v_cvt_f32_ubyte2_e32 v138, v87
	v_cvt_f32_ubyte3_e32 v139, v87
	v_readlane_b32 s30, v121, 31
	s_lshl_b32 s30, s30, 12
	s_add_u32 s28, s26, s30
	s_addc_u32 s29, s27, 0
	global_load_dwordx2 v[86:87], v162, s[28:29]
	v_fmac_f32_e32 v178, s25, v132
	v_fmac_f32_e32 v179, s25, v133
	v_fmac_f32_e32 v180, s25, v134
	v_fmac_f32_e32 v181, s25, v135
	v_fmac_f32_e32 v182, s25, v136
	v_fmac_f32_e32 v183, s25, v137
	v_fmac_f32_e32 v184, s25, v138
	v_fmac_f32_e32 v185, s25, v139
	s_waitcnt vmcnt(31)
	v_readlane_b32 s25, v247, 0
	v_cvt_f32_ubyte0_e32 v124, v24
	v_cvt_f32_ubyte1_e32 v125, v24
	v_cvt_f32_ubyte2_e32 v126, v24
	v_cvt_f32_ubyte3_e32 v127, v24
	v_cvt_f32_ubyte0_e32 v128, v25
	v_cvt_f32_ubyte1_e32 v129, v25
	v_cvt_f32_ubyte2_e32 v130, v25
	v_cvt_f32_ubyte3_e32 v131, v25
	v_readlane_b32 s30, v121, 32
	s_lshl_b32 s30, s30, 12
	s_add_u32 s28, s26, s30
	s_addc_u32 s29, s27, 0
	global_load_dwordx2 v[24:25], v162, s[28:29]
	v_lshlrev_b32_e32 v16, 2, v122
	v_lshlrev_b32_e32 v17, 2, v123
	global_load_dword v238, v16, s[64:65]
	global_load_dword v240, v16, s[60:61]
	global_load_dword v239, v17, s[64:65]
	global_load_dword v241, v17, s[60:61]
	v_fmac_f32_e32 v178, s25, v124
	v_fmac_f32_e32 v179, s25, v125
	v_fmac_f32_e32 v180, s25, v126
	v_fmac_f32_e32 v181, s25, v127
	v_fmac_f32_e32 v182, s25, v128
	v_fmac_f32_e32 v183, s25, v129
	v_fmac_f32_e32 v184, s25, v130
	v_fmac_f32_e32 v185, s25, v131
	s_waitcnt vmcnt(35)
	v_readlane_b32 s25, v247, 1
	v_cvt_f32_ubyte0_e32 v132, v26
	v_cvt_f32_ubyte1_e32 v133, v26
	v_cvt_f32_ubyte2_e32 v134, v26
	v_cvt_f32_ubyte3_e32 v135, v26
	v_cvt_f32_ubyte0_e32 v136, v27
	v_cvt_f32_ubyte1_e32 v137, v27
	v_cvt_f32_ubyte2_e32 v138, v27
	v_cvt_f32_ubyte3_e32 v139, v27
	v_readlane_b32 s30, v121, 33
	s_lshl_b32 s30, s30, 12
	s_add_u32 s28, s26, s30
	s_addc_u32 s29, s27, 0
	global_load_dwordx2 v[26:27], v162, s[28:29]
	v_fmac_f32_e32 v178, s25, v132
	v_fmac_f32_e32 v179, s25, v133
	v_fmac_f32_e32 v180, s25, v134
	v_fmac_f32_e32 v181, s25, v135
	v_fmac_f32_e32 v182, s25, v136
	v_fmac_f32_e32 v183, s25, v137
	v_fmac_f32_e32 v184, s25, v138
	v_fmac_f32_e32 v185, s25, v139
	s_waitcnt vmcnt(35)
	v_readlane_b32 s25, v247, 2
	v_cvt_f32_ubyte0_e32 v124, v28
	v_cvt_f32_ubyte1_e32 v125, v28
	v_cvt_f32_ubyte2_e32 v126, v28
	v_cvt_f32_ubyte3_e32 v127, v28
	v_cvt_f32_ubyte0_e32 v128, v29
	v_cvt_f32_ubyte1_e32 v129, v29
	v_cvt_f32_ubyte2_e32 v130, v29
	v_cvt_f32_ubyte3_e32 v131, v29
	v_readlane_b32 s30, v121, 34
	s_lshl_b32 s30, s30, 12
	s_add_u32 s28, s26, s30
	s_addc_u32 s29, s27, 0
	global_load_dwordx2 v[28:29], v162, s[28:29]
	v_fmac_f32_e32 v178, s25, v124
	v_fmac_f32_e32 v179, s25, v125
	v_fmac_f32_e32 v180, s25, v126
	v_fmac_f32_e32 v181, s25, v127
	v_fmac_f32_e32 v182, s25, v128
	v_fmac_f32_e32 v183, s25, v129
	v_fmac_f32_e32 v184, s25, v130
	v_fmac_f32_e32 v185, s25, v131
	s_waitcnt vmcnt(35)
	v_readlane_b32 s25, v247, 3
	v_cvt_f32_ubyte0_e32 v132, v30
	v_cvt_f32_ubyte1_e32 v133, v30
	v_cvt_f32_ubyte2_e32 v134, v30
	v_cvt_f32_ubyte3_e32 v135, v30
	v_cvt_f32_ubyte0_e32 v136, v31
	v_cvt_f32_ubyte1_e32 v137, v31
	v_cvt_f32_ubyte2_e32 v138, v31
	v_cvt_f32_ubyte3_e32 v139, v31
	v_readlane_b32 s30, v121, 35
	s_lshl_b32 s30, s30, 12
	s_add_u32 s28, s26, s30
	s_addc_u32 s29, s27, 0
	global_load_dwordx2 v[30:31], v162, s[28:29]
	v_fmac_f32_e32 v178, s25, v132
	v_fmac_f32_e32 v179, s25, v133
	v_fmac_f32_e32 v180, s25, v134
	v_fmac_f32_e32 v181, s25, v135
	v_fmac_f32_e32 v182, s25, v136
	v_fmac_f32_e32 v183, s25, v137
	v_fmac_f32_e32 v184, s25, v138
	v_fmac_f32_e32 v185, s25, v139
	s_waitcnt vmcnt(35)
	v_readlane_b32 s25, v247, 4
	v_cvt_f32_ubyte0_e32 v124, v32
	v_cvt_f32_ubyte1_e32 v125, v32
	v_cvt_f32_ubyte2_e32 v126, v32
	v_cvt_f32_ubyte3_e32 v127, v32
	v_cvt_f32_ubyte0_e32 v128, v33
	v_cvt_f32_ubyte1_e32 v129, v33
	v_cvt_f32_ubyte2_e32 v130, v33
	v_cvt_f32_ubyte3_e32 v131, v33
	v_readlane_b32 s30, v121, 36
	s_lshl_b32 s30, s30, 12
	s_add_u32 s28, s26, s30
	s_addc_u32 s29, s27, 0
	global_load_dwordx2 v[32:33], v162, s[28:29]
	v_fmac_f32_e32 v178, s25, v124
	v_fmac_f32_e32 v179, s25, v125
	v_fmac_f32_e32 v180, s25, v126
	v_fmac_f32_e32 v181, s25, v127
	v_fmac_f32_e32 v182, s25, v128
	v_fmac_f32_e32 v183, s25, v129
	v_fmac_f32_e32 v184, s25, v130
	v_fmac_f32_e32 v185, s25, v131
	s_waitcnt vmcnt(35)
	v_readlane_b32 s25, v247, 5
	v_cvt_f32_ubyte0_e32 v132, v34
	v_cvt_f32_ubyte1_e32 v133, v34
	v_cvt_f32_ubyte2_e32 v134, v34
	v_cvt_f32_ubyte3_e32 v135, v34
	v_cvt_f32_ubyte0_e32 v136, v35
	v_cvt_f32_ubyte1_e32 v137, v35
	v_cvt_f32_ubyte2_e32 v138, v35
	v_cvt_f32_ubyte3_e32 v139, v35
	v_readlane_b32 s30, v121, 37
	s_lshl_b32 s30, s30, 12
	s_add_u32 s28, s26, s30
	s_addc_u32 s29, s27, 0
	global_load_dwordx2 v[34:35], v162, s[28:29]
	v_fmac_f32_e32 v178, s25, v132
	v_fmac_f32_e32 v179, s25, v133
	v_fmac_f32_e32 v180, s25, v134
	v_fmac_f32_e32 v181, s25, v135
	v_fmac_f32_e32 v182, s25, v136
	v_fmac_f32_e32 v183, s25, v137
	v_fmac_f32_e32 v184, s25, v138
	v_fmac_f32_e32 v185, s25, v139
	s_waitcnt vmcnt(35)
	v_readlane_b32 s25, v247, 6
	v_cvt_f32_ubyte0_e32 v124, v36
	v_cvt_f32_ubyte1_e32 v125, v36
	v_cvt_f32_ubyte2_e32 v126, v36
	v_cvt_f32_ubyte3_e32 v127, v36
	v_cvt_f32_ubyte0_e32 v128, v37
	v_cvt_f32_ubyte1_e32 v129, v37
	v_cvt_f32_ubyte2_e32 v130, v37
	v_cvt_f32_ubyte3_e32 v131, v37
	v_readlane_b32 s30, v121, 38
	s_lshl_b32 s30, s30, 12
	s_add_u32 s28, s26, s30
	s_addc_u32 s29, s27, 0
	global_load_dwordx2 v[36:37], v162, s[28:29]
	v_fmac_f32_e32 v178, s25, v124
	v_fmac_f32_e32 v179, s25, v125
	v_fmac_f32_e32 v180, s25, v126
	v_fmac_f32_e32 v181, s25, v127
	v_fmac_f32_e32 v182, s25, v128
	v_fmac_f32_e32 v183, s25, v129
	v_fmac_f32_e32 v184, s25, v130
	v_fmac_f32_e32 v185, s25, v131
	s_waitcnt vmcnt(35)
	v_readlane_b32 s25, v247, 7
	v_cvt_f32_ubyte0_e32 v132, v38
	v_cvt_f32_ubyte1_e32 v133, v38
	v_cvt_f32_ubyte2_e32 v134, v38
	v_cvt_f32_ubyte3_e32 v135, v38
	v_cvt_f32_ubyte0_e32 v136, v39
	v_cvt_f32_ubyte1_e32 v137, v39
	v_cvt_f32_ubyte2_e32 v138, v39
	v_cvt_f32_ubyte3_e32 v139, v39
	v_readlane_b32 s30, v121, 39
	s_lshl_b32 s30, s30, 12
	s_add_u32 s28, s26, s30
	s_addc_u32 s29, s27, 0
	global_load_dwordx2 v[38:39], v162, s[28:29]
	v_fmac_f32_e32 v178, s25, v132
	v_fmac_f32_e32 v179, s25, v133
	v_fmac_f32_e32 v180, s25, v134
	v_fmac_f32_e32 v181, s25, v135
	v_fmac_f32_e32 v182, s25, v136
	v_fmac_f32_e32 v183, s25, v137
	v_fmac_f32_e32 v184, s25, v138
	v_fmac_f32_e32 v185, s25, v139
	s_waitcnt vmcnt(35)
	v_readlane_b32 s25, v247, 8
	v_cvt_f32_ubyte0_e32 v124, v40
	v_cvt_f32_ubyte1_e32 v125, v40
	v_cvt_f32_ubyte2_e32 v126, v40
	v_cvt_f32_ubyte3_e32 v127, v40
	v_cvt_f32_ubyte0_e32 v128, v41
	v_cvt_f32_ubyte1_e32 v129, v41
	v_cvt_f32_ubyte2_e32 v130, v41
	v_cvt_f32_ubyte3_e32 v131, v41
	v_readlane_b32 s30, v121, 40
	s_lshl_b32 s30, s30, 12
	s_add_u32 s28, s26, s30
	s_addc_u32 s29, s27, 0
	global_load_dwordx2 v[40:41], v162, s[28:29]
	v_fmac_f32_e32 v178, s25, v124
	v_fmac_f32_e32 v179, s25, v125
	v_fmac_f32_e32 v180, s25, v126
	v_fmac_f32_e32 v181, s25, v127
	v_fmac_f32_e32 v182, s25, v128
	v_fmac_f32_e32 v183, s25, v129
	v_fmac_f32_e32 v184, s25, v130
	v_fmac_f32_e32 v185, s25, v131
	s_waitcnt vmcnt(35)
	v_readlane_b32 s25, v247, 9
	v_cvt_f32_ubyte0_e32 v132, v42
	v_cvt_f32_ubyte1_e32 v133, v42
	v_cvt_f32_ubyte2_e32 v134, v42
	v_cvt_f32_ubyte3_e32 v135, v42
	v_cvt_f32_ubyte0_e32 v136, v43
	v_cvt_f32_ubyte1_e32 v137, v43
	v_cvt_f32_ubyte2_e32 v138, v43
	v_cvt_f32_ubyte3_e32 v139, v43
	v_readlane_b32 s30, v121, 41
	s_lshl_b32 s30, s30, 12
	s_add_u32 s28, s26, s30
	s_addc_u32 s29, s27, 0
	global_load_dwordx2 v[42:43], v162, s[28:29]
	v_fmac_f32_e32 v178, s25, v132
	v_fmac_f32_e32 v179, s25, v133
	v_fmac_f32_e32 v180, s25, v134
	v_fmac_f32_e32 v181, s25, v135
	v_fmac_f32_e32 v182, s25, v136
	v_fmac_f32_e32 v183, s25, v137
	v_fmac_f32_e32 v184, s25, v138
	v_fmac_f32_e32 v185, s25, v139
	s_waitcnt vmcnt(35)
	v_readlane_b32 s25, v247, 10
	v_cvt_f32_ubyte0_e32 v124, v44
	v_cvt_f32_ubyte1_e32 v125, v44
	v_cvt_f32_ubyte2_e32 v126, v44
	v_cvt_f32_ubyte3_e32 v127, v44
	v_cvt_f32_ubyte0_e32 v128, v45
	v_cvt_f32_ubyte1_e32 v129, v45
	v_cvt_f32_ubyte2_e32 v130, v45
	v_cvt_f32_ubyte3_e32 v131, v45
	v_readlane_b32 s30, v121, 42
	s_lshl_b32 s30, s30, 12
	s_add_u32 s28, s26, s30
	s_addc_u32 s29, s27, 0
	global_load_dwordx2 v[44:45], v162, s[28:29]
	v_fmac_f32_e32 v178, s25, v124
	v_fmac_f32_e32 v179, s25, v125
	v_fmac_f32_e32 v180, s25, v126
	v_fmac_f32_e32 v181, s25, v127
	v_fmac_f32_e32 v182, s25, v128
	v_fmac_f32_e32 v183, s25, v129
	v_fmac_f32_e32 v184, s25, v130
	v_fmac_f32_e32 v185, s25, v131
	s_waitcnt vmcnt(35)
	v_readlane_b32 s25, v247, 11
	v_cvt_f32_ubyte0_e32 v132, v46
	v_cvt_f32_ubyte1_e32 v133, v46
	v_cvt_f32_ubyte2_e32 v134, v46
	v_cvt_f32_ubyte3_e32 v135, v46
	v_cvt_f32_ubyte0_e32 v136, v47
	v_cvt_f32_ubyte1_e32 v137, v47
	v_cvt_f32_ubyte2_e32 v138, v47
	v_cvt_f32_ubyte3_e32 v139, v47
	v_readlane_b32 s30, v121, 43
	s_lshl_b32 s30, s30, 12
	s_add_u32 s28, s26, s30
	s_addc_u32 s29, s27, 0
	global_load_dwordx2 v[46:47], v162, s[28:29]
	v_fmac_f32_e32 v178, s25, v132
	v_fmac_f32_e32 v179, s25, v133
	v_fmac_f32_e32 v180, s25, v134
	v_fmac_f32_e32 v181, s25, v135
	v_fmac_f32_e32 v182, s25, v136
	v_fmac_f32_e32 v183, s25, v137
	v_fmac_f32_e32 v184, s25, v138
	v_fmac_f32_e32 v185, s25, v139
	s_waitcnt vmcnt(35)
	v_readlane_b32 s25, v247, 12
	v_cvt_f32_ubyte0_e32 v124, v48
	v_cvt_f32_ubyte1_e32 v125, v48
	v_cvt_f32_ubyte2_e32 v126, v48
	v_cvt_f32_ubyte3_e32 v127, v48
	v_cvt_f32_ubyte0_e32 v128, v49
	v_cvt_f32_ubyte1_e32 v129, v49
	v_cvt_f32_ubyte2_e32 v130, v49
	v_cvt_f32_ubyte3_e32 v131, v49
	v_readlane_b32 s30, v121, 44
	s_lshl_b32 s30, s30, 12
	s_add_u32 s28, s26, s30
	s_addc_u32 s29, s27, 0
	global_load_dwordx2 v[48:49], v162, s[28:29]
	v_fmac_f32_e32 v178, s25, v124
	v_fmac_f32_e32 v179, s25, v125
	v_fmac_f32_e32 v180, s25, v126
	v_fmac_f32_e32 v181, s25, v127
	v_fmac_f32_e32 v182, s25, v128
	v_fmac_f32_e32 v183, s25, v129
	v_fmac_f32_e32 v184, s25, v130
	v_fmac_f32_e32 v185, s25, v131
	s_waitcnt vmcnt(35)
	v_readlane_b32 s25, v247, 13
	v_cvt_f32_ubyte0_e32 v132, v50
	v_cvt_f32_ubyte1_e32 v133, v50
	v_cvt_f32_ubyte2_e32 v134, v50
	v_cvt_f32_ubyte3_e32 v135, v50
	v_cvt_f32_ubyte0_e32 v136, v51
	v_cvt_f32_ubyte1_e32 v137, v51
	v_cvt_f32_ubyte2_e32 v138, v51
	v_cvt_f32_ubyte3_e32 v139, v51
	v_readlane_b32 s30, v121, 45
	s_lshl_b32 s30, s30, 12
	s_add_u32 s28, s26, s30
	s_addc_u32 s29, s27, 0
	global_load_dwordx2 v[50:51], v162, s[28:29]
	v_fmac_f32_e32 v178, s25, v132
	v_fmac_f32_e32 v179, s25, v133
	v_fmac_f32_e32 v180, s25, v134
	v_fmac_f32_e32 v181, s25, v135
	v_fmac_f32_e32 v182, s25, v136
	v_fmac_f32_e32 v183, s25, v137
	v_fmac_f32_e32 v184, s25, v138
	v_fmac_f32_e32 v185, s25, v139
	s_waitcnt vmcnt(35)
	v_readlane_b32 s25, v247, 14
	v_cvt_f32_ubyte0_e32 v124, v52
	v_cvt_f32_ubyte1_e32 v125, v52
	v_cvt_f32_ubyte2_e32 v126, v52
	v_cvt_f32_ubyte3_e32 v127, v52
	v_cvt_f32_ubyte0_e32 v128, v53
	v_cvt_f32_ubyte1_e32 v129, v53
	v_cvt_f32_ubyte2_e32 v130, v53
	v_cvt_f32_ubyte3_e32 v131, v53
	v_readlane_b32 s30, v121, 46
	s_lshl_b32 s30, s30, 12
	s_add_u32 s28, s26, s30
	s_addc_u32 s29, s27, 0
	global_load_dwordx2 v[52:53], v162, s[28:29]
	v_fmac_f32_e32 v178, s25, v124
	v_fmac_f32_e32 v179, s25, v125
	v_fmac_f32_e32 v180, s25, v126
	v_fmac_f32_e32 v181, s25, v127
	v_fmac_f32_e32 v182, s25, v128
	v_fmac_f32_e32 v183, s25, v129
	v_fmac_f32_e32 v184, s25, v130
	v_fmac_f32_e32 v185, s25, v131
	s_waitcnt vmcnt(35)
	v_readlane_b32 s25, v247, 15
	v_cvt_f32_ubyte0_e32 v132, v54
	v_cvt_f32_ubyte1_e32 v133, v54
	v_cvt_f32_ubyte2_e32 v134, v54
	v_cvt_f32_ubyte3_e32 v135, v54
	v_cvt_f32_ubyte0_e32 v136, v55
	v_cvt_f32_ubyte1_e32 v137, v55
	v_cvt_f32_ubyte2_e32 v138, v55
	v_cvt_f32_ubyte3_e32 v139, v55
	v_readlane_b32 s30, v121, 47
	s_lshl_b32 s30, s30, 12
	s_add_u32 s28, s26, s30
	s_addc_u32 s29, s27, 0
	global_load_dwordx2 v[54:55], v162, s[28:29]
	v_fmac_f32_e32 v178, s25, v132
	v_fmac_f32_e32 v179, s25, v133
	v_fmac_f32_e32 v180, s25, v134
	v_fmac_f32_e32 v181, s25, v135
	v_fmac_f32_e32 v182, s25, v136
	v_fmac_f32_e32 v183, s25, v137
	v_fmac_f32_e32 v184, s25, v138
	v_fmac_f32_e32 v185, s25, v139
	s_waitcnt vmcnt(35)
	v_readlane_b32 s25, v247, 16
	v_cvt_f32_ubyte0_e32 v124, v56
	v_cvt_f32_ubyte1_e32 v125, v56
	v_cvt_f32_ubyte2_e32 v126, v56
	v_cvt_f32_ubyte3_e32 v127, v56
	v_cvt_f32_ubyte0_e32 v128, v57
	v_cvt_f32_ubyte1_e32 v129, v57
	v_cvt_f32_ubyte2_e32 v130, v57
	v_cvt_f32_ubyte3_e32 v131, v57
	v_readlane_b32 s30, v121, 48
	s_lshl_b32 s30, s30, 12
	s_add_u32 s28, s26, s30
	s_addc_u32 s29, s27, 0
	global_load_dwordx2 v[56:57], v162, s[28:29]
	v_fmac_f32_e32 v178, s25, v124
	v_fmac_f32_e32 v179, s25, v125
	v_fmac_f32_e32 v180, s25, v126
	v_fmac_f32_e32 v181, s25, v127
	v_fmac_f32_e32 v182, s25, v128
	v_fmac_f32_e32 v183, s25, v129
	v_fmac_f32_e32 v184, s25, v130
	v_fmac_f32_e32 v185, s25, v131
	s_waitcnt vmcnt(35)
	v_readlane_b32 s25, v247, 17
	v_cvt_f32_ubyte0_e32 v132, v58
	v_cvt_f32_ubyte1_e32 v133, v58
	v_cvt_f32_ubyte2_e32 v134, v58
	v_cvt_f32_ubyte3_e32 v135, v58
	v_cvt_f32_ubyte0_e32 v136, v59
	v_cvt_f32_ubyte1_e32 v137, v59
	v_cvt_f32_ubyte2_e32 v138, v59
	v_cvt_f32_ubyte3_e32 v139, v59
	v_readlane_b32 s30, v121, 49
	s_lshl_b32 s30, s30, 12
	s_add_u32 s28, s26, s30
	s_addc_u32 s29, s27, 0
	global_load_dwordx2 v[58:59], v162, s[28:29]
	v_fmac_f32_e32 v178, s25, v132
	v_fmac_f32_e32 v179, s25, v133
	v_fmac_f32_e32 v180, s25, v134
	v_fmac_f32_e32 v181, s25, v135
	v_fmac_f32_e32 v182, s25, v136
	v_fmac_f32_e32 v183, s25, v137
	v_fmac_f32_e32 v184, s25, v138
	v_fmac_f32_e32 v185, s25, v139
	s_waitcnt vmcnt(35)
	v_readlane_b32 s25, v247, 18
	v_cvt_f32_ubyte0_e32 v124, v60
	v_cvt_f32_ubyte1_e32 v125, v60
	v_cvt_f32_ubyte2_e32 v126, v60
	v_cvt_f32_ubyte3_e32 v127, v60
	v_cvt_f32_ubyte0_e32 v128, v61
	v_cvt_f32_ubyte1_e32 v129, v61
	v_cvt_f32_ubyte2_e32 v130, v61
	v_cvt_f32_ubyte3_e32 v131, v61
	v_readlane_b32 s30, v121, 50
	s_lshl_b32 s30, s30, 12
	s_add_u32 s28, s26, s30
	s_addc_u32 s29, s27, 0
	global_load_dwordx2 v[60:61], v162, s[28:29]
	v_fmac_f32_e32 v178, s25, v124
	v_fmac_f32_e32 v179, s25, v125
	v_fmac_f32_e32 v180, s25, v126
	v_fmac_f32_e32 v181, s25, v127
	v_fmac_f32_e32 v182, s25, v128
	v_fmac_f32_e32 v183, s25, v129
	v_fmac_f32_e32 v184, s25, v130
	v_fmac_f32_e32 v185, s25, v131
	s_waitcnt vmcnt(35)
	v_readlane_b32 s25, v247, 19
	v_cvt_f32_ubyte0_e32 v132, v62
	v_cvt_f32_ubyte1_e32 v133, v62
	v_cvt_f32_ubyte2_e32 v134, v62
	v_cvt_f32_ubyte3_e32 v135, v62
	v_cvt_f32_ubyte0_e32 v136, v63
	v_cvt_f32_ubyte1_e32 v137, v63
	v_cvt_f32_ubyte2_e32 v138, v63
	v_cvt_f32_ubyte3_e32 v139, v63
	v_readlane_b32 s30, v121, 51
	s_lshl_b32 s30, s30, 12
	s_add_u32 s28, s26, s30
	s_addc_u32 s29, s27, 0
	global_load_dwordx2 v[62:63], v162, s[28:29]
	v_fmac_f32_e32 v178, s25, v132
	v_fmac_f32_e32 v179, s25, v133
	v_fmac_f32_e32 v180, s25, v134
	v_fmac_f32_e32 v181, s25, v135
	v_fmac_f32_e32 v182, s25, v136
	v_fmac_f32_e32 v183, s25, v137
	v_fmac_f32_e32 v184, s25, v138
	v_fmac_f32_e32 v185, s25, v139
	s_waitcnt vmcnt(35)
	v_readlane_b32 s25, v247, 20
	v_cvt_f32_ubyte0_e32 v124, v64
	v_cvt_f32_ubyte1_e32 v125, v64
	v_cvt_f32_ubyte2_e32 v126, v64
	v_cvt_f32_ubyte3_e32 v127, v64
	v_cvt_f32_ubyte0_e32 v128, v65
	v_cvt_f32_ubyte1_e32 v129, v65
	v_cvt_f32_ubyte2_e32 v130, v65
	v_cvt_f32_ubyte3_e32 v131, v65
	v_readlane_b32 s30, v121, 52
	s_lshl_b32 s30, s30, 12
	s_add_u32 s28, s26, s30
	s_addc_u32 s29, s27, 0
	global_load_dwordx2 v[64:65], v162, s[28:29]
	v_fmac_f32_e32 v178, s25, v124
	v_fmac_f32_e32 v179, s25, v125
	v_fmac_f32_e32 v180, s25, v126
	v_fmac_f32_e32 v181, s25, v127
	v_fmac_f32_e32 v182, s25, v128
	v_fmac_f32_e32 v183, s25, v129
	v_fmac_f32_e32 v184, s25, v130
	v_fmac_f32_e32 v185, s25, v131
	s_waitcnt vmcnt(35)
	v_readlane_b32 s25, v247, 21
	v_cvt_f32_ubyte0_e32 v132, v66
	v_cvt_f32_ubyte1_e32 v133, v66
	v_cvt_f32_ubyte2_e32 v134, v66
	v_cvt_f32_ubyte3_e32 v135, v66
	v_cvt_f32_ubyte0_e32 v136, v67
	v_cvt_f32_ubyte1_e32 v137, v67
	v_cvt_f32_ubyte2_e32 v138, v67
	v_cvt_f32_ubyte3_e32 v139, v67
	v_readlane_b32 s30, v121, 53
	s_lshl_b32 s30, s30, 12
	s_add_u32 s28, s26, s30
	s_addc_u32 s29, s27, 0
	global_load_dwordx2 v[66:67], v162, s[28:29]
	v_fmac_f32_e32 v178, s25, v132
	v_fmac_f32_e32 v179, s25, v133
	v_fmac_f32_e32 v180, s25, v134
	v_fmac_f32_e32 v181, s25, v135
	v_fmac_f32_e32 v182, s25, v136
	v_fmac_f32_e32 v183, s25, v137
	v_fmac_f32_e32 v184, s25, v138
	v_fmac_f32_e32 v185, s25, v139
	s_waitcnt vmcnt(35)
	v_readlane_b32 s25, v247, 22
	v_cvt_f32_ubyte0_e32 v124, v68
	v_cvt_f32_ubyte1_e32 v125, v68
	v_cvt_f32_ubyte2_e32 v126, v68
	v_cvt_f32_ubyte3_e32 v127, v68
	v_cvt_f32_ubyte0_e32 v128, v69
	v_cvt_f32_ubyte1_e32 v129, v69
	v_cvt_f32_ubyte2_e32 v130, v69
	v_cvt_f32_ubyte3_e32 v131, v69
	v_readlane_b32 s30, v121, 54
	s_lshl_b32 s30, s30, 12
	s_add_u32 s28, s26, s30
	s_addc_u32 s29, s27, 0
	global_load_dwordx2 v[68:69], v162, s[28:29]
	v_fmac_f32_e32 v178, s25, v124
	v_fmac_f32_e32 v179, s25, v125
	v_fmac_f32_e32 v180, s25, v126
	v_fmac_f32_e32 v181, s25, v127
	v_fmac_f32_e32 v182, s25, v128
	v_fmac_f32_e32 v183, s25, v129
	v_fmac_f32_e32 v184, s25, v130
	v_fmac_f32_e32 v185, s25, v131
	s_waitcnt vmcnt(35)
	v_readlane_b32 s25, v247, 23
	v_cvt_f32_ubyte0_e32 v132, v70
	v_cvt_f32_ubyte1_e32 v133, v70
	v_cvt_f32_ubyte2_e32 v134, v70
	v_cvt_f32_ubyte3_e32 v135, v70
	v_cvt_f32_ubyte0_e32 v136, v71
	v_cvt_f32_ubyte1_e32 v137, v71
	v_cvt_f32_ubyte2_e32 v138, v71
	v_cvt_f32_ubyte3_e32 v139, v71
	v_readlane_b32 s30, v121, 55
	s_lshl_b32 s30, s30, 12
	s_add_u32 s28, s26, s30
	s_addc_u32 s29, s27, 0
	global_load_dwordx2 v[70:71], v162, s[28:29]
	v_fmac_f32_e32 v178, s25, v132
	v_fmac_f32_e32 v179, s25, v133
	v_fmac_f32_e32 v180, s25, v134
	v_fmac_f32_e32 v181, s25, v135
	v_fmac_f32_e32 v182, s25, v136
	v_fmac_f32_e32 v183, s25, v137
	v_fmac_f32_e32 v184, s25, v138
	v_fmac_f32_e32 v185, s25, v139
	s_waitcnt vmcnt(35)
	v_readlane_b32 s25, v247, 24
	v_cvt_f32_ubyte0_e32 v124, v72
	v_cvt_f32_ubyte1_e32 v125, v72
	v_cvt_f32_ubyte2_e32 v126, v72
	v_cvt_f32_ubyte3_e32 v127, v72
	v_cvt_f32_ubyte0_e32 v128, v73
	v_cvt_f32_ubyte1_e32 v129, v73
	v_cvt_f32_ubyte2_e32 v130, v73
	v_cvt_f32_ubyte3_e32 v131, v73
	v_readlane_b32 s30, v121, 56
	s_lshl_b32 s30, s30, 12
	s_add_u32 s28, s26, s30
	s_addc_u32 s29, s27, 0
	global_load_dwordx2 v[72:73], v162, s[28:29]
	v_fmac_f32_e32 v178, s25, v124
	v_fmac_f32_e32 v179, s25, v125
	v_fmac_f32_e32 v180, s25, v126
	v_fmac_f32_e32 v181, s25, v127
	v_fmac_f32_e32 v182, s25, v128
	v_fmac_f32_e32 v183, s25, v129
	v_fmac_f32_e32 v184, s25, v130
	v_fmac_f32_e32 v185, s25, v131
	s_waitcnt vmcnt(35)
	v_readlane_b32 s25, v247, 25
	v_cvt_f32_ubyte0_e32 v132, v74
	v_cvt_f32_ubyte1_e32 v133, v74
	v_cvt_f32_ubyte2_e32 v134, v74
	v_cvt_f32_ubyte3_e32 v135, v74
	v_cvt_f32_ubyte0_e32 v136, v75
	v_cvt_f32_ubyte1_e32 v137, v75
	v_cvt_f32_ubyte2_e32 v138, v75
	v_cvt_f32_ubyte3_e32 v139, v75
	v_readlane_b32 s30, v121, 57
	s_lshl_b32 s30, s30, 12
	s_add_u32 s28, s26, s30
	s_addc_u32 s29, s27, 0
	global_load_dwordx2 v[74:75], v162, s[28:29]
	v_fmac_f32_e32 v178, s25, v132
	v_fmac_f32_e32 v179, s25, v133
	v_fmac_f32_e32 v180, s25, v134
	v_fmac_f32_e32 v181, s25, v135
	v_fmac_f32_e32 v182, s25, v136
	v_fmac_f32_e32 v183, s25, v137
	v_fmac_f32_e32 v184, s25, v138
	v_fmac_f32_e32 v185, s25, v139
	s_waitcnt vmcnt(35)
	v_readlane_b32 s25, v247, 26
	v_cvt_f32_ubyte0_e32 v124, v76
	v_cvt_f32_ubyte1_e32 v125, v76
	v_cvt_f32_ubyte2_e32 v126, v76
	v_cvt_f32_ubyte3_e32 v127, v76
	v_cvt_f32_ubyte0_e32 v128, v77
	v_cvt_f32_ubyte1_e32 v129, v77
	v_cvt_f32_ubyte2_e32 v130, v77
	v_cvt_f32_ubyte3_e32 v131, v77
	v_readlane_b32 s30, v121, 58
	s_lshl_b32 s30, s30, 12
	s_add_u32 s28, s26, s30
	s_addc_u32 s29, s27, 0
	global_load_dwordx2 v[76:77], v162, s[28:29]
	v_fmac_f32_e32 v178, s25, v124
	v_fmac_f32_e32 v179, s25, v125
	v_fmac_f32_e32 v180, s25, v126
	v_fmac_f32_e32 v181, s25, v127
	v_fmac_f32_e32 v182, s25, v128
	v_fmac_f32_e32 v183, s25, v129
	v_fmac_f32_e32 v184, s25, v130
	v_fmac_f32_e32 v185, s25, v131
	s_waitcnt vmcnt(35)
	v_readlane_b32 s25, v247, 27
	v_cvt_f32_ubyte0_e32 v132, v78
	v_cvt_f32_ubyte1_e32 v133, v78
	v_cvt_f32_ubyte2_e32 v134, v78
	v_cvt_f32_ubyte3_e32 v135, v78
	v_cvt_f32_ubyte0_e32 v136, v79
	v_cvt_f32_ubyte1_e32 v137, v79
	v_cvt_f32_ubyte2_e32 v138, v79
	v_cvt_f32_ubyte3_e32 v139, v79
	v_readlane_b32 s30, v121, 59
	s_lshl_b32 s30, s30, 12
	s_add_u32 s28, s26, s30
	s_addc_u32 s29, s27, 0
	global_load_dwordx2 v[78:79], v162, s[28:29]
	v_fmac_f32_e32 v178, s25, v132
	v_fmac_f32_e32 v179, s25, v133
	v_fmac_f32_e32 v180, s25, v134
	v_fmac_f32_e32 v181, s25, v135
	v_fmac_f32_e32 v182, s25, v136
	v_fmac_f32_e32 v183, s25, v137
	v_fmac_f32_e32 v184, s25, v138
	v_fmac_f32_e32 v185, s25, v139
	s_waitcnt vmcnt(35)
	v_readlane_b32 s25, v247, 28
	v_cvt_f32_ubyte0_e32 v124, v80
	v_cvt_f32_ubyte1_e32 v125, v80
	v_cvt_f32_ubyte2_e32 v126, v80
	v_cvt_f32_ubyte3_e32 v127, v80
	v_cvt_f32_ubyte0_e32 v128, v81
	v_cvt_f32_ubyte1_e32 v129, v81
	v_cvt_f32_ubyte2_e32 v130, v81
	v_cvt_f32_ubyte3_e32 v131, v81
	v_readlane_b32 s30, v121, 60
	s_lshl_b32 s30, s30, 12
	s_add_u32 s28, s26, s30
	s_addc_u32 s29, s27, 0
	global_load_dwordx2 v[80:81], v162, s[28:29]
	v_fmac_f32_e32 v178, s25, v124
	v_fmac_f32_e32 v179, s25, v125
	v_fmac_f32_e32 v180, s25, v126
	v_fmac_f32_e32 v181, s25, v127
	v_fmac_f32_e32 v182, s25, v128
	v_fmac_f32_e32 v183, s25, v129
	v_fmac_f32_e32 v184, s25, v130
	v_fmac_f32_e32 v185, s25, v131
	s_waitcnt vmcnt(35)
	v_readlane_b32 s25, v247, 29
	v_cvt_f32_ubyte0_e32 v132, v82
	v_cvt_f32_ubyte1_e32 v133, v82
	v_cvt_f32_ubyte2_e32 v134, v82
	v_cvt_f32_ubyte3_e32 v135, v82
	v_cvt_f32_ubyte0_e32 v136, v83
	v_cvt_f32_ubyte1_e32 v137, v83
	v_cvt_f32_ubyte2_e32 v138, v83
	v_cvt_f32_ubyte3_e32 v139, v83
	v_readlane_b32 s30, v121, 61
	s_lshl_b32 s30, s30, 12
	s_add_u32 s28, s26, s30
	s_addc_u32 s29, s27, 0
	global_load_dwordx2 v[82:83], v162, s[28:29]
	v_fmac_f32_e32 v178, s25, v132
	v_fmac_f32_e32 v179, s25, v133
	v_fmac_f32_e32 v180, s25, v134
	v_fmac_f32_e32 v181, s25, v135
	v_fmac_f32_e32 v182, s25, v136
	v_fmac_f32_e32 v183, s25, v137
	v_fmac_f32_e32 v184, s25, v138
	v_fmac_f32_e32 v185, s25, v139
	s_waitcnt vmcnt(35)
	v_readlane_b32 s25, v247, 30
	v_cvt_f32_ubyte0_e32 v124, v84
	v_cvt_f32_ubyte1_e32 v125, v84
	v_cvt_f32_ubyte2_e32 v126, v84
	v_cvt_f32_ubyte3_e32 v127, v84
	v_cvt_f32_ubyte0_e32 v128, v85
	v_cvt_f32_ubyte1_e32 v129, v85
	v_cvt_f32_ubyte2_e32 v130, v85
	v_cvt_f32_ubyte3_e32 v131, v85
	v_readlane_b32 s30, v121, 62
	s_lshl_b32 s30, s30, 12
	s_add_u32 s28, s26, s30
	s_addc_u32 s29, s27, 0
	global_load_dwordx2 v[84:85], v162, s[28:29]
	v_fmac_f32_e32 v178, s25, v124
	v_fmac_f32_e32 v179, s25, v125
	v_fmac_f32_e32 v180, s25, v126
	v_fmac_f32_e32 v181, s25, v127
	v_fmac_f32_e32 v182, s25, v128
	v_fmac_f32_e32 v183, s25, v129
	v_fmac_f32_e32 v184, s25, v130
	v_fmac_f32_e32 v185, s25, v131
	s_waitcnt vmcnt(35)
	v_readlane_b32 s25, v247, 31
	v_cvt_f32_ubyte0_e32 v132, v86
	v_cvt_f32_ubyte1_e32 v133, v86
	v_cvt_f32_ubyte2_e32 v134, v86
	v_cvt_f32_ubyte3_e32 v135, v86
	v_cvt_f32_ubyte0_e32 v136, v87
	v_cvt_f32_ubyte1_e32 v137, v87
	v_cvt_f32_ubyte2_e32 v138, v87
	v_cvt_f32_ubyte3_e32 v139, v87
	v_readlane_b32 s30, v121, 63
	s_lshl_b32 s30, s30, 12
	s_add_u32 s28, s26, s30
	s_addc_u32 s29, s27, 0
	global_load_dwordx2 v[86:87], v162, s[28:29]
	v_fmac_f32_e32 v178, s25, v132
	v_fmac_f32_e32 v179, s25, v133
	v_fmac_f32_e32 v180, s25, v134
	v_fmac_f32_e32 v181, s25, v135
	v_fmac_f32_e32 v182, s25, v136
	v_fmac_f32_e32 v183, s25, v137
	v_fmac_f32_e32 v184, s25, v138
	v_fmac_f32_e32 v185, s25, v139
	s_waitcnt vmcnt(35)
	v_readlane_b32 s25, v247, 32
	v_cvt_f32_ubyte0_e32 v124, v24
	v_cvt_f32_ubyte1_e32 v125, v24
	v_cvt_f32_ubyte2_e32 v126, v24
	v_cvt_f32_ubyte3_e32 v127, v24
	v_cvt_f32_ubyte0_e32 v128, v25
	v_cvt_f32_ubyte1_e32 v129, v25
	v_cvt_f32_ubyte2_e32 v130, v25
	v_cvt_f32_ubyte3_e32 v131, v25
	v_fmac_f32_e32 v178, s25, v124
	v_fmac_f32_e32 v179, s25, v125
	v_fmac_f32_e32 v180, s25, v126
	v_fmac_f32_e32 v181, s25, v127
	v_fmac_f32_e32 v182, s25, v128
	v_fmac_f32_e32 v183, s25, v129
	v_fmac_f32_e32 v184, s25, v130
	v_fmac_f32_e32 v185, s25, v131
	s_waitcnt vmcnt(30)
	v_readlane_b32 s25, v247, 33
	v_cvt_f32_ubyte0_e32 v132, v26
	v_cvt_f32_ubyte1_e32 v133, v26
	v_cvt_f32_ubyte2_e32 v134, v26
	v_cvt_f32_ubyte3_e32 v135, v26
	v_cvt_f32_ubyte0_e32 v136, v27
	v_cvt_f32_ubyte1_e32 v137, v27
	v_cvt_f32_ubyte2_e32 v138, v27
	v_cvt_f32_ubyte3_e32 v139, v27
	v_fmac_f32_e32 v178, s25, v132
	v_fmac_f32_e32 v179, s25, v133
	v_fmac_f32_e32 v180, s25, v134
	v_fmac_f32_e32 v181, s25, v135
	v_fmac_f32_e32 v182, s25, v136
	v_fmac_f32_e32 v183, s25, v137
	v_fmac_f32_e32 v184, s25, v138
	v_fmac_f32_e32 v185, s25, v139
	s_waitcnt vmcnt(29)
	v_readlane_b32 s25, v247, 34
	v_cvt_f32_ubyte0_e32 v124, v28
	v_cvt_f32_ubyte1_e32 v125, v28
	v_cvt_f32_ubyte2_e32 v126, v28
	v_cvt_f32_ubyte3_e32 v127, v28
	v_cvt_f32_ubyte0_e32 v128, v29
	v_cvt_f32_ubyte1_e32 v129, v29
	v_cvt_f32_ubyte2_e32 v130, v29
	v_cvt_f32_ubyte3_e32 v131, v29
	v_fmac_f32_e32 v178, s25, v124
	v_fmac_f32_e32 v179, s25, v125
	v_fmac_f32_e32 v180, s25, v126
	v_fmac_f32_e32 v181, s25, v127
	v_fmac_f32_e32 v182, s25, v128
	v_fmac_f32_e32 v183, s25, v129
	v_fmac_f32_e32 v184, s25, v130
	v_fmac_f32_e32 v185, s25, v131
	s_waitcnt vmcnt(28)
	v_readlane_b32 s25, v247, 35
	v_cvt_f32_ubyte0_e32 v132, v30
	v_cvt_f32_ubyte1_e32 v133, v30
	v_cvt_f32_ubyte2_e32 v134, v30
	v_cvt_f32_ubyte3_e32 v135, v30
	v_cvt_f32_ubyte0_e32 v136, v31
	v_cvt_f32_ubyte1_e32 v137, v31
	v_cvt_f32_ubyte2_e32 v138, v31
	v_cvt_f32_ubyte3_e32 v139, v31
	v_fmac_f32_e32 v178, s25, v132
	v_fmac_f32_e32 v179, s25, v133
	v_fmac_f32_e32 v180, s25, v134
	v_fmac_f32_e32 v181, s25, v135
	v_fmac_f32_e32 v182, s25, v136
	v_fmac_f32_e32 v183, s25, v137
	v_fmac_f32_e32 v184, s25, v138
	v_fmac_f32_e32 v185, s25, v139
	s_waitcnt vmcnt(27)
	v_readlane_b32 s25, v247, 36
	v_cvt_f32_ubyte0_e32 v124, v32
	v_cvt_f32_ubyte1_e32 v125, v32
	v_cvt_f32_ubyte2_e32 v126, v32
	v_cvt_f32_ubyte3_e32 v127, v32
	v_cvt_f32_ubyte0_e32 v128, v33
	v_cvt_f32_ubyte1_e32 v129, v33
	v_cvt_f32_ubyte2_e32 v130, v33
	v_cvt_f32_ubyte3_e32 v131, v33
	v_fmac_f32_e32 v178, s25, v124
	v_fmac_f32_e32 v179, s25, v125
	v_fmac_f32_e32 v180, s25, v126
	v_fmac_f32_e32 v181, s25, v127
	v_fmac_f32_e32 v182, s25, v128
	v_fmac_f32_e32 v183, s25, v129
	v_fmac_f32_e32 v184, s25, v130
	v_fmac_f32_e32 v185, s25, v131
	s_waitcnt vmcnt(26)
	v_readlane_b32 s25, v247, 37
	v_cvt_f32_ubyte0_e32 v132, v34
	v_cvt_f32_ubyte1_e32 v133, v34
	v_cvt_f32_ubyte2_e32 v134, v34
	v_cvt_f32_ubyte3_e32 v135, v34
	v_cvt_f32_ubyte0_e32 v136, v35
	v_cvt_f32_ubyte1_e32 v137, v35
	v_cvt_f32_ubyte2_e32 v138, v35
	v_cvt_f32_ubyte3_e32 v139, v35
	v_fmac_f32_e32 v178, s25, v132
	v_fmac_f32_e32 v179, s25, v133
	v_fmac_f32_e32 v180, s25, v134
	v_fmac_f32_e32 v181, s25, v135
	v_fmac_f32_e32 v182, s25, v136
	v_fmac_f32_e32 v183, s25, v137
	v_fmac_f32_e32 v184, s25, v138
	v_fmac_f32_e32 v185, s25, v139
	s_waitcnt vmcnt(25)
	v_readlane_b32 s25, v247, 38
	v_cvt_f32_ubyte0_e32 v124, v36
	v_cvt_f32_ubyte1_e32 v125, v36
	v_cvt_f32_ubyte2_e32 v126, v36
	v_cvt_f32_ubyte3_e32 v127, v36
	v_cvt_f32_ubyte0_e32 v128, v37
	v_cvt_f32_ubyte1_e32 v129, v37
	v_cvt_f32_ubyte2_e32 v130, v37
	v_cvt_f32_ubyte3_e32 v131, v37
	v_fmac_f32_e32 v178, s25, v124
	v_fmac_f32_e32 v179, s25, v125
	v_fmac_f32_e32 v180, s25, v126
	v_fmac_f32_e32 v181, s25, v127
	v_fmac_f32_e32 v182, s25, v128
	v_fmac_f32_e32 v183, s25, v129
	v_fmac_f32_e32 v184, s25, v130
	v_fmac_f32_e32 v185, s25, v131
	s_waitcnt vmcnt(24)
	v_readlane_b32 s25, v247, 39
	v_cvt_f32_ubyte0_e32 v132, v38
	v_cvt_f32_ubyte1_e32 v133, v38
	v_cvt_f32_ubyte2_e32 v134, v38
	v_cvt_f32_ubyte3_e32 v135, v38
	v_cvt_f32_ubyte0_e32 v136, v39
	v_cvt_f32_ubyte1_e32 v137, v39
	v_cvt_f32_ubyte2_e32 v138, v39
	v_cvt_f32_ubyte3_e32 v139, v39
	v_fmac_f32_e32 v178, s25, v132
	v_fmac_f32_e32 v179, s25, v133
	v_fmac_f32_e32 v180, s25, v134
	v_fmac_f32_e32 v181, s25, v135
	v_fmac_f32_e32 v182, s25, v136
	v_fmac_f32_e32 v183, s25, v137
	v_fmac_f32_e32 v184, s25, v138
	v_fmac_f32_e32 v185, s25, v139
	s_waitcnt vmcnt(23)
	v_readlane_b32 s25, v247, 40
	v_cvt_f32_ubyte0_e32 v124, v40
	v_cvt_f32_ubyte1_e32 v125, v40
	v_cvt_f32_ubyte2_e32 v126, v40
	v_cvt_f32_ubyte3_e32 v127, v40
	v_cvt_f32_ubyte0_e32 v128, v41
	v_cvt_f32_ubyte1_e32 v129, v41
	v_cvt_f32_ubyte2_e32 v130, v41
	v_cvt_f32_ubyte3_e32 v131, v41
	v_fmac_f32_e32 v178, s25, v124
	v_fmac_f32_e32 v179, s25, v125
	v_fmac_f32_e32 v180, s25, v126
	v_fmac_f32_e32 v181, s25, v127
	v_fmac_f32_e32 v182, s25, v128
	v_fmac_f32_e32 v183, s25, v129
	v_fmac_f32_e32 v184, s25, v130
	v_fmac_f32_e32 v185, s25, v131
	s_waitcnt vmcnt(22)
	v_readlane_b32 s25, v247, 41
	v_cvt_f32_ubyte0_e32 v132, v42
	v_cvt_f32_ubyte1_e32 v133, v42
	v_cvt_f32_ubyte2_e32 v134, v42
	v_cvt_f32_ubyte3_e32 v135, v42
	v_cvt_f32_ubyte0_e32 v136, v43
	v_cvt_f32_ubyte1_e32 v137, v43
	v_cvt_f32_ubyte2_e32 v138, v43
	v_cvt_f32_ubyte3_e32 v139, v43
	v_fmac_f32_e32 v178, s25, v132
	v_fmac_f32_e32 v179, s25, v133
	v_fmac_f32_e32 v180, s25, v134
	v_fmac_f32_e32 v181, s25, v135
	v_fmac_f32_e32 v182, s25, v136
	v_fmac_f32_e32 v183, s25, v137
	v_fmac_f32_e32 v184, s25, v138
	v_fmac_f32_e32 v185, s25, v139
	s_waitcnt vmcnt(21)
	v_readlane_b32 s25, v247, 42
	v_cvt_f32_ubyte0_e32 v124, v44
	v_cvt_f32_ubyte1_e32 v125, v44
	v_cvt_f32_ubyte2_e32 v126, v44
	v_cvt_f32_ubyte3_e32 v127, v44
	v_cvt_f32_ubyte0_e32 v128, v45
	v_cvt_f32_ubyte1_e32 v129, v45
	v_cvt_f32_ubyte2_e32 v130, v45
	v_cvt_f32_ubyte3_e32 v131, v45
	v_fmac_f32_e32 v178, s25, v124
	v_fmac_f32_e32 v179, s25, v125
	v_fmac_f32_e32 v180, s25, v126
	v_fmac_f32_e32 v181, s25, v127
	v_fmac_f32_e32 v182, s25, v128
	v_fmac_f32_e32 v183, s25, v129
	v_fmac_f32_e32 v184, s25, v130
	v_fmac_f32_e32 v185, s25, v131
	s_waitcnt vmcnt(20)
	v_readlane_b32 s25, v247, 43
	v_cvt_f32_ubyte0_e32 v132, v46
	v_cvt_f32_ubyte1_e32 v133, v46
	v_cvt_f32_ubyte2_e32 v134, v46
	v_cvt_f32_ubyte3_e32 v135, v46
	v_cvt_f32_ubyte0_e32 v136, v47
	v_cvt_f32_ubyte1_e32 v137, v47
	v_cvt_f32_ubyte2_e32 v138, v47
	v_cvt_f32_ubyte3_e32 v139, v47
	v_fmac_f32_e32 v178, s25, v132
	v_fmac_f32_e32 v179, s25, v133
	v_fmac_f32_e32 v180, s25, v134
	v_fmac_f32_e32 v181, s25, v135
	v_fmac_f32_e32 v182, s25, v136
	v_fmac_f32_e32 v183, s25, v137
	v_fmac_f32_e32 v184, s25, v138
	v_fmac_f32_e32 v185, s25, v139
	s_waitcnt vmcnt(19)
	v_readlane_b32 s25, v247, 44
	v_cvt_f32_ubyte0_e32 v124, v48
	v_cvt_f32_ubyte1_e32 v125, v48
	v_cvt_f32_ubyte2_e32 v126, v48
	v_cvt_f32_ubyte3_e32 v127, v48
	v_cvt_f32_ubyte0_e32 v128, v49
	v_cvt_f32_ubyte1_e32 v129, v49
	v_cvt_f32_ubyte2_e32 v130, v49
	v_cvt_f32_ubyte3_e32 v131, v49
	v_fmac_f32_e32 v178, s25, v124
	v_fmac_f32_e32 v179, s25, v125
	v_fmac_f32_e32 v180, s25, v126
	v_fmac_f32_e32 v181, s25, v127
	v_fmac_f32_e32 v182, s25, v128
	v_fmac_f32_e32 v183, s25, v129
	v_fmac_f32_e32 v184, s25, v130
	v_fmac_f32_e32 v185, s25, v131
	s_waitcnt vmcnt(18)
	v_readlane_b32 s25, v247, 45
	v_cvt_f32_ubyte0_e32 v132, v50
	v_cvt_f32_ubyte1_e32 v133, v50
	v_cvt_f32_ubyte2_e32 v134, v50
	v_cvt_f32_ubyte3_e32 v135, v50
	v_cvt_f32_ubyte0_e32 v136, v51
	v_cvt_f32_ubyte1_e32 v137, v51
	v_cvt_f32_ubyte2_e32 v138, v51
	v_cvt_f32_ubyte3_e32 v139, v51
	v_fmac_f32_e32 v178, s25, v132
	v_fmac_f32_e32 v179, s25, v133
	v_fmac_f32_e32 v180, s25, v134
	v_fmac_f32_e32 v181, s25, v135
	v_fmac_f32_e32 v182, s25, v136
	v_fmac_f32_e32 v183, s25, v137
	v_fmac_f32_e32 v184, s25, v138
	v_fmac_f32_e32 v185, s25, v139
	s_waitcnt vmcnt(17)
	v_readlane_b32 s25, v247, 46
	v_cvt_f32_ubyte0_e32 v124, v52
	v_cvt_f32_ubyte1_e32 v125, v52
	v_cvt_f32_ubyte2_e32 v126, v52
	v_cvt_f32_ubyte3_e32 v127, v52
	v_cvt_f32_ubyte0_e32 v128, v53
	v_cvt_f32_ubyte1_e32 v129, v53
	v_cvt_f32_ubyte2_e32 v130, v53
	v_cvt_f32_ubyte3_e32 v131, v53
	v_fmac_f32_e32 v178, s25, v124
	v_fmac_f32_e32 v179, s25, v125
	v_fmac_f32_e32 v180, s25, v126
	v_fmac_f32_e32 v181, s25, v127
	v_fmac_f32_e32 v182, s25, v128
	v_fmac_f32_e32 v183, s25, v129
	v_fmac_f32_e32 v184, s25, v130
	v_fmac_f32_e32 v185, s25, v131
	s_waitcnt vmcnt(16)
	v_readlane_b32 s25, v247, 47
	v_cvt_f32_ubyte0_e32 v132, v54
	v_cvt_f32_ubyte1_e32 v133, v54
	v_cvt_f32_ubyte2_e32 v134, v54
	v_cvt_f32_ubyte3_e32 v135, v54
	v_cvt_f32_ubyte0_e32 v136, v55
	v_cvt_f32_ubyte1_e32 v137, v55
	v_cvt_f32_ubyte2_e32 v138, v55
	v_cvt_f32_ubyte3_e32 v139, v55
	v_fmac_f32_e32 v178, s25, v132
	v_fmac_f32_e32 v179, s25, v133
	v_fmac_f32_e32 v180, s25, v134
	v_fmac_f32_e32 v181, s25, v135
	v_fmac_f32_e32 v182, s25, v136
	v_fmac_f32_e32 v183, s25, v137
	v_fmac_f32_e32 v184, s25, v138
	v_fmac_f32_e32 v185, s25, v139
	s_waitcnt vmcnt(15)
	v_readlane_b32 s25, v247, 48
	v_cvt_f32_ubyte0_e32 v124, v56
	v_cvt_f32_ubyte1_e32 v125, v56
	v_cvt_f32_ubyte2_e32 v126, v56
	v_cvt_f32_ubyte3_e32 v127, v56
	v_cvt_f32_ubyte0_e32 v128, v57
	v_cvt_f32_ubyte1_e32 v129, v57
	v_cvt_f32_ubyte2_e32 v130, v57
	v_cvt_f32_ubyte3_e32 v131, v57
	v_fmac_f32_e32 v178, s25, v124
	v_fmac_f32_e32 v179, s25, v125
	v_fmac_f32_e32 v180, s25, v126
	v_fmac_f32_e32 v181, s25, v127
	v_fmac_f32_e32 v182, s25, v128
	v_fmac_f32_e32 v183, s25, v129
	v_fmac_f32_e32 v184, s25, v130
	v_fmac_f32_e32 v185, s25, v131
	s_waitcnt vmcnt(14)
	v_readlane_b32 s25, v247, 49
	v_cvt_f32_ubyte0_e32 v132, v58
	v_cvt_f32_ubyte1_e32 v133, v58
	v_cvt_f32_ubyte2_e32 v134, v58
	v_cvt_f32_ubyte3_e32 v135, v58
	v_cvt_f32_ubyte0_e32 v136, v59
	v_cvt_f32_ubyte1_e32 v137, v59
	v_cvt_f32_ubyte2_e32 v138, v59
	v_cvt_f32_ubyte3_e32 v139, v59
	v_fmac_f32_e32 v178, s25, v132
	v_fmac_f32_e32 v179, s25, v133
	v_fmac_f32_e32 v180, s25, v134
	v_fmac_f32_e32 v181, s25, v135
	v_fmac_f32_e32 v182, s25, v136
	v_fmac_f32_e32 v183, s25, v137
	v_fmac_f32_e32 v184, s25, v138
	v_fmac_f32_e32 v185, s25, v139
	s_waitcnt vmcnt(13)
	v_readlane_b32 s25, v247, 50
	v_cvt_f32_ubyte0_e32 v124, v60
	v_cvt_f32_ubyte1_e32 v125, v60
	v_cvt_f32_ubyte2_e32 v126, v60
	v_cvt_f32_ubyte3_e32 v127, v60
	v_cvt_f32_ubyte0_e32 v128, v61
	v_cvt_f32_ubyte1_e32 v129, v61
	v_cvt_f32_ubyte2_e32 v130, v61
	v_cvt_f32_ubyte3_e32 v131, v61
	v_fmac_f32_e32 v178, s25, v124
	v_fmac_f32_e32 v179, s25, v125
	v_fmac_f32_e32 v180, s25, v126
	v_fmac_f32_e32 v181, s25, v127
	v_fmac_f32_e32 v182, s25, v128
	v_fmac_f32_e32 v183, s25, v129
	v_fmac_f32_e32 v184, s25, v130
	v_fmac_f32_e32 v185, s25, v131
	s_waitcnt vmcnt(12)
	v_readlane_b32 s25, v247, 51
	v_cvt_f32_ubyte0_e32 v132, v62
	v_cvt_f32_ubyte1_e32 v133, v62
	v_cvt_f32_ubyte2_e32 v134, v62
	v_cvt_f32_ubyte3_e32 v135, v62
	v_cvt_f32_ubyte0_e32 v136, v63
	v_cvt_f32_ubyte1_e32 v137, v63
	v_cvt_f32_ubyte2_e32 v138, v63
	v_cvt_f32_ubyte3_e32 v139, v63
	v_fmac_f32_e32 v178, s25, v132
	v_fmac_f32_e32 v179, s25, v133
	v_fmac_f32_e32 v180, s25, v134
	v_fmac_f32_e32 v181, s25, v135
	v_fmac_f32_e32 v182, s25, v136
	v_fmac_f32_e32 v183, s25, v137
	v_fmac_f32_e32 v184, s25, v138
	v_fmac_f32_e32 v185, s25, v139
	s_waitcnt vmcnt(11)
	v_readlane_b32 s25, v247, 52
	v_cvt_f32_ubyte0_e32 v124, v64
	v_cvt_f32_ubyte1_e32 v125, v64
	v_cvt_f32_ubyte2_e32 v126, v64
	v_cvt_f32_ubyte3_e32 v127, v64
	v_cvt_f32_ubyte0_e32 v128, v65
	v_cvt_f32_ubyte1_e32 v129, v65
	v_cvt_f32_ubyte2_e32 v130, v65
	v_cvt_f32_ubyte3_e32 v131, v65
	v_fmac_f32_e32 v178, s25, v124
	v_fmac_f32_e32 v179, s25, v125
	v_fmac_f32_e32 v180, s25, v126
	v_fmac_f32_e32 v181, s25, v127
	v_fmac_f32_e32 v182, s25, v128
	v_fmac_f32_e32 v183, s25, v129
	v_fmac_f32_e32 v184, s25, v130
	v_fmac_f32_e32 v185, s25, v131
	s_waitcnt vmcnt(10)
	v_readlane_b32 s25, v247, 53
	v_cvt_f32_ubyte0_e32 v132, v66
	v_cvt_f32_ubyte1_e32 v133, v66
	v_cvt_f32_ubyte2_e32 v134, v66
	v_cvt_f32_ubyte3_e32 v135, v66
	v_cvt_f32_ubyte0_e32 v136, v67
	v_cvt_f32_ubyte1_e32 v137, v67
	v_cvt_f32_ubyte2_e32 v138, v67
	v_cvt_f32_ubyte3_e32 v139, v67
	v_fmac_f32_e32 v178, s25, v132
	v_fmac_f32_e32 v179, s25, v133
	v_fmac_f32_e32 v180, s25, v134
	v_fmac_f32_e32 v181, s25, v135
	v_fmac_f32_e32 v182, s25, v136
	v_fmac_f32_e32 v183, s25, v137
	v_fmac_f32_e32 v184, s25, v138
	v_fmac_f32_e32 v185, s25, v139
	s_waitcnt vmcnt(9)
	v_readlane_b32 s25, v247, 54
	v_cvt_f32_ubyte0_e32 v124, v68
	v_cvt_f32_ubyte1_e32 v125, v68
	v_cvt_f32_ubyte2_e32 v126, v68
	v_cvt_f32_ubyte3_e32 v127, v68
	v_cvt_f32_ubyte0_e32 v128, v69
	v_cvt_f32_ubyte1_e32 v129, v69
	v_cvt_f32_ubyte2_e32 v130, v69
	v_cvt_f32_ubyte3_e32 v131, v69
	v_fmac_f32_e32 v178, s25, v124
	v_fmac_f32_e32 v179, s25, v125
	v_fmac_f32_e32 v180, s25, v126
	v_fmac_f32_e32 v181, s25, v127
	v_fmac_f32_e32 v182, s25, v128
	v_fmac_f32_e32 v183, s25, v129
	v_fmac_f32_e32 v184, s25, v130
	v_fmac_f32_e32 v185, s25, v131
	s_waitcnt vmcnt(8)
	v_readlane_b32 s25, v247, 55
	v_cvt_f32_ubyte0_e32 v132, v70
	v_cvt_f32_ubyte1_e32 v133, v70
	v_cvt_f32_ubyte2_e32 v134, v70
	v_cvt_f32_ubyte3_e32 v135, v70
	v_cvt_f32_ubyte0_e32 v136, v71
	v_cvt_f32_ubyte1_e32 v137, v71
	v_cvt_f32_ubyte2_e32 v138, v71
	v_cvt_f32_ubyte3_e32 v139, v71
	v_fmac_f32_e32 v178, s25, v132
	v_fmac_f32_e32 v179, s25, v133
	v_fmac_f32_e32 v180, s25, v134
	v_fmac_f32_e32 v181, s25, v135
	v_fmac_f32_e32 v182, s25, v136
	v_fmac_f32_e32 v183, s25, v137
	v_fmac_f32_e32 v184, s25, v138
	v_fmac_f32_e32 v185, s25, v139
	s_waitcnt vmcnt(7)
	v_readlane_b32 s25, v247, 56
	v_cvt_f32_ubyte0_e32 v124, v72
	v_cvt_f32_ubyte1_e32 v125, v72
	v_cvt_f32_ubyte2_e32 v126, v72
	v_cvt_f32_ubyte3_e32 v127, v72
	v_cvt_f32_ubyte0_e32 v128, v73
	v_cvt_f32_ubyte1_e32 v129, v73
	v_cvt_f32_ubyte2_e32 v130, v73
	v_cvt_f32_ubyte3_e32 v131, v73
	v_fmac_f32_e32 v178, s25, v124
	v_fmac_f32_e32 v179, s25, v125
	v_fmac_f32_e32 v180, s25, v126
	v_fmac_f32_e32 v181, s25, v127
	v_fmac_f32_e32 v182, s25, v128
	v_fmac_f32_e32 v183, s25, v129
	v_fmac_f32_e32 v184, s25, v130
	v_fmac_f32_e32 v185, s25, v131
	s_waitcnt vmcnt(6)
	v_readlane_b32 s25, v247, 57
	v_cvt_f32_ubyte0_e32 v132, v74
	v_cvt_f32_ubyte1_e32 v133, v74
	v_cvt_f32_ubyte2_e32 v134, v74
	v_cvt_f32_ubyte3_e32 v135, v74
	v_cvt_f32_ubyte0_e32 v136, v75
	v_cvt_f32_ubyte1_e32 v137, v75
	v_cvt_f32_ubyte2_e32 v138, v75
	v_cvt_f32_ubyte3_e32 v139, v75
	v_fmac_f32_e32 v178, s25, v132
	v_fmac_f32_e32 v179, s25, v133
	v_fmac_f32_e32 v180, s25, v134
	v_fmac_f32_e32 v181, s25, v135
	v_fmac_f32_e32 v182, s25, v136
	v_fmac_f32_e32 v183, s25, v137
	v_fmac_f32_e32 v184, s25, v138
	v_fmac_f32_e32 v185, s25, v139
	s_waitcnt vmcnt(5)
	v_readlane_b32 s25, v247, 58
	v_cvt_f32_ubyte0_e32 v124, v76
	v_cvt_f32_ubyte1_e32 v125, v76
	v_cvt_f32_ubyte2_e32 v126, v76
	v_cvt_f32_ubyte3_e32 v127, v76
	v_cvt_f32_ubyte0_e32 v128, v77
	v_cvt_f32_ubyte1_e32 v129, v77
	v_cvt_f32_ubyte2_e32 v130, v77
	v_cvt_f32_ubyte3_e32 v131, v77
	v_fmac_f32_e32 v178, s25, v124
	v_fmac_f32_e32 v179, s25, v125
	v_fmac_f32_e32 v180, s25, v126
	v_fmac_f32_e32 v181, s25, v127
	v_fmac_f32_e32 v182, s25, v128
	v_fmac_f32_e32 v183, s25, v129
	v_fmac_f32_e32 v184, s25, v130
	v_fmac_f32_e32 v185, s25, v131
	s_waitcnt vmcnt(4)
	v_readlane_b32 s25, v247, 59
	v_cvt_f32_ubyte0_e32 v132, v78
	v_cvt_f32_ubyte1_e32 v133, v78
	v_cvt_f32_ubyte2_e32 v134, v78
	v_cvt_f32_ubyte3_e32 v135, v78
	v_cvt_f32_ubyte0_e32 v136, v79
	v_cvt_f32_ubyte1_e32 v137, v79
	v_cvt_f32_ubyte2_e32 v138, v79
	v_cvt_f32_ubyte3_e32 v139, v79
	v_fmac_f32_e32 v178, s25, v132
	v_fmac_f32_e32 v179, s25, v133
	v_fmac_f32_e32 v180, s25, v134
	v_fmac_f32_e32 v181, s25, v135
	v_fmac_f32_e32 v182, s25, v136
	v_fmac_f32_e32 v183, s25, v137
	v_fmac_f32_e32 v184, s25, v138
	v_fmac_f32_e32 v185, s25, v139
	s_waitcnt vmcnt(3)
	v_readlane_b32 s25, v247, 60
	v_cvt_f32_ubyte0_e32 v124, v80
	v_cvt_f32_ubyte1_e32 v125, v80
	v_cvt_f32_ubyte2_e32 v126, v80
	v_cvt_f32_ubyte3_e32 v127, v80
	v_cvt_f32_ubyte0_e32 v128, v81
	v_cvt_f32_ubyte1_e32 v129, v81
	v_cvt_f32_ubyte2_e32 v130, v81
	v_cvt_f32_ubyte3_e32 v131, v81
	v_fmac_f32_e32 v178, s25, v124
	v_fmac_f32_e32 v179, s25, v125
	v_fmac_f32_e32 v180, s25, v126
	v_fmac_f32_e32 v181, s25, v127
	v_fmac_f32_e32 v182, s25, v128
	v_fmac_f32_e32 v183, s25, v129
	v_fmac_f32_e32 v184, s25, v130
	v_fmac_f32_e32 v185, s25, v131
	s_waitcnt vmcnt(2)
	v_readlane_b32 s25, v247, 61
	v_cvt_f32_ubyte0_e32 v132, v82
	v_cvt_f32_ubyte1_e32 v133, v82
	v_cvt_f32_ubyte2_e32 v134, v82
	v_cvt_f32_ubyte3_e32 v135, v82
	v_cvt_f32_ubyte0_e32 v136, v83
	v_cvt_f32_ubyte1_e32 v137, v83
	v_cvt_f32_ubyte2_e32 v138, v83
	v_cvt_f32_ubyte3_e32 v139, v83
	v_fmac_f32_e32 v178, s25, v132
	v_fmac_f32_e32 v179, s25, v133
	v_fmac_f32_e32 v180, s25, v134
	v_fmac_f32_e32 v181, s25, v135
	v_fmac_f32_e32 v182, s25, v136
	v_fmac_f32_e32 v183, s25, v137
	v_fmac_f32_e32 v184, s25, v138
	v_fmac_f32_e32 v185, s25, v139
	s_waitcnt vmcnt(1)
	v_readlane_b32 s25, v247, 62
	v_cvt_f32_ubyte0_e32 v124, v84
	v_cvt_f32_ubyte1_e32 v125, v84
	v_cvt_f32_ubyte2_e32 v126, v84
	v_cvt_f32_ubyte3_e32 v127, v84
	v_cvt_f32_ubyte0_e32 v128, v85
	v_cvt_f32_ubyte1_e32 v129, v85
	v_cvt_f32_ubyte2_e32 v130, v85
	v_cvt_f32_ubyte3_e32 v131, v85
	v_fmac_f32_e32 v178, s25, v124
	v_fmac_f32_e32 v179, s25, v125
	v_fmac_f32_e32 v180, s25, v126
	v_fmac_f32_e32 v181, s25, v127
	v_fmac_f32_e32 v182, s25, v128
	v_fmac_f32_e32 v183, s25, v129
	v_fmac_f32_e32 v184, s25, v130
	v_fmac_f32_e32 v185, s25, v131
	s_waitcnt vmcnt(0)
	v_readlane_b32 s25, v247, 63
	v_cvt_f32_ubyte0_e32 v132, v86
	v_cvt_f32_ubyte1_e32 v133, v86
	v_cvt_f32_ubyte2_e32 v134, v86
	v_cvt_f32_ubyte3_e32 v135, v86
	v_cvt_f32_ubyte0_e32 v136, v87
	v_cvt_f32_ubyte1_e32 v137, v87
	v_cvt_f32_ubyte2_e32 v138, v87
	v_cvt_f32_ubyte3_e32 v139, v87
	v_fmac_f32_e32 v178, s25, v132
	v_fmac_f32_e32 v179, s25, v133
	v_fmac_f32_e32 v180, s25, v134
	v_fmac_f32_e32 v181, s25, v135
	v_fmac_f32_e32 v182, s25, v136
	v_fmac_f32_e32 v183, s25, v137
	v_fmac_f32_e32 v184, s25, v138
	v_fmac_f32_e32 v185, s25, v139
	v_lshlrev_b32_e32 v132, 16, v242
	v_and_b32_e32 v133, 0xffff0000, v242
	v_lshlrev_b32_e32 v134, 16, v243
	v_and_b32_e32 v135, 0xffff0000, v243
	v_lshlrev_b32_e32 v136, 16, v244
	v_and_b32_e32 v137, 0xffff0000, v244
	v_lshlrev_b32_e32 v138, 16, v245
	v_and_b32_e32 v139, 0xffff0000, v245
	v_add_f32_e32 v178, v178, v248
	v_add_f32_e32 v179, v179, v248
	v_add_f32_e32 v180, v180, v248
	v_add_f32_e32 v181, v181, v248
	v_add_f32_e32 v182, v182, v248
	v_add_f32_e32 v183, v183, v248
	v_add_f32_e32 v184, v184, v248
	v_add_f32_e32 v185, v185, v248
	v_add_f32_e32 v124, v132, v178
	v_add_f32_e32 v125, v133, v179
	v_add_f32_e32 v126, v134, v180
	v_add_f32_e32 v127, v135, v181
	v_add_f32_e32 v128, v136, v182
	v_add_f32_e32 v129, v137, v183
	v_add_f32_e32 v130, v138, v184
	v_add_f32_e32 v131, v139, v185
	v_mul_f32_e32 v16, v124, v124
	v_fmac_f32_e32 v16, v125, v125
	v_fmac_f32_e32 v16, v126, v126
	v_fmac_f32_e32 v16, v127, v127
	v_fmac_f32_e32 v16, v128, v128
	v_fmac_f32_e32 v16, v129, v129
	v_fmac_f32_e32 v16, v130, v130
	v_fmac_f32_e32 v16, v131, v131
	s_nop 1
	v_add_f32_dpp v17, v16, v16 quad_perm:[1,0,3,2] row_mask:0xf bank_mask:0xf
	s_nop 1
	v_add_f32_dpp v16, v17, v17 quad_perm:[2,3,0,1] row_mask:0xf bank_mask:0xf
	s_nop 1
	v_add_f32_dpp v17, v16, v16 row_half_mirror row_mask:0xf bank_mask:0xf
	s_nop 1
	v_add_f32_dpp v16, v17, v17 row_ror:8 row_mask:0xf bank_mask:0xf
	v_mov_b32_e32 v17, v16
	s_nop 1
	v_permlane16_swap_b32_e32 v16, v17
	v_add_f32_e32 v16, v16, v17
	v_mov_b32_e32 v17, v16
	s_nop 1
	v_permlane32_swap_b32_e32 v16, v17
	v_add_f32_e32 v16, v16, v17
	global_store_dwordx4 v[20:21], v[124:127], off
	global_store_dwordx4 v[20:21], v[128:131], off offset:16
	s_lshl_b32 s30, s16, 5
	s_add_u32 s28, s62, s30
	s_addc_u32 s29, s63, 0
	s_mov_b64 exec, 1
	global_store_dword v19, v16, s[28:29]
	s_mov_b64 exec, -1
	v_readlane_b32 s30, v122, 0
	s_lshl_b32 s30, s30, 12
	s_add_u32 s28, s26, s30
	s_addc_u32 s29, s27, 0
	global_load_dwordx2 v[24:25], v162, s[28:29]
	v_readlane_b32 s30, v122, 1
	s_lshl_b32 s30, s30, 12
	s_add_u32 s28, s26, s30
	s_addc_u32 s29, s27, 0
	global_load_dwordx2 v[26:27], v162, s[28:29]
	v_readlane_b32 s30, v122, 2
	s_lshl_b32 s30, s30, 12
	s_add_u32 s28, s26, s30
	s_addc_u32 s29, s27, 0
	global_load_dwordx2 v[28:29], v162, s[28:29]
	v_readlane_b32 s30, v122, 3
	s_lshl_b32 s30, s30, 12
	s_add_u32 s28, s26, s30
	s_addc_u32 s29, s27, 0
	global_load_dwordx2 v[30:31], v162, s[28:29]
	v_readlane_b32 s30, v122, 4
	s_lshl_b32 s30, s30, 12
	s_add_u32 s28, s26, s30
	s_addc_u32 s29, s27, 0
	global_load_dwordx2 v[32:33], v162, s[28:29]
	v_readlane_b32 s30, v122, 5
	s_lshl_b32 s30, s30, 12
	s_add_u32 s28, s26, s30
	s_addc_u32 s29, s27, 0
	global_load_dwordx2 v[34:35], v162, s[28:29]
	v_readlane_b32 s30, v122, 6
	s_lshl_b32 s30, s30, 12
	s_add_u32 s28, s26, s30
	s_addc_u32 s29, s27, 0
	global_load_dwordx2 v[36:37], v162, s[28:29]
	v_readlane_b32 s30, v122, 7
	s_lshl_b32 s30, s30, 12
	s_add_u32 s28, s26, s30
	s_addc_u32 s29, s27, 0
	global_load_dwordx2 v[38:39], v162, s[28:29]
	v_readlane_b32 s30, v122, 8
	s_lshl_b32 s30, s30, 12
	s_add_u32 s28, s26, s30
	s_addc_u32 s29, s27, 0
	global_load_dwordx2 v[40:41], v162, s[28:29]
	v_readlane_b32 s30, v122, 9
	s_lshl_b32 s30, s30, 12
	s_add_u32 s28, s26, s30
	s_addc_u32 s29, s27, 0
	global_load_dwordx2 v[42:43], v162, s[28:29]
	v_readlane_b32 s30, v122, 10
	s_lshl_b32 s30, s30, 12
	s_add_u32 s28, s26, s30
	s_addc_u32 s29, s27, 0
	global_load_dwordx2 v[44:45], v162, s[28:29]
	v_readlane_b32 s30, v122, 11
	s_lshl_b32 s30, s30, 12
	s_add_u32 s28, s26, s30
	s_addc_u32 s29, s27, 0
	global_load_dwordx2 v[46:47], v162, s[28:29]
	v_readlane_b32 s30, v122, 12
	s_lshl_b32 s30, s30, 12
	s_add_u32 s28, s26, s30
	s_addc_u32 s29, s27, 0
	global_load_dwordx2 v[48:49], v162, s[28:29]
	v_readlane_b32 s30, v122, 13
	s_lshl_b32 s30, s30, 12
	s_add_u32 s28, s26, s30
	s_addc_u32 s29, s27, 0
	global_load_dwordx2 v[50:51], v162, s[28:29]
	v_readlane_b32 s30, v122, 14
	s_lshl_b32 s30, s30, 12
	s_add_u32 s28, s26, s30
	s_addc_u32 s29, s27, 0
	global_load_dwordx2 v[52:53], v162, s[28:29]
	v_readlane_b32 s30, v122, 15
	s_lshl_b32 s30, s30, 12
	s_add_u32 s28, s26, s30
	s_addc_u32 s29, s27, 0
	global_load_dwordx2 v[54:55], v162, s[28:29]
	v_readlane_b32 s30, v122, 16
	s_lshl_b32 s30, s30, 12
	s_add_u32 s28, s26, s30
	s_addc_u32 s29, s27, 0
	global_load_dwordx2 v[56:57], v162, s[28:29]
	v_readlane_b32 s30, v122, 17
	s_lshl_b32 s30, s30, 12
	s_add_u32 s28, s26, s30
	s_addc_u32 s29, s27, 0
	global_load_dwordx2 v[58:59], v162, s[28:29]
	v_readlane_b32 s30, v122, 18
	s_lshl_b32 s30, s30, 12
	s_add_u32 s28, s26, s30
	s_addc_u32 s29, s27, 0
	global_load_dwordx2 v[60:61], v162, s[28:29]
	v_readlane_b32 s30, v122, 19
	s_lshl_b32 s30, s30, 12
	s_add_u32 s28, s26, s30
	s_addc_u32 s29, s27, 0
	global_load_dwordx2 v[62:63], v162, s[28:29]
	v_readlane_b32 s30, v122, 20
	s_lshl_b32 s30, s30, 12
	s_add_u32 s28, s26, s30
	s_addc_u32 s29, s27, 0
	global_load_dwordx2 v[64:65], v162, s[28:29]
	v_readlane_b32 s30, v122, 21
	s_lshl_b32 s30, s30, 12
	s_add_u32 s28, s26, s30
	s_addc_u32 s29, s27, 0
	global_load_dwordx2 v[66:67], v162, s[28:29]
	v_readlane_b32 s30, v122, 22
	s_lshl_b32 s30, s30, 12
	s_add_u32 s28, s26, s30
	s_addc_u32 s29, s27, 0
	global_load_dwordx2 v[68:69], v162, s[28:29]
	v_readlane_b32 s30, v122, 23
	s_lshl_b32 s30, s30, 12
	s_add_u32 s28, s26, s30
	s_addc_u32 s29, s27, 0
	global_load_dwordx2 v[70:71], v162, s[28:29]
	v_readlane_b32 s30, v122, 24
	s_lshl_b32 s30, s30, 12
	s_add_u32 s28, s26, s30
	s_addc_u32 s29, s27, 0
	global_load_dwordx2 v[72:73], v162, s[28:29]
	v_readlane_b32 s30, v122, 25
	s_lshl_b32 s30, s30, 12
	s_add_u32 s28, s26, s30
	s_addc_u32 s29, s27, 0
	global_load_dwordx2 v[74:75], v162, s[28:29]
	v_readlane_b32 s30, v122, 26
	s_lshl_b32 s30, s30, 12
	s_add_u32 s28, s26, s30
	s_addc_u32 s29, s27, 0
	global_load_dwordx2 v[76:77], v162, s[28:29]
	v_readlane_b32 s30, v122, 27
	s_lshl_b32 s30, s30, 12
	s_add_u32 s28, s26, s30
	s_addc_u32 s29, s27, 0
	global_load_dwordx2 v[78:79], v162, s[28:29]
	v_readlane_b32 s30, v122, 28
	s_lshl_b32 s30, s30, 12
	s_add_u32 s28, s26, s30
	s_addc_u32 s29, s27, 0
	global_load_dwordx2 v[80:81], v162, s[28:29]
	v_readlane_b32 s30, v122, 29
	s_lshl_b32 s30, s30, 12
	s_add_u32 s28, s26, s30
	s_addc_u32 s29, s27, 0
	global_load_dwordx2 v[82:83], v162, s[28:29]
	v_readlane_b32 s30, v122, 30
	s_lshl_b32 s30, s30, 12
	s_add_u32 s28, s26, s30
	s_addc_u32 s29, s27, 0
	global_load_dwordx2 v[84:85], v162, s[28:29]
	v_readlane_b32 s30, v122, 31
	s_lshl_b32 s30, s30, 12
	s_add_u32 s28, s26, s30
	s_addc_u32 s29, s27, 0
	global_load_dwordx2 v[86:87], v162, s[28:29]
	s_add_i32 s16, s16, 1
	s_cmp_lt_i32 s16, s17
	s_cbranch_scc1 .Lpb_tok
	s_waitcnt vmcnt(0)
	s_waitcnt vmcnt(0)
	v_cmp_eq_u32_e32 vcc, 0, v0
	s_waitcnt vmcnt(0) lgkmcnt(0)
	s_barrier
	s_and_saveexec_b64 s[2:3], vcc
	s_cbranch_execz .Lgbc_1444
	v_readlane_b32 s4, v237, 5
	s_waitcnt vmcnt(0) expcnt(0) lgkmcnt(0)
	s_nop 0
	v_mov_b32_e32 v1, s4
	ds_read_b32 v3, v1
	ds_read_b32 v1, v1 offset:4
	s_waitcnt lgkmcnt(1)
	v_cmp_ne_u32_e32 vcc, 0, v3
	s_branch .Lgbc_1412
	v_readlane_b32 s4, v237, 2
	v_readlane_b32 s5, v237, 3
	s_load_dwordx2 s[8:9], s[6:7], 0x4
	s_lshl_b64 s[4:5], s[4:5], 2
	v_readlane_b32 s6, v237, 0
	s_add_u32 s4, s6, s4
	v_readlane_b32 s6, v237, 1
	s_addc_u32 s5, s6, s5
	s_add_u32 s6, s4, 0x1000
	s_addc_u32 s7, s5, 0
	s_waitcnt lgkmcnt(0)
	s_mul_i32 s20, s8, s38
	s_add_u32 s8, s4, 0x1100
	s_mul_i32 s20, s20, s9
	s_addc_u32 s9, s5, 0
	s_add_u32 s10, s4, 0x1200
	s_addc_u32 s11, s5, 0
	s_add_u32 s12, s4, 0x1300
	s_addc_u32 s13, s5, 0
	s_mov_b32 s21, 1
	v_mov_b32_e32 v17, 0
	s_branch .Lgbc_1400

.Lgbc_1444:
	s_or_b64 exec, exec, s[2:3]
	s_waitcnt lgkmcnt(0)
	s_barrier
	s_mov_b64 exec, -1
	s_load_dwordx2 s[12:13], s[0:1], 0xc0
	s_load_dwordx2 s[4:5], s[0:1], 0xb8
	s_load_dwordx2 s[6:7], s[0:1], 0xb0
	v_lshlrev_b32_e32 v2, 5, v0
	v_mov_b32_e32 v3, 0
	v_mov_b32_e32 v173, 0x358637bd
	v_mov_b32_e32 v174, 0x260
	s_mov_b32 s51, 0xf800000
	s_mov_b32 s31, 0
	s_lshl_b32 s16, s33, 5
	s_add_i32 s17, s16, 32
	s_waitcnt lgkmcnt(0)
	v_lshl_add_u64 v[4:5], v[2:3], 0, s[6:7]
	global_load_dwordx4 v[100:103], v[4:5], off
	global_load_dwordx4 v[104:107], v[4:5], off offset:16
	v_lshl_add_u64 v[6:7], v[2:3], 0, s[4:5]
	s_add_u32 s62, s12, 0x25d00000
	s_addc_u32 s63, s13, 0
	v_mov_b32_e32 v9, 0
.Lpc_tok:
	s_lshl_b32 s30, s16, 14
	v_lshl_add_u64 v[4:5], v[6:7], 0, s[30:31]
	global_load_dwordx4 v[10:13], v[4:5], off
	global_load_dwordx4 v[14:17], v[4:5], off offset:16
	s_lshl_b32 s30, s16, 5
	s_add_u32 s28, s62, s30
	s_addc_u32 s29, s63, 0
	global_load_dwordx4 v[24:27], v9, s[28:29]
	global_load_dwordx4 v[28:31], v9, s[28:29] offset:16
	s_waitcnt vmcnt(0)
	v_add_f32_e32 v18, 0, v24
	v_add_f32_e32 v18, v18, v25
	v_add_f32_e32 v18, v18, v26
	v_add_f32_e32 v18, v18, v27
	v_add_f32_e32 v18, v18, v28
	v_add_f32_e32 v18, v18, v29
	v_add_f32_e32 v18, v18, v30
	v_add_f32_e32 v18, v18, v31
	v_fmamk_f32 v18, v18, 0x39800000, v173
	v_mul_f32_e32 v19, 0x4f800000, v18
	v_cmp_gt_f32_e32 vcc, s51, v18
	s_nop 1
	v_cndmask_b32_e32 v18, v18, v19, vcc
	v_sqrt_f32_e32 v19, v18
	s_nop 0
	v_add_u32_e32 v20, -1, v19
	v_fma_f32 v22, -v20, v19, v18
	v_add_u32_e32 v21, 1, v19
	v_cmp_ge_f32_e64 s[14:15], 0, v22
	s_nop 1
	v_cndmask_b32_e64 v20, v19, v20, s[14:15]
	v_fma_f32 v19, -v21, v19, v18
	v_cmp_lt_f32_e64 s[14:15], 0, v19
	s_nop 1
	v_cndmask_b32_e64 v19, v20, v21, s[14:15]
	v_mul_f32_e32 v20, 0x37800000, v19
	v_cndmask_b32_e32 v19, v19, v20, vcc
	v_cmp_class_f32_e32 vcc, v18, v174
	s_nop 1
	v_cndmask_b32_e32 v18, v19, v18, vcc
	v_div_scale_f32 v19, s[14:15], v18, v18, 1.0
	v_rcp_f32_e32 v20, v19
	s_nop 0
	v_fma_f32 v21, -v19, v20, 1.0
	v_fmac_f32_e32 v20, v21, v20
	v_div_scale_f32 v21, vcc, 1.0, v18, 1.0
	v_mul_f32_e32 v22, v21, v20
	v_fma_f32 v23, -v19, v22, v21
	v_fmac_f32_e32 v22, v23, v20
	v_fma_f32 v19, -v19, v22, v21
	v_div_fmas_f32 v19, v19, v20, v22
	v_div_fixup_f32 v18, v19, v18, 1.0
	v_pk_mul_f32 v[10:11], v[10:11], v[18:19] op_sel_hi:[1,0]
	v_pk_mul_f32 v[12:13], v[12:13], v[18:19] op_sel_hi:[1,0]
	v_pk_mul_f32 v[14:15], v[14:15], v[18:19] op_sel_hi:[1,0]
	v_pk_mul_f32 v[16:17], v[16:17], v[18:19] op_sel_hi:[1,0]
	v_pk_mul_f32 v[10:11], v[10:11], v[100:101]
	v_pk_mul_f32 v[12:13], v[12:13], v[102:103]
	v_pk_mul_f32 v[14:15], v[14:15], v[104:105]
	v_pk_mul_f32 v[16:17], v[16:17], v[106:107]
	global_store_dwordx4 v[4:5], v[10:13], off
	global_store_dwordx4 v[4:5], v[14:17], off offset:16
	s_nop 1
	s_add_i32 s16, s16, 1
	s_cmp_lt_i32 s16, s17
	s_cbranch_scc1 .Lpc_tok
	s_waitcnt vmcnt(0)
	s_branch .LBB0_1485
	s_cmp_gt_i32 s56, 12
	s_cselect_b64 s[2:3], -1, 0
	s_cmp_lt_i32 s57, 13
	s_cselect_b64 s[4:5], -1, 0
	s_or_b64 s[2:3], s[2:3], s[4:5]
	s_and_b64 vcc, exec, s[2:3]
	s_cbranch_vccnz .LBB0_1485
	s_load_dword s25, s[0:1], 0xd8
	s_waitcnt lgkmcnt(0)
	s_and_b32 s2, s25, 7
	s_cmp_lg_u32 s2, 0
	v_readfirstlane_b32 s2, v0
	s_cbranch_scc1 .LBB0_1466
	s_ashr_i32 s4, s33, 31
	s_lshr_b32 s4, s4, 29
	s_add_i32 s4, s33, s4
	s_ashr_i32 s5, s4, 3
	s_and_b32 s4, s4, -8
	s_ashr_i32 s3, s25, 3
	s_sub_i32 s4, s33, s4
	s_mul_i32 s3, s3, s4
	s_add_i32 s33, s3, s5
